# P1 (layer-0 projection) epilogue: per-row-group vmcnt(0) store drains removed in all four variants (gains waited once)
# baseline (speedup 1.0000x reference)
; __device__ __forceinline__ unsigned pk4_fp8(float a, float b, float c, float d) { unsigned w = 0u; w = __builtin_amdgcn_cvt_pk_fp8_f32(a, b, w, false); w = __builtin_amdgcn_cvt_pk_fp8_f32(c, d, w, true); return w; }
; template <bool F8OUT = false> __device__ __forceinline__ void head_tile_store(const f32x4 (&acc)[2][2][4][2], bf16_t* obase  , int opitch, const float* gain, float scale, const f32x2e* rope, int row0, int fq) {
;     ...
;             if (gain) {
;                 float ss = 0.f;
; #pragma unroll
;                 for (int bj = 0; bj < 2; ++bj)
; #pragma unroll
;                     for (int n = 0; n < 2; ++n) ss += (x[bj][n][0] * x[bj][n][0] + x[bj][n][1] * x[bj][n][1]) + (x[bj][n][2] * x[bj][n][2] + x[bj][n][3] * x[bj][n][3]);
;                 ss += __shfl_xor(ss, 16); ss += __shfl_xor(ss, 32);
;                 const float r = scale / sqrtf(ss * (1.f / 64.f) + 1e-6f);
; #pragma unroll
;                 for (int bj = 0; bj < 2; ++bj)
; #pragma unroll
;                     for (int n = 0; n < 2; ++n) x[bj][n] = x[bj][n] * r * g[bj][n];
;             }
;     ...
;             if constexpr (F8OUT) { unsigned char* rowp8 = (unsigned char*)obase + (size_t)row * opitch + 8 * fq; typedef unsigned u32x2_ __attribute__((ext_vector_type(2)));
; #pragma unroll
;                 for (int bj = 0; bj < 2; ++bj) *(u32x2_*)(rowp8 + 32 * bj) = (u32x2_){pk4_fp8(x[bj][0][0], x[bj][0][1], x[bj][0][2], x[bj][0][3]), pk4_fp8(x[bj][1][0], x[bj][1][1], x[bj][1][2], x[bj][1][3])};
;                 continue; }
.LBB0_169:
	v_mov_b32_e32 v162, v175
	v_mov_b32_e32 v163, v175
	v_cvt_pk_fp8_f32 v162, v18, v19
	v_cvt_pk_fp8_f32 v163, v22, v23
	v_mov_b32_e32 v18, v175
	v_mov_b32_e32 v19, v175
	v_cvt_pk_fp8_f32 v18, v26, v27
	v_cvt_pk_fp8_f32 v19, v30, v31
	v_readlane_b32 s0, v255, 27
	v_cvt_pk_fp8_f32 v162, v20, v21 op_sel:[0,0,1]
	v_cvt_pk_fp8_f32 v163, v24, v25 op_sel:[0,0,1]
	v_readlane_b32 s1, v255, 28
	v_ashrrev_i32_e32 v189, 31, v188
	v_cvt_pk_fp8_f32 v18, v28, v29 op_sel:[0,0,1]
	v_cvt_pk_fp8_f32 v19, v32, v33 op_sel:[0,0,1]
	v_lshl_add_u64 v[190:191], s[0:1], 0, v[190:191]
	v_lshlrev_b64 v[20:21], 7, v[188:189]
	v_lshl_add_u64 v[20:21], v[190:191], 0, v[20:21]
	global_store_dwordx2 v[20:21], v[162:163], off
	global_store_dwordx2 v[20:21], v[18:19], off offset:32
	v_mov_b64_e32 v[18:19], v[130:131]
	v_mov_b64_e32 v[22:23], v[134:135]
	v_mov_b64_e32 v[30:31], v[138:139]
	v_mov_b64_e32 v[26:27], v[142:143]
	s_and_b64 vcc, exec, s[6:7]
	v_mov_b64_e32 v[20:21], v[132:133]
	v_mov_b64_e32 v[24:25], v[136:137]
	v_mov_b64_e32 v[32:33], v[140:141]
	v_mov_b64_e32 v[28:29], v[144:145]
	s_cbranch_vccnz .LBB0_171
	v_pk_mul_f32 v[18:19], v[144:145], v[144:145]
	v_pk_mul_f32 v[20:21], v[142:143], v[142:143]
	s_nop 0
	v_pk_mov_b32 v[22:23], v[20:21], v[18:19] op_sel:[1,0]
	v_mov_b32_e32 v21, v19
	v_pk_add_f32 v[18:19], v[22:23], v[20:21]
	v_pk_mul_f32 v[20:21], v[140:141], v[140:141]
	v_pk_mul_f32 v[22:23], v[138:139], v[138:139]
	v_pk_add_f32 v[18:19], v[18:19], v[18:19] op_sel:[0,1] op_sel_hi:[1,0]
	v_pk_mov_b32 v[24:25], v[22:23], v[20:21] op_sel:[1,0]
	v_mov_b32_e32 v23, v21
	v_pk_add_f32 v[20:21], v[24:25], v[22:23]
	v_mul_f32_e32 v22, v130, v130
	v_mul_f32_e32 v23, v131, v131
	v_pk_add_f32 v[20:21], v[20:21], v[20:21] op_sel:[0,1] op_sel_hi:[1,0]
	v_mov_b32_e32 v19, v22
	v_mov_b32_e32 v21, v23
	v_pk_add_f32 v[18:19], v[18:19], v[20:21]
	v_mul_f32_e32 v20, v135, v135
	v_mul_f32_e32 v22, v137, v137
	v_mul_f32_e32 v24, v132, v132
	v_mul_f32_e32 v25, v133, v133
	v_pk_fma_f32 v[20:21], v[134:135], v[134:135], v[20:21] op_sel_hi:[1,1,0]
	v_pk_fma_f32 v[22:23], v[136:137], v[136:137], v[22:23] op_sel_hi:[1,1,0]
	v_mov_b32_e32 v21, v24
	v_mov_b32_e32 v23, v25
	v_pk_add_f32 v[20:21], v[20:21], v[22:23]
	s_nop 0
	v_pk_add_f32 v[18:19], v[18:19], v[20:21]
	v_and_b32_e32 v20, 64, v212
	v_add_f32_e32 v18, v18, v19
	v_xor_b32_e32 v19, 16, v212
	v_add_u32_e32 v20, 64, v20
	v_cmp_lt_i32_e32 vcc, v19, v20
	s_nop 1
	v_cndmask_b32_e32 v19, v212, v19, vcc
	v_lshlrev_b32_e32 v19, 2, v19
	ds_bpermute_b32 v19, v19, v18
	s_waitcnt lgkmcnt(0)
	v_add_f32_e32 v18, v18, v19
	v_xor_b32_e32 v19, 32, v212
	v_cmp_lt_i32_e32 vcc, v19, v20
	s_nop 1
	v_cndmask_b32_e32 v19, v212, v19, vcc
	v_lshlrev_b32_e32 v19, 2, v19
	ds_bpermute_b32 v19, v19, v18
	s_waitcnt lgkmcnt(0)
	v_add_f32_e32 v18, v18, v19
	v_fmamk_f32 v18, v18, 0x3c800000, v210
	v_mul_f32_e32 v19, 0x4f800000, v18
	v_cmp_gt_f32_e32 vcc, s28, v18
	s_nop 1
	v_cndmask_b32_e32 v18, v18, v19, vcc
	v_sqrt_f32_e32 v19, v18
	s_nop 0
	v_add_u32_e32 v20, -1, v19
	v_fma_f32 v21, -v20, v19, v18
	v_cmp_ge_f32_e64 s[10:11], 0, v21
	v_add_u32_e32 v21, 1, v19
	s_nop 0
	v_cndmask_b32_e64 v20, v19, v20, s[10:11]
	v_fma_f32 v19, -v21, v19, v18
	v_cmp_lt_f32_e64 s[10:11], 0, v19
	s_nop 1
	v_cndmask_b32_e64 v19, v20, v21, s[10:11]
	v_mul_f32_e32 v20, 0x37800000, v19
	v_cndmask_b32_e32 v19, v19, v20, vcc
	v_cmp_class_f32_e32 vcc, v18, v211
	s_nop 1
	v_cndmask_b32_e32 v18, v19, v18, vcc
	v_div_scale_f32 v19, s[0:1], v18, v18, 1.0
	v_rcp_f32_e32 v20, v19
	s_nop 0
	v_fma_f32 v21, -v19, v20, 1.0
	v_fmac_f32_e32 v20, v21, v20
	v_div_scale_f32 v21, vcc, 1.0, v18, 1.0
	v_mul_f32_e32 v22, v21, v20
	v_fma_f32 v23, -v19, v22, v21
	v_fmac_f32_e32 v22, v23, v20
	v_fma_f32 v19, -v19, v22, v21
	v_div_fmas_f32 v19, v19, v20, v22
	v_div_fixup_f32 v18, v19, v18, 1.0
	v_pk_mul_f32 v[20:21], v[142:143], v[18:19] op_sel_hi:[1,0]
	v_pk_mul_f32 v[22:23], v[144:145], v[18:19] op_sel_hi:[1,0]
	s_nop 0
	v_pk_mul_f32 v[26:27], v[14:15], v[20:21]
	v_pk_mul_f32 v[28:29], v[16:17], v[22:23]
	v_pk_mul_f32 v[20:21], v[138:139], v[18:19] op_sel_hi:[1,0]
	v_pk_mul_f32 v[22:23], v[140:141], v[18:19] op_sel_hi:[1,0]
	v_pk_mul_f32 v[30:31], v[10:11], v[20:21]
	v_pk_mul_f32 v[32:33], v[12:13], v[22:23]
	v_pk_mul_f32 v[20:21], v[134:135], v[18:19] op_sel_hi:[1,0]
	v_pk_mul_f32 v[22:23], v[136:137], v[18:19] op_sel_hi:[1,0]
	v_pk_mul_f32 v[162:163], v[130:131], v[18:19] op_sel_hi:[1,0]
	v_pk_mul_f32 v[18:19], v[132:133], v[18:19] op_sel_hi:[1,0]
	v_pk_mul_f32 v[24:25], v[8:9], v[22:23]
	v_pk_mul_f32 v[22:23], v[6:7], v[20:21]
	v_pk_mul_f32 v[20:21], v[4:5], v[18:19]
	v_pk_mul_f32 v[18:19], v[2:3], v[162:163]

; __device__ __forceinline__ unsigned pk4_fp8(float a, float b, float c, float d) { unsigned w = 0u; w = __builtin_amdgcn_cvt_pk_fp8_f32(a, b, w, false); w = __builtin_amdgcn_cvt_pk_fp8_f32(c, d, w, true); return w; }
; template <bool F8OUT = false> __device__ __forceinline__ void head_tile_store(const f32x4 (&acc)[2][2][4][2], bf16_t* obase  , int opitch, const float* gain, float scale, const f32x2e* rope, int row0, int fq) {
;     ...
;             if (gain) {
;                 float ss = 0.f;
; #pragma unroll
;                 for (int bj = 0; bj < 2; ++bj)
; #pragma unroll
;                     for (int n = 0; n < 2; ++n) ss += (x[bj][n][0] * x[bj][n][0] + x[bj][n][1] * x[bj][n][1]) + (x[bj][n][2] * x[bj][n][2] + x[bj][n][3] * x[bj][n][3]);
;                 ss += __shfl_xor(ss, 16); ss += __shfl_xor(ss, 32);
;                 const float r = scale / sqrtf(ss * (1.f / 64.f) + 1e-6f);
; #pragma unroll
;                 for (int bj = 0; bj < 2; ++bj)
; #pragma unroll
;                     for (int n = 0; n < 2; ++n) x[bj][n] = x[bj][n] * r * g[bj][n];
;             }
;     ...
;             if constexpr (F8OUT) { unsigned char* rowp8 = (unsigned char*)obase + (size_t)row * opitch + 8 * fq; typedef unsigned u32x2_ __attribute__((ext_vector_type(2)));
; #pragma unroll
;                 for (int bj = 0; bj < 2; ++bj) *(u32x2_*)(rowp8 + 32 * bj) = (u32x2_){pk4_fp8(x[bj][0][0], x[bj][0][1], x[bj][0][2], x[bj][0][3]), pk4_fp8(x[bj][1][0], x[bj][1][1], x[bj][1][2], x[bj][1][3])};
;                 continue; }
.LBB0_173:
	v_mov_b32_e32 v164, v175
	v_cvt_pk_fp8_f32 v164, v26, v27
	v_mov_b32_e32 v26, v175
	v_mov_b32_e32 v27, v175
	v_cvt_pk_fp8_f32 v26, v22, v23
	v_cvt_pk_fp8_f32 v27, v18, v19
	v_mov_b32_e32 v165, v175
	v_cvt_pk_fp8_f32 v165, v30, v31
	v_cvt_pk_fp8_f32 v26, v24, v25 op_sel:[0,0,1]
	v_cvt_pk_fp8_f32 v27, v20, v21 op_sel:[0,0,1]
	v_ashrrev_i32_e32 v195, 31, v194
	v_lshlrev_b64 v[162:163], 7, v[194:195]
	v_cvt_pk_fp8_f32 v164, v28, v29 op_sel:[0,0,1]
	v_cvt_pk_fp8_f32 v165, v32, v33 op_sel:[0,0,1]
	v_lshl_add_u64 v[162:163], v[190:191], 0, v[162:163]
	global_store_dwordx2 v[162:163], v[26:27], off offset:32
	v_mov_b64_e32 v[18:19], v[114:115]
	v_mov_b64_e32 v[22:23], v[118:119]
	v_mov_b64_e32 v[30:31], v[122:123]
	v_mov_b64_e32 v[26:27], v[126:127]
	s_and_b64 vcc, exec, s[6:7]
	v_mov_b64_e32 v[20:21], v[116:117]
	v_mov_b64_e32 v[24:25], v[120:121]
	v_mov_b64_e32 v[32:33], v[124:125]
	v_mov_b64_e32 v[28:29], v[128:129]
	global_store_dwordx2 v[162:163], v[164:165], off
	s_cbranch_vccnz .LBB0_175
	v_pk_mul_f32 v[18:19], v[128:129], v[128:129]
	v_pk_mul_f32 v[20:21], v[126:127], v[126:127]
	s_nop 0
	v_pk_mov_b32 v[22:23], v[20:21], v[18:19] op_sel:[1,0]
	v_mov_b32_e32 v21, v19
	v_pk_add_f32 v[18:19], v[22:23], v[20:21]
	v_pk_mul_f32 v[20:21], v[124:125], v[124:125]
	v_pk_mul_f32 v[22:23], v[122:123], v[122:123]
	v_pk_add_f32 v[18:19], v[18:19], v[18:19] op_sel:[0,1] op_sel_hi:[1,0]
	v_pk_mov_b32 v[24:25], v[22:23], v[20:21] op_sel:[1,0]
	v_mov_b32_e32 v23, v21
	v_pk_add_f32 v[20:21], v[24:25], v[22:23]
	v_mul_f32_e32 v22, v114, v114
	v_mul_f32_e32 v23, v115, v115
	v_pk_add_f32 v[20:21], v[20:21], v[20:21] op_sel:[0,1] op_sel_hi:[1,0]
	v_mov_b32_e32 v19, v22
	v_mov_b32_e32 v21, v23
	v_pk_add_f32 v[18:19], v[18:19], v[20:21]
	v_mul_f32_e32 v20, v119, v119
	v_mul_f32_e32 v22, v121, v121
	v_mul_f32_e32 v24, v116, v116
	v_mul_f32_e32 v25, v117, v117
	v_pk_fma_f32 v[20:21], v[118:119], v[118:119], v[20:21] op_sel_hi:[1,1,0]
	v_pk_fma_f32 v[22:23], v[120:121], v[120:121], v[22:23] op_sel_hi:[1,1,0]
	v_mov_b32_e32 v21, v24
	v_mov_b32_e32 v23, v25
	v_pk_add_f32 v[20:21], v[20:21], v[22:23]
	s_nop 0
	v_pk_add_f32 v[18:19], v[18:19], v[20:21]
	v_and_b32_e32 v20, 64, v212
	v_add_f32_e32 v18, v18, v19
	v_xor_b32_e32 v19, 16, v212
	v_add_u32_e32 v20, 64, v20
	v_cmp_lt_i32_e32 vcc, v19, v20
	s_nop 1
	v_cndmask_b32_e32 v19, v212, v19, vcc
	v_lshlrev_b32_e32 v19, 2, v19
	ds_bpermute_b32 v19, v19, v18
	s_waitcnt lgkmcnt(0)
	v_add_f32_e32 v18, v18, v19
	v_xor_b32_e32 v19, 32, v212
	v_cmp_lt_i32_e32 vcc, v19, v20
	s_nop 1
	v_cndmask_b32_e32 v19, v212, v19, vcc
	v_lshlrev_b32_e32 v19, 2, v19
	ds_bpermute_b32 v19, v19, v18
	s_waitcnt lgkmcnt(0)
	v_add_f32_e32 v18, v18, v19
	v_fmamk_f32 v18, v18, 0x3c800000, v210
	v_mul_f32_e32 v19, 0x4f800000, v18
	v_cmp_gt_f32_e32 vcc, s28, v18
	s_nop 1
	v_cndmask_b32_e32 v18, v18, v19, vcc
	v_sqrt_f32_e32 v19, v18
	s_nop 0
	v_add_u32_e32 v20, -1, v19
	v_fma_f32 v21, -v20, v19, v18
	v_cmp_ge_f32_e64 s[10:11], 0, v21
	v_add_u32_e32 v21, 1, v19
	s_nop 0
	v_cndmask_b32_e64 v20, v19, v20, s[10:11]
	v_fma_f32 v19, -v21, v19, v18
	v_cmp_lt_f32_e64 s[10:11], 0, v19
	s_nop 1
	v_cndmask_b32_e64 v19, v20, v21, s[10:11]
	v_mul_f32_e32 v20, 0x37800000, v19
	v_cndmask_b32_e32 v19, v19, v20, vcc
	v_cmp_class_f32_e32 vcc, v18, v211
	s_nop 1
	v_cndmask_b32_e32 v18, v19, v18, vcc
	v_div_scale_f32 v19, s[0:1], v18, v18, 1.0
	v_rcp_f32_e32 v20, v19
	s_nop 0
	v_fma_f32 v21, -v19, v20, 1.0
	v_fmac_f32_e32 v20, v21, v20
	v_div_scale_f32 v21, vcc, 1.0, v18, 1.0
	v_mul_f32_e32 v22, v21, v20
	v_fma_f32 v23, -v19, v22, v21
	v_fmac_f32_e32 v22, v23, v20
	v_fma_f32 v19, -v19, v22, v21
	v_div_fmas_f32 v19, v19, v20, v22
	v_div_fixup_f32 v18, v19, v18, 1.0
	v_pk_mul_f32 v[20:21], v[126:127], v[18:19] op_sel_hi:[1,0]
	v_pk_mul_f32 v[22:23], v[128:129], v[18:19] op_sel_hi:[1,0]
	s_nop 0
	v_pk_mul_f32 v[26:27], v[14:15], v[20:21]
	v_pk_mul_f32 v[28:29], v[16:17], v[22:23]
	v_pk_mul_f32 v[20:21], v[122:123], v[18:19] op_sel_hi:[1,0]
	v_pk_mul_f32 v[22:23], v[124:125], v[18:19] op_sel_hi:[1,0]
	v_pk_mul_f32 v[30:31], v[10:11], v[20:21]
	v_pk_mul_f32 v[32:33], v[12:13], v[22:23]
	v_pk_mul_f32 v[20:21], v[118:119], v[18:19] op_sel_hi:[1,0]
	v_pk_mul_f32 v[22:23], v[120:121], v[18:19] op_sel_hi:[1,0]
	v_pk_mul_f32 v[162:163], v[114:115], v[18:19] op_sel_hi:[1,0]
	v_pk_mul_f32 v[18:19], v[116:117], v[18:19] op_sel_hi:[1,0]
	v_pk_mul_f32 v[24:25], v[8:9], v[22:23]
	v_pk_mul_f32 v[22:23], v[6:7], v[20:21]
	v_pk_mul_f32 v[20:21], v[4:5], v[18:19]
	v_pk_mul_f32 v[18:19], v[2:3], v[162:163]

; __device__ __forceinline__ unsigned pk4_fp8(float a, float b, float c, float d) { unsigned w = 0u; w = __builtin_amdgcn_cvt_pk_fp8_f32(a, b, w, false); w = __builtin_amdgcn_cvt_pk_fp8_f32(c, d, w, true); return w; }
; template <bool F8OUT = false> __device__ __forceinline__ void head_tile_store(const f32x4 (&acc)[2][2][4][2], bf16_t* obase  , int opitch, const float* gain, float scale, const f32x2e* rope, int row0, int fq) {
;     ...
;             if (gain) {
;                 float ss = 0.f;
; #pragma unroll
;                 for (int bj = 0; bj < 2; ++bj)
; #pragma unroll
;                     for (int n = 0; n < 2; ++n) ss += (x[bj][n][0] * x[bj][n][0] + x[bj][n][1] * x[bj][n][1]) + (x[bj][n][2] * x[bj][n][2] + x[bj][n][3] * x[bj][n][3]);
;                 ss += __shfl_xor(ss, 16); ss += __shfl_xor(ss, 32);
;                 const float r = scale / sqrtf(ss * (1.f / 64.f) + 1e-6f);
; #pragma unroll
;                 for (int bj = 0; bj < 2; ++bj)
; #pragma unroll
;                     for (int n = 0; n < 2; ++n) x[bj][n] = x[bj][n] * r * g[bj][n];
;             }
;     ...
;             if constexpr (F8OUT) { unsigned char* rowp8 = (unsigned char*)obase + (size_t)row * opitch + 8 * fq; typedef unsigned u32x2_ __attribute__((ext_vector_type(2)));
; #pragma unroll
;                 for (int bj = 0; bj < 2; ++bj) *(u32x2_*)(rowp8 + 32 * bj) = (u32x2_){pk4_fp8(x[bj][0][0], x[bj][0][1], x[bj][0][2], x[bj][0][3]), pk4_fp8(x[bj][1][0], x[bj][1][1], x[bj][1][2], x[bj][1][3])};
;                 continue; }
.LBB0_177:
	v_mov_b32_e32 v164, v175
	v_cvt_pk_fp8_f32 v164, v26, v27
	v_mov_b32_e32 v26, v175
	v_mov_b32_e32 v27, v175
	v_cvt_pk_fp8_f32 v26, v22, v23
	v_cvt_pk_fp8_f32 v27, v18, v19
	v_mov_b32_e32 v165, v175
	v_cvt_pk_fp8_f32 v165, v30, v31
	v_cvt_pk_fp8_f32 v26, v24, v25 op_sel:[0,0,1]
	v_cvt_pk_fp8_f32 v27, v20, v21 op_sel:[0,0,1]
	v_ashrrev_i32_e32 v197, 31, v196
	v_lshlrev_b64 v[162:163], 7, v[196:197]
	v_cvt_pk_fp8_f32 v164, v28, v29 op_sel:[0,0,1]
	v_cvt_pk_fp8_f32 v165, v32, v33 op_sel:[0,0,1]
	v_lshl_add_u64 v[162:163], v[190:191], 0, v[162:163]
	global_store_dwordx2 v[162:163], v[26:27], off offset:32
	v_mov_b64_e32 v[18:19], v[98:99]
	v_mov_b64_e32 v[22:23], v[102:103]
	v_mov_b64_e32 v[30:31], v[106:107]
	v_mov_b64_e32 v[26:27], v[110:111]
	s_and_b64 vcc, exec, s[6:7]
	v_mov_b64_e32 v[20:21], v[100:101]
	v_mov_b64_e32 v[24:25], v[104:105]
	v_mov_b64_e32 v[32:33], v[108:109]
	v_mov_b64_e32 v[28:29], v[112:113]
	global_store_dwordx2 v[162:163], v[164:165], off
	s_cbranch_vccnz .LBB0_179
	v_pk_mul_f32 v[18:19], v[112:113], v[112:113]
	v_pk_mul_f32 v[20:21], v[110:111], v[110:111]
	s_nop 0
	v_pk_mov_b32 v[22:23], v[20:21], v[18:19] op_sel:[1,0]
	v_mov_b32_e32 v21, v19
	v_pk_add_f32 v[18:19], v[22:23], v[20:21]
	v_pk_mul_f32 v[20:21], v[108:109], v[108:109]
	v_pk_mul_f32 v[22:23], v[106:107], v[106:107]
	v_pk_add_f32 v[18:19], v[18:19], v[18:19] op_sel:[0,1] op_sel_hi:[1,0]
	v_pk_mov_b32 v[24:25], v[22:23], v[20:21] op_sel:[1,0]
	v_mov_b32_e32 v23, v21
	v_pk_add_f32 v[20:21], v[24:25], v[22:23]
	v_mul_f32_e32 v22, v98, v98
	v_mul_f32_e32 v23, v99, v99
	v_pk_add_f32 v[20:21], v[20:21], v[20:21] op_sel:[0,1] op_sel_hi:[1,0]
	v_mov_b32_e32 v19, v22
	v_mov_b32_e32 v21, v23
	v_pk_add_f32 v[18:19], v[18:19], v[20:21]
	v_mul_f32_e32 v20, v103, v103
	v_mul_f32_e32 v22, v105, v105
	v_mul_f32_e32 v24, v100, v100
	v_mul_f32_e32 v25, v101, v101
	v_pk_fma_f32 v[20:21], v[102:103], v[102:103], v[20:21] op_sel_hi:[1,1,0]
	v_pk_fma_f32 v[22:23], v[104:105], v[104:105], v[22:23] op_sel_hi:[1,1,0]
	v_mov_b32_e32 v21, v24
	v_mov_b32_e32 v23, v25
	v_pk_add_f32 v[20:21], v[20:21], v[22:23]
	s_nop 0
	v_pk_add_f32 v[18:19], v[18:19], v[20:21]
	v_and_b32_e32 v20, 64, v212
	v_add_f32_e32 v18, v18, v19
	v_xor_b32_e32 v19, 16, v212
	v_add_u32_e32 v20, 64, v20
	v_cmp_lt_i32_e32 vcc, v19, v20
	s_nop 1
	v_cndmask_b32_e32 v19, v212, v19, vcc
	v_lshlrev_b32_e32 v19, 2, v19
	ds_bpermute_b32 v19, v19, v18
	s_waitcnt lgkmcnt(0)
	v_add_f32_e32 v18, v18, v19
	v_xor_b32_e32 v19, 32, v212
	v_cmp_lt_i32_e32 vcc, v19, v20
	s_nop 1
	v_cndmask_b32_e32 v19, v212, v19, vcc
	v_lshlrev_b32_e32 v19, 2, v19
	ds_bpermute_b32 v19, v19, v18
	s_waitcnt lgkmcnt(0)
	v_add_f32_e32 v18, v18, v19
	v_fmamk_f32 v18, v18, 0x3c800000, v210
	v_mul_f32_e32 v19, 0x4f800000, v18
	v_cmp_gt_f32_e32 vcc, s28, v18
	s_nop 1
	v_cndmask_b32_e32 v18, v18, v19, vcc
	v_sqrt_f32_e32 v19, v18
	s_nop 0
	v_add_u32_e32 v20, -1, v19
	v_fma_f32 v21, -v20, v19, v18
	v_cmp_ge_f32_e64 s[10:11], 0, v21
	v_add_u32_e32 v21, 1, v19
	s_nop 0
	v_cndmask_b32_e64 v20, v19, v20, s[10:11]
	v_fma_f32 v19, -v21, v19, v18
	v_cmp_lt_f32_e64 s[10:11], 0, v19
	s_nop 1
	v_cndmask_b32_e64 v19, v20, v21, s[10:11]
	v_mul_f32_e32 v20, 0x37800000, v19
	v_cndmask_b32_e32 v19, v19, v20, vcc
	v_cmp_class_f32_e32 vcc, v18, v211
	s_nop 1
	v_cndmask_b32_e32 v18, v19, v18, vcc
	v_div_scale_f32 v19, s[0:1], v18, v18, 1.0
	v_rcp_f32_e32 v20, v19
	s_nop 0
	v_fma_f32 v21, -v19, v20, 1.0
	v_fmac_f32_e32 v20, v21, v20
	v_div_scale_f32 v21, vcc, 1.0, v18, 1.0
	v_mul_f32_e32 v22, v21, v20
	v_fma_f32 v23, -v19, v22, v21
	v_fmac_f32_e32 v22, v23, v20
	v_fma_f32 v19, -v19, v22, v21
	v_div_fmas_f32 v19, v19, v20, v22
	v_div_fixup_f32 v18, v19, v18, 1.0
	v_pk_mul_f32 v[20:21], v[110:111], v[18:19] op_sel_hi:[1,0]
	v_pk_mul_f32 v[22:23], v[112:113], v[18:19] op_sel_hi:[1,0]
	s_nop 0
	v_pk_mul_f32 v[26:27], v[14:15], v[20:21]
	v_pk_mul_f32 v[28:29], v[16:17], v[22:23]
	v_pk_mul_f32 v[20:21], v[106:107], v[18:19] op_sel_hi:[1,0]
	v_pk_mul_f32 v[22:23], v[108:109], v[18:19] op_sel_hi:[1,0]
	v_pk_mul_f32 v[30:31], v[10:11], v[20:21]
	v_pk_mul_f32 v[32:33], v[12:13], v[22:23]
	v_pk_mul_f32 v[20:21], v[102:103], v[18:19] op_sel_hi:[1,0]
	v_pk_mul_f32 v[22:23], v[104:105], v[18:19] op_sel_hi:[1,0]
	v_pk_mul_f32 v[162:163], v[98:99], v[18:19] op_sel_hi:[1,0]
	v_pk_mul_f32 v[18:19], v[100:101], v[18:19] op_sel_hi:[1,0]
	v_pk_mul_f32 v[24:25], v[8:9], v[22:23]
	v_pk_mul_f32 v[22:23], v[6:7], v[20:21]
	v_pk_mul_f32 v[20:21], v[4:5], v[18:19]
	v_pk_mul_f32 v[18:19], v[2:3], v[162:163]

; __device__ __forceinline__ unsigned pk4_fp8(float a, float b, float c, float d) { unsigned w = 0u; w = __builtin_amdgcn_cvt_pk_fp8_f32(a, b, w, false); w = __builtin_amdgcn_cvt_pk_fp8_f32(c, d, w, true); return w; }
; template <bool F8OUT = false> __device__ __forceinline__ void head_tile_store(const f32x4 (&acc)[2][2][4][2], bf16_t* obase  , int opitch, const float* gain, float scale, const f32x2e* rope, int row0, int fq) {
;     ...
;             if (gain) {
;                 float ss = 0.f;
; #pragma unroll
;                 for (int bj = 0; bj < 2; ++bj)
; #pragma unroll
;                     for (int n = 0; n < 2; ++n) ss += (x[bj][n][0] * x[bj][n][0] + x[bj][n][1] * x[bj][n][1]) + (x[bj][n][2] * x[bj][n][2] + x[bj][n][3] * x[bj][n][3]);
;                 ss += __shfl_xor(ss, 16); ss += __shfl_xor(ss, 32);
;                 const float r = scale / sqrtf(ss * (1.f / 64.f) + 1e-6f);
; #pragma unroll
;                 for (int bj = 0; bj < 2; ++bj)
; #pragma unroll
;                     for (int n = 0; n < 2; ++n) x[bj][n] = x[bj][n] * r * g[bj][n];
;             }
;     ...
;             if constexpr (F8OUT) { unsigned char* rowp8 = (unsigned char*)obase + (size_t)row * opitch + 8 * fq; typedef unsigned u32x2_ __attribute__((ext_vector_type(2)));
; #pragma unroll
;                 for (int bj = 0; bj < 2; ++bj) *(u32x2_*)(rowp8 + 32 * bj) = (u32x2_){pk4_fp8(x[bj][0][0], x[bj][0][1], x[bj][0][2], x[bj][0][3]), pk4_fp8(x[bj][1][0], x[bj][1][1], x[bj][1][2], x[bj][1][3])};
;                 continue; }
.LBB0_181:
	v_mov_b32_e32 v164, v175
	v_cvt_pk_fp8_f32 v164, v26, v27
	v_mov_b32_e32 v26, v175
	v_mov_b32_e32 v27, v175
	v_cvt_pk_fp8_f32 v26, v22, v23
	v_cvt_pk_fp8_f32 v27, v18, v19
	v_mov_b32_e32 v165, v175
	v_cvt_pk_fp8_f32 v165, v30, v31
	v_cvt_pk_fp8_f32 v26, v24, v25 op_sel:[0,0,1]
	v_cvt_pk_fp8_f32 v27, v20, v21 op_sel:[0,0,1]
	v_ashrrev_i32_e32 v201, 31, v200
	v_lshlrev_b64 v[162:163], 7, v[200:201]
	v_cvt_pk_fp8_f32 v164, v28, v29 op_sel:[0,0,1]
	v_cvt_pk_fp8_f32 v165, v32, v33 op_sel:[0,0,1]
	v_lshl_add_u64 v[162:163], v[190:191], 0, v[162:163]
	global_store_dwordx2 v[162:163], v[26:27], off offset:32
	v_mov_b64_e32 v[18:19], v[82:83]
	v_mov_b64_e32 v[22:23], v[86:87]
	v_mov_b64_e32 v[30:31], v[90:91]
	v_mov_b64_e32 v[26:27], v[94:95]
	s_and_b64 vcc, exec, s[6:7]
	v_mov_b64_e32 v[20:21], v[84:85]
	v_mov_b64_e32 v[24:25], v[88:89]
	v_mov_b64_e32 v[32:33], v[92:93]
	v_mov_b64_e32 v[28:29], v[96:97]
	global_store_dwordx2 v[162:163], v[164:165], off
	s_cbranch_vccnz .LBB0_183
	v_pk_mul_f32 v[18:19], v[96:97], v[96:97]
	v_pk_mul_f32 v[20:21], v[94:95], v[94:95]
	s_nop 0
	v_pk_mov_b32 v[22:23], v[20:21], v[18:19] op_sel:[1,0]
	v_mov_b32_e32 v21, v19
	v_pk_add_f32 v[18:19], v[22:23], v[20:21]
	v_pk_mul_f32 v[20:21], v[92:93], v[92:93]
	v_pk_mul_f32 v[22:23], v[90:91], v[90:91]
	v_pk_add_f32 v[18:19], v[18:19], v[18:19] op_sel:[0,1] op_sel_hi:[1,0]
	v_pk_mov_b32 v[24:25], v[22:23], v[20:21] op_sel:[1,0]
	v_mov_b32_e32 v23, v21
	v_pk_add_f32 v[20:21], v[24:25], v[22:23]
	v_mul_f32_e32 v22, v82, v82
	v_mul_f32_e32 v23, v83, v83
	v_pk_add_f32 v[20:21], v[20:21], v[20:21] op_sel:[0,1] op_sel_hi:[1,0]
	v_mov_b32_e32 v19, v22
	v_mov_b32_e32 v21, v23
	v_pk_add_f32 v[18:19], v[18:19], v[20:21]
	v_mul_f32_e32 v20, v87, v87
	v_mul_f32_e32 v22, v89, v89
	v_mul_f32_e32 v24, v84, v84
	v_mul_f32_e32 v25, v85, v85
	v_pk_fma_f32 v[20:21], v[86:87], v[86:87], v[20:21] op_sel_hi:[1,1,0]
	v_pk_fma_f32 v[22:23], v[88:89], v[88:89], v[22:23] op_sel_hi:[1,1,0]
	v_mov_b32_e32 v21, v24
	v_mov_b32_e32 v23, v25
	v_pk_add_f32 v[20:21], v[20:21], v[22:23]
	s_nop 0
	v_pk_add_f32 v[18:19], v[18:19], v[20:21]
	v_and_b32_e32 v20, 64, v212
	v_add_f32_e32 v18, v18, v19
	v_xor_b32_e32 v19, 16, v212
	v_add_u32_e32 v20, 64, v20
	v_cmp_lt_i32_e32 vcc, v19, v20
	s_nop 1
	v_cndmask_b32_e32 v19, v212, v19, vcc
	v_lshlrev_b32_e32 v19, 2, v19
	ds_bpermute_b32 v19, v19, v18
	s_waitcnt lgkmcnt(0)
	v_add_f32_e32 v18, v18, v19
	v_xor_b32_e32 v19, 32, v212
	v_cmp_lt_i32_e32 vcc, v19, v20
	s_nop 1
	v_cndmask_b32_e32 v19, v212, v19, vcc
	v_lshlrev_b32_e32 v19, 2, v19
	ds_bpermute_b32 v19, v19, v18
	s_waitcnt lgkmcnt(0)
	v_add_f32_e32 v18, v18, v19
	v_fmamk_f32 v18, v18, 0x3c800000, v210
	v_mul_f32_e32 v19, 0x4f800000, v18
	v_cmp_gt_f32_e32 vcc, s28, v18
	s_nop 1
	v_cndmask_b32_e32 v18, v18, v19, vcc
	v_sqrt_f32_e32 v19, v18
	s_nop 0
	v_add_u32_e32 v20, -1, v19
	v_fma_f32 v21, -v20, v19, v18
	v_cmp_ge_f32_e64 s[10:11], 0, v21
	v_add_u32_e32 v21, 1, v19
	s_nop 0
	v_cndmask_b32_e64 v20, v19, v20, s[10:11]
	v_fma_f32 v19, -v21, v19, v18
	v_cmp_lt_f32_e64 s[10:11], 0, v19
	s_nop 1
	v_cndmask_b32_e64 v19, v20, v21, s[10:11]
	v_mul_f32_e32 v20, 0x37800000, v19
	v_cndmask_b32_e32 v19, v19, v20, vcc
	v_cmp_class_f32_e32 vcc, v18, v211
	s_nop 1
	v_cndmask_b32_e32 v18, v19, v18, vcc
	v_div_scale_f32 v19, s[0:1], v18, v18, 1.0
	v_rcp_f32_e32 v20, v19
	s_nop 0
	v_fma_f32 v21, -v19, v20, 1.0
	v_fmac_f32_e32 v20, v21, v20
	v_div_scale_f32 v21, vcc, 1.0, v18, 1.0
	v_mul_f32_e32 v22, v21, v20
	v_fma_f32 v23, -v19, v22, v21
	v_fmac_f32_e32 v22, v23, v20
	v_fma_f32 v19, -v19, v22, v21
	v_div_fmas_f32 v19, v19, v20, v22
	v_div_fixup_f32 v18, v19, v18, 1.0
	v_pk_mul_f32 v[20:21], v[94:95], v[18:19] op_sel_hi:[1,0]
	v_pk_mul_f32 v[22:23], v[96:97], v[18:19] op_sel_hi:[1,0]
	s_nop 0
	v_pk_mul_f32 v[26:27], v[14:15], v[20:21]
	v_pk_mul_f32 v[28:29], v[16:17], v[22:23]
	v_pk_mul_f32 v[20:21], v[90:91], v[18:19] op_sel_hi:[1,0]
	v_pk_mul_f32 v[22:23], v[92:93], v[18:19] op_sel_hi:[1,0]
	v_pk_mul_f32 v[30:31], v[10:11], v[20:21]
	v_pk_mul_f32 v[32:33], v[12:13], v[22:23]
	v_pk_mul_f32 v[20:21], v[86:87], v[18:19] op_sel_hi:[1,0]
	v_pk_mul_f32 v[22:23], v[88:89], v[18:19] op_sel_hi:[1,0]
	v_pk_mul_f32 v[162:163], v[82:83], v[18:19] op_sel_hi:[1,0]
	v_pk_mul_f32 v[18:19], v[84:85], v[18:19] op_sel_hi:[1,0]
	v_pk_mul_f32 v[24:25], v[8:9], v[22:23]
	v_pk_mul_f32 v[22:23], v[6:7], v[20:21]
	v_pk_mul_f32 v[20:21], v[4:5], v[18:19]
	v_pk_mul_f32 v[18:19], v[2:3], v[162:163]

; __device__ __forceinline__ unsigned pk4_fp8(float a, float b, float c, float d) { unsigned w = 0u; w = __builtin_amdgcn_cvt_pk_fp8_f32(a, b, w, false); w = __builtin_amdgcn_cvt_pk_fp8_f32(c, d, w, true); return w; }
; template <bool F8OUT = false> __device__ __forceinline__ void head_tile_store(const f32x4 (&acc)[2][2][4][2], bf16_t* obase  , int opitch, const float* gain, float scale, const f32x2e* rope, int row0, int fq) {
;     ...
;             if (gain) {
;                 float ss = 0.f;
; #pragma unroll
;                 for (int bj = 0; bj < 2; ++bj)
; #pragma unroll
;                     for (int n = 0; n < 2; ++n) ss += (x[bj][n][0] * x[bj][n][0] + x[bj][n][1] * x[bj][n][1]) + (x[bj][n][2] * x[bj][n][2] + x[bj][n][3] * x[bj][n][3]);
;                 ss += __shfl_xor(ss, 16); ss += __shfl_xor(ss, 32);
;                 const float r = scale / sqrtf(ss * (1.f / 64.f) + 1e-6f);
; #pragma unroll
;                 for (int bj = 0; bj < 2; ++bj)
; #pragma unroll
;                     for (int n = 0; n < 2; ++n) x[bj][n] = x[bj][n] * r * g[bj][n];
;             }
;     ...
;             if constexpr (F8OUT) { unsigned char* rowp8 = (unsigned char*)obase + (size_t)row * opitch + 8 * fq; typedef unsigned u32x2_ __attribute__((ext_vector_type(2)));
; #pragma unroll
;                 for (int bj = 0; bj < 2; ++bj) *(u32x2_*)(rowp8 + 32 * bj) = (u32x2_){pk4_fp8(x[bj][0][0], x[bj][0][1], x[bj][0][2], x[bj][0][3]), pk4_fp8(x[bj][1][0], x[bj][1][1], x[bj][1][2], x[bj][1][3])};
;                 continue; }
.LBB0_185:
	v_mov_b32_e32 v164, v175
	v_cvt_pk_fp8_f32 v164, v26, v27
	v_mov_b32_e32 v26, v175
	v_mov_b32_e32 v27, v175
	v_cvt_pk_fp8_f32 v26, v22, v23
	v_cvt_pk_fp8_f32 v27, v18, v19
	v_mov_b32_e32 v165, v175
	v_cvt_pk_fp8_f32 v165, v30, v31
	v_cvt_pk_fp8_f32 v26, v24, v25 op_sel:[0,0,1]
	v_cvt_pk_fp8_f32 v27, v20, v21 op_sel:[0,0,1]
	v_ashrrev_i32_e32 v201, 31, v200
	v_lshlrev_b64 v[162:163], 7, v[200:201]
	v_cvt_pk_fp8_f32 v164, v28, v29 op_sel:[0,0,1]
	v_cvt_pk_fp8_f32 v165, v32, v33 op_sel:[0,0,1]
	v_lshl_add_u64 v[162:163], v[190:191], 0, v[162:163]
	global_store_dwordx2 v[162:163], v[26:27], off offset:32
	v_mov_b64_e32 v[18:19], v[66:67]
	v_mov_b64_e32 v[22:23], v[70:71]
	v_mov_b64_e32 v[30:31], v[74:75]
	v_mov_b64_e32 v[26:27], v[78:79]
	s_and_b64 vcc, exec, s[6:7]
	v_mov_b64_e32 v[20:21], v[68:69]
	v_mov_b64_e32 v[24:25], v[72:73]
	v_mov_b64_e32 v[32:33], v[76:77]
	v_mov_b64_e32 v[28:29], v[80:81]
	global_store_dwordx2 v[162:163], v[164:165], off
	s_cbranch_vccnz .LBB0_187
	v_pk_mul_f32 v[18:19], v[80:81], v[80:81]
	v_pk_mul_f32 v[20:21], v[78:79], v[78:79]
	s_nop 0
	v_pk_mov_b32 v[22:23], v[20:21], v[18:19] op_sel:[1,0]
	v_mov_b32_e32 v21, v19
	v_pk_add_f32 v[18:19], v[22:23], v[20:21]
	v_pk_mul_f32 v[20:21], v[76:77], v[76:77]
	v_pk_mul_f32 v[22:23], v[74:75], v[74:75]
	v_pk_add_f32 v[18:19], v[18:19], v[18:19] op_sel:[0,1] op_sel_hi:[1,0]
	v_pk_mov_b32 v[24:25], v[22:23], v[20:21] op_sel:[1,0]
	v_mov_b32_e32 v23, v21
	v_pk_add_f32 v[20:21], v[24:25], v[22:23]
	v_mul_f32_e32 v22, v66, v66
	v_mul_f32_e32 v23, v67, v67
	v_pk_add_f32 v[20:21], v[20:21], v[20:21] op_sel:[0,1] op_sel_hi:[1,0]
	v_mov_b32_e32 v19, v22
	v_mov_b32_e32 v21, v23
	v_pk_add_f32 v[18:19], v[18:19], v[20:21]
	v_mul_f32_e32 v20, v71, v71
	v_mul_f32_e32 v22, v73, v73
	v_mul_f32_e32 v24, v68, v68
	v_mul_f32_e32 v25, v69, v69
	v_pk_fma_f32 v[20:21], v[70:71], v[70:71], v[20:21] op_sel_hi:[1,1,0]
	v_pk_fma_f32 v[22:23], v[72:73], v[72:73], v[22:23] op_sel_hi:[1,1,0]
	v_mov_b32_e32 v21, v24
	v_mov_b32_e32 v23, v25
	v_pk_add_f32 v[20:21], v[20:21], v[22:23]
	s_nop 0
	v_pk_add_f32 v[18:19], v[18:19], v[20:21]
	v_and_b32_e32 v20, 64, v212
	v_add_f32_e32 v18, v18, v19
	v_xor_b32_e32 v19, 16, v212
	v_add_u32_e32 v20, 64, v20
	v_cmp_lt_i32_e32 vcc, v19, v20
	s_nop 1
	v_cndmask_b32_e32 v19, v212, v19, vcc
	v_lshlrev_b32_e32 v19, 2, v19
	ds_bpermute_b32 v19, v19, v18
	s_waitcnt lgkmcnt(0)
	v_add_f32_e32 v18, v18, v19
	v_xor_b32_e32 v19, 32, v212
	v_cmp_lt_i32_e32 vcc, v19, v20
	s_nop 1
	v_cndmask_b32_e32 v19, v212, v19, vcc
	v_lshlrev_b32_e32 v19, 2, v19
	ds_bpermute_b32 v19, v19, v18
	s_waitcnt lgkmcnt(0)
	v_add_f32_e32 v18, v18, v19
	v_fmamk_f32 v18, v18, 0x3c800000, v210
	v_mul_f32_e32 v19, 0x4f800000, v18
	v_cmp_gt_f32_e32 vcc, s28, v18
	s_nop 1
	v_cndmask_b32_e32 v18, v18, v19, vcc
	v_sqrt_f32_e32 v19, v18
	s_nop 0
	v_add_u32_e32 v20, -1, v19
	v_fma_f32 v21, -v20, v19, v18
	v_cmp_ge_f32_e64 s[10:11], 0, v21
	v_add_u32_e32 v21, 1, v19
	s_nop 0
	v_cndmask_b32_e64 v20, v19, v20, s[10:11]
	v_fma_f32 v19, -v21, v19, v18
	v_cmp_lt_f32_e64 s[10:11], 0, v19
	s_nop 1
	v_cndmask_b32_e64 v19, v20, v21, s[10:11]
	v_mul_f32_e32 v20, 0x37800000, v19
	v_cndmask_b32_e32 v19, v19, v20, vcc
	v_cmp_class_f32_e32 vcc, v18, v211
	s_nop 1
	v_cndmask_b32_e32 v18, v19, v18, vcc
	v_div_scale_f32 v19, s[0:1], v18, v18, 1.0
	v_rcp_f32_e32 v20, v19
	s_nop 0
	v_fma_f32 v21, -v19, v20, 1.0
	v_fmac_f32_e32 v20, v21, v20
	v_div_scale_f32 v21, vcc, 1.0, v18, 1.0
	v_mul_f32_e32 v22, v21, v20
	v_fma_f32 v23, -v19, v22, v21
	v_fmac_f32_e32 v22, v23, v20
	v_fma_f32 v19, -v19, v22, v21
	v_div_fmas_f32 v19, v19, v20, v22
	v_div_fixup_f32 v18, v19, v18, 1.0
	v_pk_mul_f32 v[20:21], v[78:79], v[18:19] op_sel_hi:[1,0]
	v_pk_mul_f32 v[22:23], v[80:81], v[18:19] op_sel_hi:[1,0]
	s_nop 0
	v_pk_mul_f32 v[26:27], v[14:15], v[20:21]
	v_pk_mul_f32 v[28:29], v[16:17], v[22:23]
	v_pk_mul_f32 v[20:21], v[74:75], v[18:19] op_sel_hi:[1,0]
	v_pk_mul_f32 v[22:23], v[76:77], v[18:19] op_sel_hi:[1,0]
	v_pk_mul_f32 v[30:31], v[10:11], v[20:21]
	v_pk_mul_f32 v[32:33], v[12:13], v[22:23]
	v_pk_mul_f32 v[20:21], v[70:71], v[18:19] op_sel_hi:[1,0]
	v_pk_mul_f32 v[22:23], v[72:73], v[18:19] op_sel_hi:[1,0]
	v_pk_mul_f32 v[162:163], v[66:67], v[18:19] op_sel_hi:[1,0]
	v_pk_mul_f32 v[18:19], v[68:69], v[18:19] op_sel_hi:[1,0]
	v_pk_mul_f32 v[24:25], v[8:9], v[22:23]
	v_pk_mul_f32 v[22:23], v[6:7], v[20:21]
	v_pk_mul_f32 v[20:21], v[4:5], v[18:19]
	v_pk_mul_f32 v[18:19], v[2:3], v[162:163]

; __device__ __forceinline__ unsigned pk4_fp8(float a, float b, float c, float d) { unsigned w = 0u; w = __builtin_amdgcn_cvt_pk_fp8_f32(a, b, w, false); w = __builtin_amdgcn_cvt_pk_fp8_f32(c, d, w, true); return w; }
; template <bool F8OUT = false> __device__ __forceinline__ void head_tile_store(const f32x4 (&acc)[2][2][4][2], bf16_t* obase  , int opitch, const float* gain, float scale, const f32x2e* rope, int row0, int fq) {
;     ...
;             if (gain) {
;                 float ss = 0.f;
; #pragma unroll
;                 for (int bj = 0; bj < 2; ++bj)
; #pragma unroll
;                     for (int n = 0; n < 2; ++n) ss += (x[bj][n][0] * x[bj][n][0] + x[bj][n][1] * x[bj][n][1]) + (x[bj][n][2] * x[bj][n][2] + x[bj][n][3] * x[bj][n][3]);
;                 ss += __shfl_xor(ss, 16); ss += __shfl_xor(ss, 32);
;                 const float r = scale / sqrtf(ss * (1.f / 64.f) + 1e-6f);
; #pragma unroll
;                 for (int bj = 0; bj < 2; ++bj)
; #pragma unroll
;                     for (int n = 0; n < 2; ++n) x[bj][n] = x[bj][n] * r * g[bj][n];
;             }
;     ...
;             if constexpr (F8OUT) { unsigned char* rowp8 = (unsigned char*)obase + (size_t)row * opitch + 8 * fq; typedef unsigned u32x2_ __attribute__((ext_vector_type(2)));
; #pragma unroll
;                 for (int bj = 0; bj < 2; ++bj) *(u32x2_*)(rowp8 + 32 * bj) = (u32x2_){pk4_fp8(x[bj][0][0], x[bj][0][1], x[bj][0][2], x[bj][0][3]), pk4_fp8(x[bj][1][0], x[bj][1][1], x[bj][1][2], x[bj][1][3])};
;                 continue; }
.LBB0_189:
	v_mov_b32_e32 v164, v175
	v_cvt_pk_fp8_f32 v164, v26, v27
	v_mov_b32_e32 v26, v175
	v_mov_b32_e32 v27, v175
	v_cvt_pk_fp8_f32 v26, v22, v23
	v_cvt_pk_fp8_f32 v27, v18, v19
	v_mov_b32_e32 v165, v175
	v_cvt_pk_fp8_f32 v165, v30, v31
	v_cvt_pk_fp8_f32 v26, v24, v25 op_sel:[0,0,1]
	v_cvt_pk_fp8_f32 v27, v20, v21 op_sel:[0,0,1]
	v_ashrrev_i32_e32 v199, 31, v198
	v_lshlrev_b64 v[162:163], 7, v[198:199]
	v_cvt_pk_fp8_f32 v164, v28, v29 op_sel:[0,0,1]
	v_cvt_pk_fp8_f32 v165, v32, v33 op_sel:[0,0,1]
	v_lshl_add_u64 v[162:163], v[190:191], 0, v[162:163]
	global_store_dwordx2 v[162:163], v[26:27], off offset:32
	v_mov_b64_e32 v[18:19], v[50:51]
	v_mov_b64_e32 v[22:23], v[54:55]
	v_mov_b64_e32 v[30:31], v[58:59]
	v_mov_b64_e32 v[26:27], v[62:63]
	s_and_b64 vcc, exec, s[6:7]
	v_mov_b64_e32 v[20:21], v[52:53]
	v_mov_b64_e32 v[24:25], v[56:57]
	v_mov_b64_e32 v[32:33], v[60:61]
	v_mov_b64_e32 v[28:29], v[64:65]
	global_store_dwordx2 v[162:163], v[164:165], off
	s_cbranch_vccnz .LBB0_191
	v_pk_mul_f32 v[18:19], v[64:65], v[64:65]
	v_pk_mul_f32 v[20:21], v[62:63], v[62:63]
	s_nop 0
	v_pk_mov_b32 v[22:23], v[20:21], v[18:19] op_sel:[1,0]
	v_mov_b32_e32 v21, v19
	v_pk_add_f32 v[18:19], v[22:23], v[20:21]
	v_pk_mul_f32 v[20:21], v[60:61], v[60:61]
	v_pk_mul_f32 v[22:23], v[58:59], v[58:59]
	v_pk_add_f32 v[18:19], v[18:19], v[18:19] op_sel:[0,1] op_sel_hi:[1,0]
	v_pk_mov_b32 v[24:25], v[22:23], v[20:21] op_sel:[1,0]
	v_mov_b32_e32 v23, v21
	v_pk_add_f32 v[20:21], v[24:25], v[22:23]
	v_mul_f32_e32 v22, v50, v50
	v_mul_f32_e32 v23, v51, v51
	v_pk_add_f32 v[20:21], v[20:21], v[20:21] op_sel:[0,1] op_sel_hi:[1,0]
	v_mov_b32_e32 v19, v22
	v_mov_b32_e32 v21, v23
	v_pk_add_f32 v[18:19], v[18:19], v[20:21]
	v_mul_f32_e32 v20, v55, v55
	v_mul_f32_e32 v22, v57, v57
	v_mul_f32_e32 v24, v52, v52
	v_mul_f32_e32 v25, v53, v53
	v_pk_fma_f32 v[20:21], v[54:55], v[54:55], v[20:21] op_sel_hi:[1,1,0]
	v_pk_fma_f32 v[22:23], v[56:57], v[56:57], v[22:23] op_sel_hi:[1,1,0]
	v_mov_b32_e32 v21, v24
	v_mov_b32_e32 v23, v25
	v_pk_add_f32 v[20:21], v[20:21], v[22:23]
	s_nop 0
	v_pk_add_f32 v[18:19], v[18:19], v[20:21]
	v_and_b32_e32 v20, 64, v212
	v_add_f32_e32 v18, v18, v19
	v_xor_b32_e32 v19, 16, v212
	v_add_u32_e32 v20, 64, v20
	v_cmp_lt_i32_e32 vcc, v19, v20
	s_nop 1
	v_cndmask_b32_e32 v19, v212, v19, vcc
	v_lshlrev_b32_e32 v19, 2, v19
	ds_bpermute_b32 v19, v19, v18
	s_waitcnt lgkmcnt(0)
	v_add_f32_e32 v18, v18, v19
	v_xor_b32_e32 v19, 32, v212
	v_cmp_lt_i32_e32 vcc, v19, v20
	s_nop 1
	v_cndmask_b32_e32 v19, v212, v19, vcc
	v_lshlrev_b32_e32 v19, 2, v19
	ds_bpermute_b32 v19, v19, v18
	s_waitcnt lgkmcnt(0)
	v_add_f32_e32 v18, v18, v19
	v_fmamk_f32 v18, v18, 0x3c800000, v210
	v_mul_f32_e32 v19, 0x4f800000, v18
	v_cmp_gt_f32_e32 vcc, s28, v18
	s_nop 1
	v_cndmask_b32_e32 v18, v18, v19, vcc
	v_sqrt_f32_e32 v19, v18
	s_nop 0
	v_add_u32_e32 v20, -1, v19
	v_fma_f32 v21, -v20, v19, v18
	v_cmp_ge_f32_e64 s[10:11], 0, v21
	v_add_u32_e32 v21, 1, v19
	s_nop 0
	v_cndmask_b32_e64 v20, v19, v20, s[10:11]
	v_fma_f32 v19, -v21, v19, v18
	v_cmp_lt_f32_e64 s[10:11], 0, v19
	s_nop 1
	v_cndmask_b32_e64 v19, v20, v21, s[10:11]
	v_mul_f32_e32 v20, 0x37800000, v19
	v_cndmask_b32_e32 v19, v19, v20, vcc
	v_cmp_class_f32_e32 vcc, v18, v211
	s_nop 1
	v_cndmask_b32_e32 v18, v19, v18, vcc
	v_div_scale_f32 v19, s[0:1], v18, v18, 1.0
	v_rcp_f32_e32 v20, v19
	s_nop 0
	v_fma_f32 v21, -v19, v20, 1.0
	v_fmac_f32_e32 v20, v21, v20
	v_div_scale_f32 v21, vcc, 1.0, v18, 1.0
	v_mul_f32_e32 v22, v21, v20
	v_fma_f32 v23, -v19, v22, v21
	v_fmac_f32_e32 v22, v23, v20
	v_fma_f32 v19, -v19, v22, v21
	v_div_fmas_f32 v19, v19, v20, v22
	v_div_fixup_f32 v18, v19, v18, 1.0
	v_pk_mul_f32 v[20:21], v[62:63], v[18:19] op_sel_hi:[1,0]
	v_pk_mul_f32 v[22:23], v[64:65], v[18:19] op_sel_hi:[1,0]
	s_nop 0
	v_pk_mul_f32 v[26:27], v[14:15], v[20:21]
	v_pk_mul_f32 v[28:29], v[16:17], v[22:23]
	v_pk_mul_f32 v[20:21], v[58:59], v[18:19] op_sel_hi:[1,0]
	v_pk_mul_f32 v[22:23], v[60:61], v[18:19] op_sel_hi:[1,0]
	v_pk_mul_f32 v[30:31], v[10:11], v[20:21]
	v_pk_mul_f32 v[32:33], v[12:13], v[22:23]
	v_pk_mul_f32 v[20:21], v[54:55], v[18:19] op_sel_hi:[1,0]
	v_pk_mul_f32 v[22:23], v[56:57], v[18:19] op_sel_hi:[1,0]
	v_pk_mul_f32 v[162:163], v[50:51], v[18:19] op_sel_hi:[1,0]
	v_pk_mul_f32 v[18:19], v[52:53], v[18:19] op_sel_hi:[1,0]
	v_pk_mul_f32 v[24:25], v[8:9], v[22:23]
	v_pk_mul_f32 v[22:23], v[6:7], v[20:21]
	v_pk_mul_f32 v[20:21], v[4:5], v[18:19]
	v_pk_mul_f32 v[18:19], v[2:3], v[162:163]

; __device__ __forceinline__ unsigned pk4_fp8(float a, float b, float c, float d) { unsigned w = 0u; w = __builtin_amdgcn_cvt_pk_fp8_f32(a, b, w, false); w = __builtin_amdgcn_cvt_pk_fp8_f32(c, d, w, true); return w; }
; template <bool F8OUT = false> __device__ __forceinline__ void head_tile_store(const f32x4 (&acc)[2][2][4][2], bf16_t* obase  , int opitch, const float* gain, float scale, const f32x2e* rope, int row0, int fq) {
;     ...
;             if (gain) {
;                 float ss = 0.f;
; #pragma unroll
;                 for (int bj = 0; bj < 2; ++bj)
; #pragma unroll
;                     for (int n = 0; n < 2; ++n) ss += (x[bj][n][0] * x[bj][n][0] + x[bj][n][1] * x[bj][n][1]) + (x[bj][n][2] * x[bj][n][2] + x[bj][n][3] * x[bj][n][3]);
;                 ss += __shfl_xor(ss, 16); ss += __shfl_xor(ss, 32);
;                 const float r = scale / sqrtf(ss * (1.f / 64.f) + 1e-6f);
; #pragma unroll
;                 for (int bj = 0; bj < 2; ++bj)
; #pragma unroll
;                     for (int n = 0; n < 2; ++n) x[bj][n] = x[bj][n] * r * g[bj][n];
;             }
;     ...
;             if constexpr (F8OUT) { unsigned char* rowp8 = (unsigned char*)obase + (size_t)row * opitch + 8 * fq; typedef unsigned u32x2_ __attribute__((ext_vector_type(2)));
; #pragma unroll
;                 for (int bj = 0; bj < 2; ++bj) *(u32x2_*)(rowp8 + 32 * bj) = (u32x2_){pk4_fp8(x[bj][0][0], x[bj][0][1], x[bj][0][2], x[bj][0][3]), pk4_fp8(x[bj][1][0], x[bj][1][1], x[bj][1][2], x[bj][1][3])};
;                 continue; }
.LBB0_193:
	v_mov_b32_e32 v164, v175
	v_cvt_pk_fp8_f32 v164, v26, v27
	v_mov_b32_e32 v26, v175
	v_mov_b32_e32 v27, v175
	v_cvt_pk_fp8_f32 v26, v22, v23
	v_cvt_pk_fp8_f32 v27, v18, v19
	v_mov_b32_e32 v165, v175
	v_cvt_pk_fp8_f32 v165, v30, v31
	v_cvt_pk_fp8_f32 v26, v24, v25 op_sel:[0,0,1]
	v_cvt_pk_fp8_f32 v27, v20, v21 op_sel:[0,0,1]
	v_ashrrev_i32_e32 v193, 31, v192
	v_lshlrev_b64 v[162:163], 7, v[192:193]
	v_cvt_pk_fp8_f32 v164, v28, v29 op_sel:[0,0,1]
	v_cvt_pk_fp8_f32 v165, v32, v33 op_sel:[0,0,1]
	v_lshl_add_u64 v[162:163], v[190:191], 0, v[162:163]
	global_store_dwordx2 v[162:163], v[26:27], off offset:32
	v_mov_b64_e32 v[18:19], v[34:35]
	v_mov_b64_e32 v[22:23], v[38:39]
	v_mov_b64_e32 v[30:31], v[42:43]
	v_mov_b64_e32 v[26:27], v[46:47]
	s_and_b64 vcc, exec, s[6:7]
	v_mov_b64_e32 v[20:21], v[36:37]
	v_mov_b64_e32 v[24:25], v[40:41]
	v_mov_b64_e32 v[32:33], v[44:45]
	v_mov_b64_e32 v[28:29], v[48:49]
	global_store_dwordx2 v[162:163], v[164:165], off
	s_cbranch_vccnz .LBB0_195
	v_pk_mul_f32 v[18:19], v[48:49], v[48:49]
	v_pk_mul_f32 v[20:21], v[46:47], v[46:47]
	s_nop 0
	v_pk_mov_b32 v[22:23], v[20:21], v[18:19] op_sel:[1,0]
	v_mov_b32_e32 v21, v19
	v_pk_add_f32 v[18:19], v[22:23], v[20:21]
	v_pk_mul_f32 v[20:21], v[44:45], v[44:45]
	v_pk_mul_f32 v[22:23], v[42:43], v[42:43]
	v_pk_add_f32 v[18:19], v[18:19], v[18:19] op_sel:[0,1] op_sel_hi:[1,0]
	v_pk_mov_b32 v[24:25], v[22:23], v[20:21] op_sel:[1,0]
	v_mov_b32_e32 v23, v21
	v_pk_add_f32 v[20:21], v[24:25], v[22:23]
	v_mul_f32_e32 v22, v34, v34
	v_mul_f32_e32 v23, v35, v35
	v_pk_add_f32 v[20:21], v[20:21], v[20:21] op_sel:[0,1] op_sel_hi:[1,0]
	v_mov_b32_e32 v19, v22
	v_mov_b32_e32 v21, v23
	v_pk_add_f32 v[18:19], v[18:19], v[20:21]
	v_mul_f32_e32 v20, v39, v39
	v_mul_f32_e32 v22, v41, v41
	v_mul_f32_e32 v24, v36, v36
	v_mul_f32_e32 v25, v37, v37
	v_pk_fma_f32 v[20:21], v[38:39], v[38:39], v[20:21] op_sel_hi:[1,1,0]
	v_pk_fma_f32 v[22:23], v[40:41], v[40:41], v[22:23] op_sel_hi:[1,1,0]
	v_mov_b32_e32 v21, v24
	v_mov_b32_e32 v23, v25
	v_pk_add_f32 v[20:21], v[20:21], v[22:23]
	s_nop 0
	v_pk_add_f32 v[18:19], v[18:19], v[20:21]
	v_and_b32_e32 v20, 64, v212
	v_add_f32_e32 v18, v18, v19
	v_xor_b32_e32 v19, 16, v212
	v_add_u32_e32 v20, 64, v20
	v_cmp_lt_i32_e32 vcc, v19, v20
	s_nop 1
	v_cndmask_b32_e32 v19, v212, v19, vcc
	v_lshlrev_b32_e32 v19, 2, v19
	ds_bpermute_b32 v19, v19, v18
	s_waitcnt lgkmcnt(0)
	v_add_f32_e32 v18, v18, v19
	v_xor_b32_e32 v19, 32, v212
	v_cmp_lt_i32_e32 vcc, v19, v20
	s_nop 1
	v_cndmask_b32_e32 v19, v212, v19, vcc
	v_lshlrev_b32_e32 v19, 2, v19
	ds_bpermute_b32 v19, v19, v18
	s_waitcnt lgkmcnt(0)
	v_add_f32_e32 v18, v18, v19
	v_fmamk_f32 v18, v18, 0x3c800000, v210
	v_mul_f32_e32 v19, 0x4f800000, v18
	v_cmp_gt_f32_e32 vcc, s28, v18
	s_nop 1
	v_cndmask_b32_e32 v18, v18, v19, vcc
	v_sqrt_f32_e32 v19, v18
	s_nop 0
	v_add_u32_e32 v20, -1, v19
	v_fma_f32 v21, -v20, v19, v18
	v_cmp_ge_f32_e64 s[6:7], 0, v21
	v_add_u32_e32 v21, 1, v19
	s_nop 0
	v_cndmask_b32_e64 v20, v19, v20, s[6:7]
	v_fma_f32 v19, -v21, v19, v18
	v_cmp_lt_f32_e64 s[6:7], 0, v19
	s_nop 1
	v_cndmask_b32_e64 v19, v20, v21, s[6:7]
	v_mul_f32_e32 v20, 0x37800000, v19
	v_cndmask_b32_e32 v19, v19, v20, vcc
	v_cmp_class_f32_e32 vcc, v18, v211
	s_nop 1
	v_cndmask_b32_e32 v18, v19, v18, vcc
	v_div_scale_f32 v19, s[0:1], v18, v18, 1.0
	v_rcp_f32_e32 v20, v19
	s_nop 0
	v_fma_f32 v21, -v19, v20, 1.0
	v_fmac_f32_e32 v20, v21, v20
	v_div_scale_f32 v21, vcc, 1.0, v18, 1.0
	v_mul_f32_e32 v22, v21, v20
	v_fma_f32 v23, -v19, v22, v21
	v_fmac_f32_e32 v22, v23, v20
	v_fma_f32 v19, -v19, v22, v21
	v_div_fmas_f32 v19, v19, v20, v22
	v_div_fixup_f32 v18, v19, v18, 1.0
	v_pk_mul_f32 v[20:21], v[46:47], v[18:19] op_sel_hi:[1,0]
	v_pk_mul_f32 v[22:23], v[48:49], v[18:19] op_sel_hi:[1,0]
	s_nop 0
	v_pk_mul_f32 v[26:27], v[14:15], v[20:21]
	v_pk_mul_f32 v[28:29], v[16:17], v[22:23]
	v_pk_mul_f32 v[14:15], v[42:43], v[18:19] op_sel_hi:[1,0]
	v_pk_mul_f32 v[16:17], v[44:45], v[18:19] op_sel_hi:[1,0]
	v_pk_mul_f32 v[30:31], v[10:11], v[14:15]
	v_pk_mul_f32 v[32:33], v[12:13], v[16:17]
	v_pk_mul_f32 v[10:11], v[38:39], v[18:19] op_sel_hi:[1,0]
	v_pk_mul_f32 v[12:13], v[40:41], v[18:19] op_sel_hi:[1,0]
	v_pk_mul_f32 v[22:23], v[6:7], v[10:11]
	v_pk_mul_f32 v[24:25], v[8:9], v[12:13]
	v_pk_mul_f32 v[6:7], v[34:35], v[18:19] op_sel_hi:[1,0]
	v_pk_mul_f32 v[8:9], v[36:37], v[18:19] op_sel_hi:[1,0]
	v_pk_mul_f32 v[18:19], v[2:3], v[6:7]
	v_pk_mul_f32 v[20:21], v[4:5], v[8:9]
; template <bool F8OUT = false> __device__ __forceinline__ void head_tile_store(const f32x4 (&acc)[2][2][4][2], bf16_t* obase  , int opitch, const float* gain, float scale, const f32x2e* rope, int row0, int fq) {
;     ...
;             if (rope) {
;                 const int t = row & 8191; const bool second = (fq & 2) != 0;
; #pragma unroll
;                 for (int bj = 0; bj < 2; ++bj) { const int pos = bj ? (t & 63) : (t >> 6); const f32x2e* tb = rope + pos * 16 + 8 * (fq & 1);
; #pragma unroll
;                     for (int n = 0; n < 2; ++n)
; #pragma unroll
;                         for (int e = 0; e < 4; ++e) { const float p = __shfl_xor(x[bj][n][e], 32); const f32x2e cs = tb[4 * n + e]; const float v = x[bj][n][e];
;                             x[bj][n][e] = second ? (p * cs.y + v * cs.x) : (v * cs.x - p * cs.y); } }
;             }
.LBB0_195:
	s_and_b64 vcc, exec, s[8:9]
	s_nop 0
	v_add_u32_e32 v6, 0xb0, v188
	s_cbranch_vccnz .LBB0_197
	v_and_b32_e32 v3, 64, v212
	v_xor_b32_e32 v2, 32, v212
	v_add_u32_e32 v3, 64, v3
	v_cmp_lt_i32_e32 vcc, v2, v3
	v_mov_b32_e32 v197, v175
	s_nop 0
	v_cndmask_b32_e32 v2, v212, v2, vcc
	v_lshlrev_b32_e32 v7, 2, v2
	v_lshlrev_b32_e32 v2, 1, v6
	v_and_b32_e32 v174, 0x3f80, v2
	v_lshl_add_u64 v[16:17], v[186:187], 0, v[174:175]
	v_add_u32_e32 v238, s100, v16
	ds_read_b128 v[2:5], v238 offset:48
	ds_read_b128 v[8:11], v238 offset:32
	ds_read_b128 v[12:15], v238 offset:16
	ds_read_b128 v[162:165], v238
	ds_bpermute_b32 v188, v7, v26
	ds_bpermute_b32 v189, v7, v27
	s_waitcnt lgkmcnt(0)
	v_mov_b32_e32 v16, v163
	v_mov_b32_e32 v17, v165
	s_waitcnt lgkmcnt(0)
	v_pk_mul_f32 v[16:17], v[16:17], v[188:189]
	v_mov_b32_e32 v163, v164
	v_cndmask_b32_e64 v17, v17, -v17, s[4:5]
	v_cndmask_b32_e64 v16, v16, -v16, s[4:5]
	v_pk_fma_f32 v[26:27], v[26:27], v[162:163], v[16:17]
	ds_bpermute_b32 v16, v7, v28
	ds_bpermute_b32 v17, v7, v29
	v_mov_b32_e32 v162, v13
	v_mov_b32_e32 v163, v15
	v_mov_b32_e32 v13, v14
	s_waitcnt lgkmcnt(0)
	v_pk_mul_f32 v[16:17], v[162:163], v[16:17]
	s_nop 0
	v_cndmask_b32_e64 v15, v17, -v17, s[4:5]
	v_cndmask_b32_e64 v14, v16, -v16, s[4:5]
	v_pk_fma_f32 v[28:29], v[28:29], v[12:13], v[14:15]
	ds_bpermute_b32 v12, v7, v30
	ds_bpermute_b32 v13, v7, v31
	v_mov_b32_e32 v14, v9
	v_mov_b32_e32 v15, v11
	v_mov_b32_e32 v9, v10
	v_lshl_add_u64 v[16:17], v[186:187], 0, v[196:197]
	s_waitcnt lgkmcnt(0)
	v_pk_mul_f32 v[12:13], v[14:15], v[12:13]
	ds_bpermute_b32 v186, v7, v22
	v_cndmask_b32_e64 v11, v13, -v13, s[4:5]
	v_cndmask_b32_e64 v10, v12, -v12, s[4:5]
	v_pk_fma_f32 v[30:31], v[30:31], v[8:9], v[10:11]
	ds_bpermute_b32 v8, v7, v32
	ds_bpermute_b32 v9, v7, v33
	v_mov_b32_e32 v10, v3
	v_mov_b32_e32 v11, v5
	v_mov_b32_e32 v3, v4
	ds_bpermute_b32 v187, v7, v23
	s_waitcnt lgkmcnt(1)
	v_pk_mul_f32 v[8:9], v[10:11], v[8:9]
	s_nop 0
	v_cndmask_b32_e64 v5, v9, -v9, s[4:5]
	v_cndmask_b32_e64 v4, v8, -v8, s[4:5]
	v_pk_fma_f32 v[32:33], v[32:33], v[2:3], v[4:5]
	v_add_u32_e32 v238, s100, v16
	ds_read_b128 v[2:5], v238 offset:48
	ds_read_b128 v[8:11], v238 offset:32
	ds_read_b128 v[12:15], v238 offset:16
	ds_read_b128 v[162:165], v238
	s_waitcnt lgkmcnt(0)
	v_mov_b32_e32 v16, v163
	v_mov_b32_e32 v17, v165
	s_waitcnt lgkmcnt(0)
	v_pk_mul_f32 v[16:17], v[16:17], v[186:187]
	v_mov_b32_e32 v163, v164
	v_cndmask_b32_e64 v17, v17, -v17, s[4:5]
	v_cndmask_b32_e64 v16, v16, -v16, s[4:5]
	v_pk_fma_f32 v[22:23], v[22:23], v[162:163], v[16:17]
	ds_bpermute_b32 v16, v7, v24
	ds_bpermute_b32 v17, v7, v25
	v_mov_b32_e32 v162, v13
	v_mov_b32_e32 v163, v15
	v_mov_b32_e32 v13, v14
	s_waitcnt lgkmcnt(0)
	v_pk_mul_f32 v[16:17], v[162:163], v[16:17]
	s_nop 0
	v_cndmask_b32_e64 v15, v17, -v17, s[4:5]
	v_cndmask_b32_e64 v14, v16, -v16, s[4:5]
	v_pk_fma_f32 v[24:25], v[24:25], v[12:13], v[14:15]
	ds_bpermute_b32 v12, v7, v18
	ds_bpermute_b32 v13, v7, v19
	v_mov_b32_e32 v14, v9
	v_mov_b32_e32 v15, v11
	v_mov_b32_e32 v9, v10
	s_waitcnt lgkmcnt(0)
	v_pk_mul_f32 v[12:13], v[14:15], v[12:13]
	s_nop 0
	v_cndmask_b32_e64 v11, v13, -v13, s[4:5]
	v_cndmask_b32_e64 v10, v12, -v12, s[4:5]
	v_pk_fma_f32 v[18:19], v[18:19], v[8:9], v[10:11]
	ds_bpermute_b32 v8, v7, v20
	ds_bpermute_b32 v9, v7, v21
	v_mov_b32_e32 v10, v3
	v_mov_b32_e32 v11, v5
	v_mov_b32_e32 v3, v4
	s_waitcnt lgkmcnt(0)
	v_pk_mul_f32 v[8:9], v[10:11], v[8:9]
	s_nop 0
	v_cndmask_b32_e64 v5, v9, -v9, s[4:5]
	v_cndmask_b32_e64 v4, v8, -v8, s[4:5]
	v_pk_fma_f32 v[20:21], v[20:21], v[2:3], v[4:5]

; __device__ __forceinline__ unsigned pk4_fp8(float a, float b, float c, float d) { unsigned w = 0u; w = __builtin_amdgcn_cvt_pk_fp8_f32(a, b, w, false); w = __builtin_amdgcn_cvt_pk_fp8_f32(c, d, w, true); return w; }
; template <bool F8OUT = false> __device__ __forceinline__ void head_tile_store(const f32x4 (&acc)[2][2][4][2], bf16_t* obase  , int opitch, const float* gain, float scale, const f32x2e* rope, int row0, int fq) {
;     ...
;             if (gain) {
;                 float ss = 0.f;
; #pragma unroll
;                 for (int bj = 0; bj < 2; ++bj)
; #pragma unroll
;                     for (int n = 0; n < 2; ++n) ss += (x[bj][n][0] * x[bj][n][0] + x[bj][n][1] * x[bj][n][1]) + (x[bj][n][2] * x[bj][n][2] + x[bj][n][3] * x[bj][n][3]);
;                 ss += __shfl_xor(ss, 16); ss += __shfl_xor(ss, 32);
;                 const float r = scale / sqrtf(ss * (1.f / 64.f) + 1e-6f);
; #pragma unroll
;                 for (int bj = 0; bj < 2; ++bj)
; #pragma unroll
;                     for (int n = 0; n < 2; ++n) x[bj][n] = x[bj][n] * r * g[bj][n];
;             }
;     ...
;             if constexpr (F8OUT) { unsigned char* rowp8 = (unsigned char*)obase + (size_t)row * opitch + 8 * fq; typedef unsigned u32x2_ __attribute__((ext_vector_type(2)));
; #pragma unroll
;                 for (int bj = 0; bj < 2; ++bj) *(u32x2_*)(rowp8 + 32 * bj) = (u32x2_){pk4_fp8(x[bj][0][0], x[bj][0][1], x[bj][0][2], x[bj][0][3]), pk4_fp8(x[bj][1][0], x[bj][1][1], x[bj][1][2], x[bj][1][3])};
;                 continue; }
.LBB0_206:
	v_mov_b32_e32 v162, v175
	v_mov_b32_e32 v163, v175
	v_cvt_pk_fp8_f32 v162, v18, v19
	v_cvt_pk_fp8_f32 v163, v22, v23
	v_mov_b32_e32 v18, v175
	v_mov_b32_e32 v19, v175
	v_cvt_pk_fp8_f32 v18, v26, v27
	v_cvt_pk_fp8_f32 v19, v30, v31
	s_lshl_b32 s0, s18, 6
	s_add_u32 s0, s70, s0
	v_cvt_pk_fp8_f32 v162, v20, v21 op_sel:[0,0,1]
	v_cvt_pk_fp8_f32 v163, v24, v25 op_sel:[0,0,1]
	s_addc_u32 s1, s71, 0
	v_ashrrev_i32_e32 v189, 31, v188
	v_cvt_pk_fp8_f32 v18, v28, v29 op_sel:[0,0,1]
	v_cvt_pk_fp8_f32 v19, v32, v33 op_sel:[0,0,1]
	v_lshl_add_u64 v[190:191], s[0:1], 0, v[190:191]
	v_lshlrev_b64 v[20:21], 9, v[188:189]
	v_lshl_add_u64 v[20:21], v[190:191], 0, v[20:21]
	global_store_dwordx2 v[20:21], v[162:163], off
	global_store_dwordx2 v[20:21], v[18:19], off offset:32
	v_mov_b64_e32 v[18:19], v[130:131]
	v_mov_b64_e32 v[22:23], v[134:135]
	v_mov_b64_e32 v[30:31], v[138:139]
	v_mov_b64_e32 v[26:27], v[142:143]
	s_and_b64 vcc, exec, s[6:7]
	v_mov_b64_e32 v[20:21], v[132:133]
	v_mov_b64_e32 v[24:25], v[136:137]
	v_mov_b64_e32 v[32:33], v[140:141]
	v_mov_b64_e32 v[28:29], v[144:145]
	s_cbranch_vccnz .LBB0_208
	v_pk_mul_f32 v[18:19], v[144:145], v[144:145]
	v_pk_mul_f32 v[20:21], v[142:143], v[142:143]
	s_nop 0
	v_pk_mov_b32 v[22:23], v[20:21], v[18:19] op_sel:[1,0]
	v_mov_b32_e32 v21, v19
	v_pk_add_f32 v[18:19], v[22:23], v[20:21]
	v_pk_mul_f32 v[20:21], v[140:141], v[140:141]
	v_pk_mul_f32 v[22:23], v[138:139], v[138:139]
	v_pk_add_f32 v[18:19], v[18:19], v[18:19] op_sel:[0,1] op_sel_hi:[1,0]
	v_pk_mov_b32 v[24:25], v[22:23], v[20:21] op_sel:[1,0]
	v_mov_b32_e32 v23, v21
	v_pk_add_f32 v[20:21], v[24:25], v[22:23]
	v_mul_f32_e32 v22, v130, v130
	v_mul_f32_e32 v23, v131, v131
	v_pk_add_f32 v[20:21], v[20:21], v[20:21] op_sel:[0,1] op_sel_hi:[1,0]
	v_mov_b32_e32 v19, v22
	v_mov_b32_e32 v21, v23
	v_pk_add_f32 v[18:19], v[18:19], v[20:21]
	v_mul_f32_e32 v20, v135, v135
	v_mul_f32_e32 v22, v137, v137
	v_mul_f32_e32 v24, v132, v132
	v_mul_f32_e32 v25, v133, v133
	v_pk_fma_f32 v[20:21], v[134:135], v[134:135], v[20:21] op_sel_hi:[1,1,0]
	v_pk_fma_f32 v[22:23], v[136:137], v[136:137], v[22:23] op_sel_hi:[1,1,0]
	v_mov_b32_e32 v21, v24
	v_mov_b32_e32 v23, v25
	v_pk_add_f32 v[20:21], v[20:21], v[22:23]
	s_nop 0
	v_pk_add_f32 v[18:19], v[18:19], v[20:21]
	v_and_b32_e32 v20, 64, v212
	v_add_f32_e32 v18, v18, v19
	v_xor_b32_e32 v19, 16, v212
	v_add_u32_e32 v20, 64, v20
	v_cmp_lt_i32_e32 vcc, v19, v20
	s_nop 1
	v_cndmask_b32_e32 v19, v212, v19, vcc
	v_lshlrev_b32_e32 v19, 2, v19
	ds_bpermute_b32 v19, v19, v18
	s_waitcnt lgkmcnt(0)
	v_add_f32_e32 v18, v18, v19
	v_xor_b32_e32 v19, 32, v212
	v_cmp_lt_i32_e32 vcc, v19, v20
	s_nop 1
	v_cndmask_b32_e32 v19, v212, v19, vcc
	v_lshlrev_b32_e32 v19, 2, v19
	ds_bpermute_b32 v19, v19, v18
	s_waitcnt lgkmcnt(0)
	v_add_f32_e32 v18, v18, v19
	v_fmamk_f32 v18, v18, 0x3c800000, v210
	v_mul_f32_e32 v19, 0x4f800000, v18
	v_cmp_gt_f32_e32 vcc, s28, v18
	s_nop 1
	v_cndmask_b32_e32 v18, v18, v19, vcc
	v_sqrt_f32_e32 v19, v18
	s_nop 0
	v_add_u32_e32 v20, -1, v19
	v_fma_f32 v21, -v20, v19, v18
	v_cmp_ge_f32_e64 s[10:11], 0, v21
	v_add_u32_e32 v21, 1, v19
	s_nop 0
	v_cndmask_b32_e64 v20, v19, v20, s[10:11]
	v_fma_f32 v19, -v21, v19, v18
	v_cmp_lt_f32_e64 s[10:11], 0, v19
	s_nop 1
	v_cndmask_b32_e64 v19, v20, v21, s[10:11]
	v_mul_f32_e32 v20, 0x37800000, v19
	v_cndmask_b32_e32 v19, v19, v20, vcc
	v_cmp_class_f32_e32 vcc, v18, v211
	s_nop 1
	v_cndmask_b32_e32 v18, v19, v18, vcc
	v_div_scale_f32 v19, s[0:1], v18, v18, s29
	v_rcp_f32_e32 v20, v19
	s_nop 0
	v_fma_f32 v21, -v19, v20, 1.0
	v_fmac_f32_e32 v20, v21, v20
	v_div_scale_f32 v21, vcc, s29, v18, s29
	v_mul_f32_e32 v22, v21, v20
	v_fma_f32 v23, -v19, v22, v21
	v_fmac_f32_e32 v22, v23, v20
	v_fma_f32 v19, -v19, v22, v21
	v_div_fmas_f32 v19, v19, v20, v22
	v_div_fixup_f32 v18, v19, v18, s29
	v_pk_mul_f32 v[20:21], v[142:143], v[18:19] op_sel_hi:[1,0]
	v_pk_mul_f32 v[22:23], v[144:145], v[18:19] op_sel_hi:[1,0]
	s_nop 0
	v_pk_mul_f32 v[26:27], v[14:15], v[20:21]
	v_pk_mul_f32 v[28:29], v[16:17], v[22:23]
	v_pk_mul_f32 v[20:21], v[138:139], v[18:19] op_sel_hi:[1,0]
	v_pk_mul_f32 v[22:23], v[140:141], v[18:19] op_sel_hi:[1,0]
	v_pk_mul_f32 v[30:31], v[10:11], v[20:21]
	v_pk_mul_f32 v[32:33], v[12:13], v[22:23]
	v_pk_mul_f32 v[20:21], v[134:135], v[18:19] op_sel_hi:[1,0]
	v_pk_mul_f32 v[22:23], v[136:137], v[18:19] op_sel_hi:[1,0]
	v_pk_mul_f32 v[162:163], v[130:131], v[18:19] op_sel_hi:[1,0]
	v_pk_mul_f32 v[18:19], v[132:133], v[18:19] op_sel_hi:[1,0]
	v_pk_mul_f32 v[24:25], v[8:9], v[22:23]
	v_pk_mul_f32 v[22:23], v[6:7], v[20:21]
	v_pk_mul_f32 v[20:21], v[4:5], v[18:19]
	v_pk_mul_f32 v[18:19], v[2:3], v[162:163]

; __device__ __forceinline__ unsigned pk4_fp8(float a, float b, float c, float d) { unsigned w = 0u; w = __builtin_amdgcn_cvt_pk_fp8_f32(a, b, w, false); w = __builtin_amdgcn_cvt_pk_fp8_f32(c, d, w, true); return w; }
; template <bool F8OUT = false> __device__ __forceinline__ void head_tile_store(const f32x4 (&acc)[2][2][4][2], bf16_t* obase  , int opitch, const float* gain, float scale, const f32x2e* rope, int row0, int fq) {
;     ...
;             if (gain) {
;                 float ss = 0.f;
; #pragma unroll
;                 for (int bj = 0; bj < 2; ++bj)
; #pragma unroll
;                     for (int n = 0; n < 2; ++n) ss += (x[bj][n][0] * x[bj][n][0] + x[bj][n][1] * x[bj][n][1]) + (x[bj][n][2] * x[bj][n][2] + x[bj][n][3] * x[bj][n][3]);
;                 ss += __shfl_xor(ss, 16); ss += __shfl_xor(ss, 32);
;                 const float r = scale / sqrtf(ss * (1.f / 64.f) + 1e-6f);
; #pragma unroll
;                 for (int bj = 0; bj < 2; ++bj)
; #pragma unroll
;                     for (int n = 0; n < 2; ++n) x[bj][n] = x[bj][n] * r * g[bj][n];
;             }
;     ...
;             if constexpr (F8OUT) { unsigned char* rowp8 = (unsigned char*)obase + (size_t)row * opitch + 8 * fq; typedef unsigned u32x2_ __attribute__((ext_vector_type(2)));
; #pragma unroll
;                 for (int bj = 0; bj < 2; ++bj) *(u32x2_*)(rowp8 + 32 * bj) = (u32x2_){pk4_fp8(x[bj][0][0], x[bj][0][1], x[bj][0][2], x[bj][0][3]), pk4_fp8(x[bj][1][0], x[bj][1][1], x[bj][1][2], x[bj][1][3])};
;                 continue; }
.LBB0_210:
	v_mov_b32_e32 v164, v175
	v_cvt_pk_fp8_f32 v164, v26, v27
	v_mov_b32_e32 v26, v175
	v_mov_b32_e32 v27, v175
	v_cvt_pk_fp8_f32 v26, v22, v23
	v_cvt_pk_fp8_f32 v27, v18, v19
	v_mov_b32_e32 v165, v175
	v_cvt_pk_fp8_f32 v165, v30, v31
	v_cvt_pk_fp8_f32 v26, v24, v25 op_sel:[0,0,1]
	v_cvt_pk_fp8_f32 v27, v20, v21 op_sel:[0,0,1]
	v_ashrrev_i32_e32 v195, 31, v194
	v_lshlrev_b64 v[162:163], 9, v[194:195]
	v_cvt_pk_fp8_f32 v164, v28, v29 op_sel:[0,0,1]
	v_cvt_pk_fp8_f32 v165, v32, v33 op_sel:[0,0,1]
	v_lshl_add_u64 v[162:163], v[190:191], 0, v[162:163]
	global_store_dwordx2 v[162:163], v[26:27], off offset:32
	v_mov_b64_e32 v[18:19], v[114:115]
	v_mov_b64_e32 v[22:23], v[118:119]
	v_mov_b64_e32 v[30:31], v[122:123]
	v_mov_b64_e32 v[26:27], v[126:127]
	s_and_b64 vcc, exec, s[6:7]
	v_mov_b64_e32 v[20:21], v[116:117]
	v_mov_b64_e32 v[24:25], v[120:121]
	v_mov_b64_e32 v[32:33], v[124:125]
	v_mov_b64_e32 v[28:29], v[128:129]
	global_store_dwordx2 v[162:163], v[164:165], off
	s_cbranch_vccnz .LBB0_212
	v_pk_mul_f32 v[18:19], v[128:129], v[128:129]
	v_pk_mul_f32 v[20:21], v[126:127], v[126:127]
	s_nop 0
	v_pk_mov_b32 v[22:23], v[20:21], v[18:19] op_sel:[1,0]
	v_mov_b32_e32 v21, v19
	v_pk_add_f32 v[18:19], v[22:23], v[20:21]
	v_pk_mul_f32 v[20:21], v[124:125], v[124:125]
	v_pk_mul_f32 v[22:23], v[122:123], v[122:123]
	v_pk_add_f32 v[18:19], v[18:19], v[18:19] op_sel:[0,1] op_sel_hi:[1,0]
	v_pk_mov_b32 v[24:25], v[22:23], v[20:21] op_sel:[1,0]
	v_mov_b32_e32 v23, v21
	v_pk_add_f32 v[20:21], v[24:25], v[22:23]
	v_mul_f32_e32 v22, v114, v114
	v_mul_f32_e32 v23, v115, v115
	v_pk_add_f32 v[20:21], v[20:21], v[20:21] op_sel:[0,1] op_sel_hi:[1,0]
	v_mov_b32_e32 v19, v22
	v_mov_b32_e32 v21, v23
	v_pk_add_f32 v[18:19], v[18:19], v[20:21]
	v_mul_f32_e32 v20, v119, v119
	v_mul_f32_e32 v22, v121, v121
	v_mul_f32_e32 v24, v116, v116
	v_mul_f32_e32 v25, v117, v117
	v_pk_fma_f32 v[20:21], v[118:119], v[118:119], v[20:21] op_sel_hi:[1,1,0]
	v_pk_fma_f32 v[22:23], v[120:121], v[120:121], v[22:23] op_sel_hi:[1,1,0]
	v_mov_b32_e32 v21, v24
	v_mov_b32_e32 v23, v25
	v_pk_add_f32 v[20:21], v[20:21], v[22:23]
	s_nop 0
	v_pk_add_f32 v[18:19], v[18:19], v[20:21]
	v_and_b32_e32 v20, 64, v212
	v_add_f32_e32 v18, v18, v19
	v_xor_b32_e32 v19, 16, v212
	v_add_u32_e32 v20, 64, v20
	v_cmp_lt_i32_e32 vcc, v19, v20
	s_nop 1
	v_cndmask_b32_e32 v19, v212, v19, vcc
	v_lshlrev_b32_e32 v19, 2, v19
	ds_bpermute_b32 v19, v19, v18
	s_waitcnt lgkmcnt(0)
	v_add_f32_e32 v18, v18, v19
	v_xor_b32_e32 v19, 32, v212
	v_cmp_lt_i32_e32 vcc, v19, v20
	s_nop 1
	v_cndmask_b32_e32 v19, v212, v19, vcc
	v_lshlrev_b32_e32 v19, 2, v19
	ds_bpermute_b32 v19, v19, v18
	s_waitcnt lgkmcnt(0)
	v_add_f32_e32 v18, v18, v19
	v_fmamk_f32 v18, v18, 0x3c800000, v210
	v_mul_f32_e32 v19, 0x4f800000, v18
	v_cmp_gt_f32_e32 vcc, s28, v18
	s_nop 1
	v_cndmask_b32_e32 v18, v18, v19, vcc
	v_sqrt_f32_e32 v19, v18
	s_nop 0
	v_add_u32_e32 v20, -1, v19
	v_fma_f32 v21, -v20, v19, v18
	v_cmp_ge_f32_e64 s[10:11], 0, v21
	v_add_u32_e32 v21, 1, v19
	s_nop 0
	v_cndmask_b32_e64 v20, v19, v20, s[10:11]
	v_fma_f32 v19, -v21, v19, v18
	v_cmp_lt_f32_e64 s[10:11], 0, v19
	s_nop 1
	v_cndmask_b32_e64 v19, v20, v21, s[10:11]
	v_mul_f32_e32 v20, 0x37800000, v19
	v_cndmask_b32_e32 v19, v19, v20, vcc
	v_cmp_class_f32_e32 vcc, v18, v211
	s_nop 1
	v_cndmask_b32_e32 v18, v19, v18, vcc
	v_div_scale_f32 v19, s[0:1], v18, v18, s29
	v_rcp_f32_e32 v20, v19
	s_nop 0
	v_fma_f32 v21, -v19, v20, 1.0
	v_fmac_f32_e32 v20, v21, v20
	v_div_scale_f32 v21, vcc, s29, v18, s29
	v_mul_f32_e32 v22, v21, v20
	v_fma_f32 v23, -v19, v22, v21
	v_fmac_f32_e32 v22, v23, v20
	v_fma_f32 v19, -v19, v22, v21
	v_div_fmas_f32 v19, v19, v20, v22
	v_div_fixup_f32 v18, v19, v18, s29
	v_pk_mul_f32 v[20:21], v[126:127], v[18:19] op_sel_hi:[1,0]
	v_pk_mul_f32 v[22:23], v[128:129], v[18:19] op_sel_hi:[1,0]
	s_nop 0
	v_pk_mul_f32 v[26:27], v[14:15], v[20:21]
	v_pk_mul_f32 v[28:29], v[16:17], v[22:23]
	v_pk_mul_f32 v[20:21], v[122:123], v[18:19] op_sel_hi:[1,0]
	v_pk_mul_f32 v[22:23], v[124:125], v[18:19] op_sel_hi:[1,0]
	v_pk_mul_f32 v[30:31], v[10:11], v[20:21]
	v_pk_mul_f32 v[32:33], v[12:13], v[22:23]
	v_pk_mul_f32 v[20:21], v[118:119], v[18:19] op_sel_hi:[1,0]
	v_pk_mul_f32 v[22:23], v[120:121], v[18:19] op_sel_hi:[1,0]
	v_pk_mul_f32 v[162:163], v[114:115], v[18:19] op_sel_hi:[1,0]
	v_pk_mul_f32 v[18:19], v[116:117], v[18:19] op_sel_hi:[1,0]
	v_pk_mul_f32 v[24:25], v[8:9], v[22:23]
	v_pk_mul_f32 v[22:23], v[6:7], v[20:21]
	v_pk_mul_f32 v[20:21], v[4:5], v[18:19]
	v_pk_mul_f32 v[18:19], v[2:3], v[162:163]

; __device__ __forceinline__ unsigned pk4_fp8(float a, float b, float c, float d) { unsigned w = 0u; w = __builtin_amdgcn_cvt_pk_fp8_f32(a, b, w, false); w = __builtin_amdgcn_cvt_pk_fp8_f32(c, d, w, true); return w; }
; template <bool F8OUT = false> __device__ __forceinline__ void head_tile_store(const f32x4 (&acc)[2][2][4][2], bf16_t* obase  , int opitch, const float* gain, float scale, const f32x2e* rope, int row0, int fq) {
;     ...
;             if (gain) {
;                 float ss = 0.f;
; #pragma unroll
;                 for (int bj = 0; bj < 2; ++bj)
; #pragma unroll
;                     for (int n = 0; n < 2; ++n) ss += (x[bj][n][0] * x[bj][n][0] + x[bj][n][1] * x[bj][n][1]) + (x[bj][n][2] * x[bj][n][2] + x[bj][n][3] * x[bj][n][3]);
;                 ss += __shfl_xor(ss, 16); ss += __shfl_xor(ss, 32);
;                 const float r = scale / sqrtf(ss * (1.f / 64.f) + 1e-6f);
; #pragma unroll
;                 for (int bj = 0; bj < 2; ++bj)
; #pragma unroll
;                     for (int n = 0; n < 2; ++n) x[bj][n] = x[bj][n] * r * g[bj][n];
;             }
;     ...
;             if constexpr (F8OUT) { unsigned char* rowp8 = (unsigned char*)obase + (size_t)row * opitch + 8 * fq; typedef unsigned u32x2_ __attribute__((ext_vector_type(2)));
; #pragma unroll
;                 for (int bj = 0; bj < 2; ++bj) *(u32x2_*)(rowp8 + 32 * bj) = (u32x2_){pk4_fp8(x[bj][0][0], x[bj][0][1], x[bj][0][2], x[bj][0][3]), pk4_fp8(x[bj][1][0], x[bj][1][1], x[bj][1][2], x[bj][1][3])};
;                 continue; }
.LBB0_214:
	v_mov_b32_e32 v164, v175
	v_cvt_pk_fp8_f32 v164, v26, v27
	v_mov_b32_e32 v26, v175
	v_mov_b32_e32 v27, v175
	v_cvt_pk_fp8_f32 v26, v22, v23
	v_cvt_pk_fp8_f32 v27, v18, v19
	v_mov_b32_e32 v165, v175
	v_cvt_pk_fp8_f32 v165, v30, v31
	v_cvt_pk_fp8_f32 v26, v24, v25 op_sel:[0,0,1]
	v_cvt_pk_fp8_f32 v27, v20, v21 op_sel:[0,0,1]
	v_ashrrev_i32_e32 v197, 31, v196
	v_lshlrev_b64 v[162:163], 9, v[196:197]
	v_cvt_pk_fp8_f32 v164, v28, v29 op_sel:[0,0,1]
	v_cvt_pk_fp8_f32 v165, v32, v33 op_sel:[0,0,1]
	v_lshl_add_u64 v[162:163], v[190:191], 0, v[162:163]
	global_store_dwordx2 v[162:163], v[26:27], off offset:32
	v_mov_b64_e32 v[18:19], v[98:99]
	v_mov_b64_e32 v[22:23], v[102:103]
	v_mov_b64_e32 v[30:31], v[106:107]
	v_mov_b64_e32 v[26:27], v[110:111]
	s_and_b64 vcc, exec, s[6:7]
	v_mov_b64_e32 v[20:21], v[100:101]
	v_mov_b64_e32 v[24:25], v[104:105]
	v_mov_b64_e32 v[32:33], v[108:109]
	v_mov_b64_e32 v[28:29], v[112:113]
	global_store_dwordx2 v[162:163], v[164:165], off
	s_cbranch_vccnz .LBB0_216
	v_pk_mul_f32 v[18:19], v[112:113], v[112:113]
	v_pk_mul_f32 v[20:21], v[110:111], v[110:111]
	s_nop 0
	v_pk_mov_b32 v[22:23], v[20:21], v[18:19] op_sel:[1,0]
	v_mov_b32_e32 v21, v19
	v_pk_add_f32 v[18:19], v[22:23], v[20:21]
	v_pk_mul_f32 v[20:21], v[108:109], v[108:109]
	v_pk_mul_f32 v[22:23], v[106:107], v[106:107]
	v_pk_add_f32 v[18:19], v[18:19], v[18:19] op_sel:[0,1] op_sel_hi:[1,0]
	v_pk_mov_b32 v[24:25], v[22:23], v[20:21] op_sel:[1,0]
	v_mov_b32_e32 v23, v21
	v_pk_add_f32 v[20:21], v[24:25], v[22:23]
	v_mul_f32_e32 v22, v98, v98
	v_mul_f32_e32 v23, v99, v99
	v_pk_add_f32 v[20:21], v[20:21], v[20:21] op_sel:[0,1] op_sel_hi:[1,0]
	v_mov_b32_e32 v19, v22
	v_mov_b32_e32 v21, v23
	v_pk_add_f32 v[18:19], v[18:19], v[20:21]
	v_mul_f32_e32 v20, v103, v103
	v_mul_f32_e32 v22, v105, v105
	v_mul_f32_e32 v24, v100, v100
	v_mul_f32_e32 v25, v101, v101
	v_pk_fma_f32 v[20:21], v[102:103], v[102:103], v[20:21] op_sel_hi:[1,1,0]
	v_pk_fma_f32 v[22:23], v[104:105], v[104:105], v[22:23] op_sel_hi:[1,1,0]
	v_mov_b32_e32 v21, v24
	v_mov_b32_e32 v23, v25
	v_pk_add_f32 v[20:21], v[20:21], v[22:23]
	s_nop 0
	v_pk_add_f32 v[18:19], v[18:19], v[20:21]
	v_and_b32_e32 v20, 64, v212
	v_add_f32_e32 v18, v18, v19
	v_xor_b32_e32 v19, 16, v212
	v_add_u32_e32 v20, 64, v20
	v_cmp_lt_i32_e32 vcc, v19, v20
	s_nop 1
	v_cndmask_b32_e32 v19, v212, v19, vcc
	v_lshlrev_b32_e32 v19, 2, v19
	ds_bpermute_b32 v19, v19, v18
	s_waitcnt lgkmcnt(0)
	v_add_f32_e32 v18, v18, v19
	v_xor_b32_e32 v19, 32, v212
	v_cmp_lt_i32_e32 vcc, v19, v20
	s_nop 1
	v_cndmask_b32_e32 v19, v212, v19, vcc
	v_lshlrev_b32_e32 v19, 2, v19
	ds_bpermute_b32 v19, v19, v18
	s_waitcnt lgkmcnt(0)
	v_add_f32_e32 v18, v18, v19
	v_fmamk_f32 v18, v18, 0x3c800000, v210
	v_mul_f32_e32 v19, 0x4f800000, v18
	v_cmp_gt_f32_e32 vcc, s28, v18
	s_nop 1
	v_cndmask_b32_e32 v18, v18, v19, vcc
	v_sqrt_f32_e32 v19, v18
	s_nop 0
	v_add_u32_e32 v20, -1, v19
	v_fma_f32 v21, -v20, v19, v18
	v_cmp_ge_f32_e64 s[10:11], 0, v21
	v_add_u32_e32 v21, 1, v19
	s_nop 0
	v_cndmask_b32_e64 v20, v19, v20, s[10:11]
	v_fma_f32 v19, -v21, v19, v18
	v_cmp_lt_f32_e64 s[10:11], 0, v19
	s_nop 1
	v_cndmask_b32_e64 v19, v20, v21, s[10:11]
	v_mul_f32_e32 v20, 0x37800000, v19
	v_cndmask_b32_e32 v19, v19, v20, vcc
	v_cmp_class_f32_e32 vcc, v18, v211
	s_nop 1
	v_cndmask_b32_e32 v18, v19, v18, vcc
	v_div_scale_f32 v19, s[0:1], v18, v18, s29
	v_rcp_f32_e32 v20, v19
	s_nop 0
	v_fma_f32 v21, -v19, v20, 1.0
	v_fmac_f32_e32 v20, v21, v20
	v_div_scale_f32 v21, vcc, s29, v18, s29
	v_mul_f32_e32 v22, v21, v20
	v_fma_f32 v23, -v19, v22, v21
	v_fmac_f32_e32 v22, v23, v20
	v_fma_f32 v19, -v19, v22, v21
	v_div_fmas_f32 v19, v19, v20, v22
	v_div_fixup_f32 v18, v19, v18, s29
	v_pk_mul_f32 v[20:21], v[110:111], v[18:19] op_sel_hi:[1,0]
	v_pk_mul_f32 v[22:23], v[112:113], v[18:19] op_sel_hi:[1,0]
	s_nop 0
	v_pk_mul_f32 v[26:27], v[14:15], v[20:21]
	v_pk_mul_f32 v[28:29], v[16:17], v[22:23]
	v_pk_mul_f32 v[20:21], v[106:107], v[18:19] op_sel_hi:[1,0]
	v_pk_mul_f32 v[22:23], v[108:109], v[18:19] op_sel_hi:[1,0]
	v_pk_mul_f32 v[30:31], v[10:11], v[20:21]
	v_pk_mul_f32 v[32:33], v[12:13], v[22:23]
	v_pk_mul_f32 v[20:21], v[102:103], v[18:19] op_sel_hi:[1,0]
	v_pk_mul_f32 v[22:23], v[104:105], v[18:19] op_sel_hi:[1,0]
	v_pk_mul_f32 v[162:163], v[98:99], v[18:19] op_sel_hi:[1,0]
	v_pk_mul_f32 v[18:19], v[100:101], v[18:19] op_sel_hi:[1,0]
	v_pk_mul_f32 v[24:25], v[8:9], v[22:23]
	v_pk_mul_f32 v[22:23], v[6:7], v[20:21]
	v_pk_mul_f32 v[20:21], v[4:5], v[18:19]
	v_pk_mul_f32 v[18:19], v[2:3], v[162:163]

; __device__ __forceinline__ unsigned pk4_fp8(float a, float b, float c, float d) { unsigned w = 0u; w = __builtin_amdgcn_cvt_pk_fp8_f32(a, b, w, false); w = __builtin_amdgcn_cvt_pk_fp8_f32(c, d, w, true); return w; }
; template <bool F8OUT = false> __device__ __forceinline__ void head_tile_store(const f32x4 (&acc)[2][2][4][2], bf16_t* obase  , int opitch, const float* gain, float scale, const f32x2e* rope, int row0, int fq) {
;     ...
;             if (gain) {
;                 float ss = 0.f;
; #pragma unroll
;                 for (int bj = 0; bj < 2; ++bj)
; #pragma unroll
;                     for (int n = 0; n < 2; ++n) ss += (x[bj][n][0] * x[bj][n][0] + x[bj][n][1] * x[bj][n][1]) + (x[bj][n][2] * x[bj][n][2] + x[bj][n][3] * x[bj][n][3]);
;                 ss += __shfl_xor(ss, 16); ss += __shfl_xor(ss, 32);
;                 const float r = scale / sqrtf(ss * (1.f / 64.f) + 1e-6f);
; #pragma unroll
;                 for (int bj = 0; bj < 2; ++bj)
; #pragma unroll
;                     for (int n = 0; n < 2; ++n) x[bj][n] = x[bj][n] * r * g[bj][n];
;             }
;     ...
;             if constexpr (F8OUT) { unsigned char* rowp8 = (unsigned char*)obase + (size_t)row * opitch + 8 * fq; typedef unsigned u32x2_ __attribute__((ext_vector_type(2)));
; #pragma unroll
;                 for (int bj = 0; bj < 2; ++bj) *(u32x2_*)(rowp8 + 32 * bj) = (u32x2_){pk4_fp8(x[bj][0][0], x[bj][0][1], x[bj][0][2], x[bj][0][3]), pk4_fp8(x[bj][1][0], x[bj][1][1], x[bj][1][2], x[bj][1][3])};
;                 continue; }
.LBB0_218:
	v_mov_b32_e32 v164, v175
	v_cvt_pk_fp8_f32 v164, v26, v27
	v_mov_b32_e32 v26, v175
	v_mov_b32_e32 v27, v175
	v_cvt_pk_fp8_f32 v26, v22, v23
	v_cvt_pk_fp8_f32 v27, v18, v19
	v_mov_b32_e32 v165, v175
	v_cvt_pk_fp8_f32 v165, v30, v31
	v_cvt_pk_fp8_f32 v26, v24, v25 op_sel:[0,0,1]
	v_cvt_pk_fp8_f32 v27, v20, v21 op_sel:[0,0,1]
	v_ashrrev_i32_e32 v201, 31, v200
	v_lshlrev_b64 v[162:163], 9, v[200:201]
	v_cvt_pk_fp8_f32 v164, v28, v29 op_sel:[0,0,1]
	v_cvt_pk_fp8_f32 v165, v32, v33 op_sel:[0,0,1]
	v_lshl_add_u64 v[162:163], v[190:191], 0, v[162:163]
	global_store_dwordx2 v[162:163], v[26:27], off offset:32
	v_mov_b64_e32 v[18:19], v[82:83]
	v_mov_b64_e32 v[22:23], v[86:87]
	v_mov_b64_e32 v[30:31], v[90:91]
	v_mov_b64_e32 v[26:27], v[94:95]
	s_and_b64 vcc, exec, s[6:7]
	v_mov_b64_e32 v[20:21], v[84:85]
	v_mov_b64_e32 v[24:25], v[88:89]
	v_mov_b64_e32 v[32:33], v[92:93]
	v_mov_b64_e32 v[28:29], v[96:97]
	global_store_dwordx2 v[162:163], v[164:165], off
	s_cbranch_vccnz .LBB0_220
	v_pk_mul_f32 v[18:19], v[96:97], v[96:97]
	v_pk_mul_f32 v[20:21], v[94:95], v[94:95]
	s_nop 0
	v_pk_mov_b32 v[22:23], v[20:21], v[18:19] op_sel:[1,0]
	v_mov_b32_e32 v21, v19
	v_pk_add_f32 v[18:19], v[22:23], v[20:21]
	v_pk_mul_f32 v[20:21], v[92:93], v[92:93]
	v_pk_mul_f32 v[22:23], v[90:91], v[90:91]
	v_pk_add_f32 v[18:19], v[18:19], v[18:19] op_sel:[0,1] op_sel_hi:[1,0]
	v_pk_mov_b32 v[24:25], v[22:23], v[20:21] op_sel:[1,0]
	v_mov_b32_e32 v23, v21
	v_pk_add_f32 v[20:21], v[24:25], v[22:23]
	v_mul_f32_e32 v22, v82, v82
	v_mul_f32_e32 v23, v83, v83
	v_pk_add_f32 v[20:21], v[20:21], v[20:21] op_sel:[0,1] op_sel_hi:[1,0]
	v_mov_b32_e32 v19, v22
	v_mov_b32_e32 v21, v23
	v_pk_add_f32 v[18:19], v[18:19], v[20:21]
	v_mul_f32_e32 v20, v87, v87
	v_mul_f32_e32 v22, v89, v89
	v_mul_f32_e32 v24, v84, v84
	v_mul_f32_e32 v25, v85, v85
	v_pk_fma_f32 v[20:21], v[86:87], v[86:87], v[20:21] op_sel_hi:[1,1,0]
	v_pk_fma_f32 v[22:23], v[88:89], v[88:89], v[22:23] op_sel_hi:[1,1,0]
	v_mov_b32_e32 v21, v24
	v_mov_b32_e32 v23, v25
	v_pk_add_f32 v[20:21], v[20:21], v[22:23]
	s_nop 0
	v_pk_add_f32 v[18:19], v[18:19], v[20:21]
	v_and_b32_e32 v20, 64, v212
	v_add_f32_e32 v18, v18, v19
	v_xor_b32_e32 v19, 16, v212
	v_add_u32_e32 v20, 64, v20
	v_cmp_lt_i32_e32 vcc, v19, v20
	s_nop 1
	v_cndmask_b32_e32 v19, v212, v19, vcc
	v_lshlrev_b32_e32 v19, 2, v19
	ds_bpermute_b32 v19, v19, v18
	s_waitcnt lgkmcnt(0)
	v_add_f32_e32 v18, v18, v19
	v_xor_b32_e32 v19, 32, v212
	v_cmp_lt_i32_e32 vcc, v19, v20
	s_nop 1
	v_cndmask_b32_e32 v19, v212, v19, vcc
	v_lshlrev_b32_e32 v19, 2, v19
	ds_bpermute_b32 v19, v19, v18
	s_waitcnt lgkmcnt(0)
	v_add_f32_e32 v18, v18, v19
	v_fmamk_f32 v18, v18, 0x3c800000, v210
	v_mul_f32_e32 v19, 0x4f800000, v18
	v_cmp_gt_f32_e32 vcc, s28, v18
	s_nop 1
	v_cndmask_b32_e32 v18, v18, v19, vcc
	v_sqrt_f32_e32 v19, v18
	s_nop 0
	v_add_u32_e32 v20, -1, v19
	v_fma_f32 v21, -v20, v19, v18
	v_cmp_ge_f32_e64 s[10:11], 0, v21
	v_add_u32_e32 v21, 1, v19
	s_nop 0
	v_cndmask_b32_e64 v20, v19, v20, s[10:11]
	v_fma_f32 v19, -v21, v19, v18
	v_cmp_lt_f32_e64 s[10:11], 0, v19
	s_nop 1
	v_cndmask_b32_e64 v19, v20, v21, s[10:11]
	v_mul_f32_e32 v20, 0x37800000, v19
	v_cndmask_b32_e32 v19, v19, v20, vcc
	v_cmp_class_f32_e32 vcc, v18, v211
	s_nop 1
	v_cndmask_b32_e32 v18, v19, v18, vcc
	v_div_scale_f32 v19, s[0:1], v18, v18, s29
	v_rcp_f32_e32 v20, v19
	s_nop 0
	v_fma_f32 v21, -v19, v20, 1.0
	v_fmac_f32_e32 v20, v21, v20
	v_div_scale_f32 v21, vcc, s29, v18, s29
	v_mul_f32_e32 v22, v21, v20
	v_fma_f32 v23, -v19, v22, v21
	v_fmac_f32_e32 v22, v23, v20
	v_fma_f32 v19, -v19, v22, v21
	v_div_fmas_f32 v19, v19, v20, v22
	v_div_fixup_f32 v18, v19, v18, s29
	v_pk_mul_f32 v[20:21], v[94:95], v[18:19] op_sel_hi:[1,0]
	v_pk_mul_f32 v[22:23], v[96:97], v[18:19] op_sel_hi:[1,0]
	s_nop 0
	v_pk_mul_f32 v[26:27], v[14:15], v[20:21]
	v_pk_mul_f32 v[28:29], v[16:17], v[22:23]
	v_pk_mul_f32 v[20:21], v[90:91], v[18:19] op_sel_hi:[1,0]
	v_pk_mul_f32 v[22:23], v[92:93], v[18:19] op_sel_hi:[1,0]
	v_pk_mul_f32 v[30:31], v[10:11], v[20:21]
	v_pk_mul_f32 v[32:33], v[12:13], v[22:23]
	v_pk_mul_f32 v[20:21], v[86:87], v[18:19] op_sel_hi:[1,0]
	v_pk_mul_f32 v[22:23], v[88:89], v[18:19] op_sel_hi:[1,0]
	v_pk_mul_f32 v[162:163], v[82:83], v[18:19] op_sel_hi:[1,0]
	v_pk_mul_f32 v[18:19], v[84:85], v[18:19] op_sel_hi:[1,0]
	v_pk_mul_f32 v[24:25], v[8:9], v[22:23]
	v_pk_mul_f32 v[22:23], v[6:7], v[20:21]
	v_pk_mul_f32 v[20:21], v[4:5], v[18:19]
	v_pk_mul_f32 v[18:19], v[2:3], v[162:163]

; __device__ __forceinline__ unsigned pk4_fp8(float a, float b, float c, float d) { unsigned w = 0u; w = __builtin_amdgcn_cvt_pk_fp8_f32(a, b, w, false); w = __builtin_amdgcn_cvt_pk_fp8_f32(c, d, w, true); return w; }
; template <bool F8OUT = false> __device__ __forceinline__ void head_tile_store(const f32x4 (&acc)[2][2][4][2], bf16_t* obase  , int opitch, const float* gain, float scale, const f32x2e* rope, int row0, int fq) {
;     ...
;             if (gain) {
;                 float ss = 0.f;
; #pragma unroll
;                 for (int bj = 0; bj < 2; ++bj)
; #pragma unroll
;                     for (int n = 0; n < 2; ++n) ss += (x[bj][n][0] * x[bj][n][0] + x[bj][n][1] * x[bj][n][1]) + (x[bj][n][2] * x[bj][n][2] + x[bj][n][3] * x[bj][n][3]);
;                 ss += __shfl_xor(ss, 16); ss += __shfl_xor(ss, 32);
;                 const float r = scale / sqrtf(ss * (1.f / 64.f) + 1e-6f);
; #pragma unroll
;                 for (int bj = 0; bj < 2; ++bj)
; #pragma unroll
;                     for (int n = 0; n < 2; ++n) x[bj][n] = x[bj][n] * r * g[bj][n];
;             }
;     ...
;             if constexpr (F8OUT) { unsigned char* rowp8 = (unsigned char*)obase + (size_t)row * opitch + 8 * fq; typedef unsigned u32x2_ __attribute__((ext_vector_type(2)));
; #pragma unroll
;                 for (int bj = 0; bj < 2; ++bj) *(u32x2_*)(rowp8 + 32 * bj) = (u32x2_){pk4_fp8(x[bj][0][0], x[bj][0][1], x[bj][0][2], x[bj][0][3]), pk4_fp8(x[bj][1][0], x[bj][1][1], x[bj][1][2], x[bj][1][3])};
;                 continue; }
.LBB0_222:
	v_mov_b32_e32 v164, v175
	v_cvt_pk_fp8_f32 v164, v26, v27
	v_mov_b32_e32 v26, v175
	v_mov_b32_e32 v27, v175
	v_cvt_pk_fp8_f32 v26, v22, v23
	v_cvt_pk_fp8_f32 v27, v18, v19
	v_mov_b32_e32 v165, v175
	v_cvt_pk_fp8_f32 v165, v30, v31
	v_cvt_pk_fp8_f32 v26, v24, v25 op_sel:[0,0,1]
	v_cvt_pk_fp8_f32 v27, v20, v21 op_sel:[0,0,1]
	v_ashrrev_i32_e32 v201, 31, v200
	v_lshlrev_b64 v[162:163], 9, v[200:201]
	v_cvt_pk_fp8_f32 v164, v28, v29 op_sel:[0,0,1]
	v_cvt_pk_fp8_f32 v165, v32, v33 op_sel:[0,0,1]
	v_lshl_add_u64 v[162:163], v[190:191], 0, v[162:163]
	global_store_dwordx2 v[162:163], v[26:27], off offset:32
	v_mov_b64_e32 v[18:19], v[66:67]
	v_mov_b64_e32 v[22:23], v[70:71]
	v_mov_b64_e32 v[30:31], v[74:75]
	v_mov_b64_e32 v[26:27], v[78:79]
	s_and_b64 vcc, exec, s[6:7]
	v_mov_b64_e32 v[20:21], v[68:69]
	v_mov_b64_e32 v[24:25], v[72:73]
	v_mov_b64_e32 v[32:33], v[76:77]
	v_mov_b64_e32 v[28:29], v[80:81]
	global_store_dwordx2 v[162:163], v[164:165], off
	s_cbranch_vccnz .LBB0_224
	v_pk_mul_f32 v[18:19], v[80:81], v[80:81]
	v_pk_mul_f32 v[20:21], v[78:79], v[78:79]
	s_nop 0
	v_pk_mov_b32 v[22:23], v[20:21], v[18:19] op_sel:[1,0]
	v_mov_b32_e32 v21, v19
	v_pk_add_f32 v[18:19], v[22:23], v[20:21]
	v_pk_mul_f32 v[20:21], v[76:77], v[76:77]
	v_pk_mul_f32 v[22:23], v[74:75], v[74:75]
	v_pk_add_f32 v[18:19], v[18:19], v[18:19] op_sel:[0,1] op_sel_hi:[1,0]
	v_pk_mov_b32 v[24:25], v[22:23], v[20:21] op_sel:[1,0]
	v_mov_b32_e32 v23, v21
	v_pk_add_f32 v[20:21], v[24:25], v[22:23]
	v_mul_f32_e32 v22, v66, v66
	v_mul_f32_e32 v23, v67, v67
	v_pk_add_f32 v[20:21], v[20:21], v[20:21] op_sel:[0,1] op_sel_hi:[1,0]
	v_mov_b32_e32 v19, v22
	v_mov_b32_e32 v21, v23
	v_pk_add_f32 v[18:19], v[18:19], v[20:21]
	v_mul_f32_e32 v20, v71, v71
	v_mul_f32_e32 v22, v73, v73
	v_mul_f32_e32 v24, v68, v68
	v_mul_f32_e32 v25, v69, v69
	v_pk_fma_f32 v[20:21], v[70:71], v[70:71], v[20:21] op_sel_hi:[1,1,0]
	v_pk_fma_f32 v[22:23], v[72:73], v[72:73], v[22:23] op_sel_hi:[1,1,0]
	v_mov_b32_e32 v21, v24
	v_mov_b32_e32 v23, v25
	v_pk_add_f32 v[20:21], v[20:21], v[22:23]
	s_nop 0
	v_pk_add_f32 v[18:19], v[18:19], v[20:21]
	v_and_b32_e32 v20, 64, v212
	v_add_f32_e32 v18, v18, v19
	v_xor_b32_e32 v19, 16, v212
	v_add_u32_e32 v20, 64, v20
	v_cmp_lt_i32_e32 vcc, v19, v20
	s_nop 1
	v_cndmask_b32_e32 v19, v212, v19, vcc
	v_lshlrev_b32_e32 v19, 2, v19
	ds_bpermute_b32 v19, v19, v18
	s_waitcnt lgkmcnt(0)
	v_add_f32_e32 v18, v18, v19
	v_xor_b32_e32 v19, 32, v212
	v_cmp_lt_i32_e32 vcc, v19, v20
	s_nop 1
	v_cndmask_b32_e32 v19, v212, v19, vcc
	v_lshlrev_b32_e32 v19, 2, v19
	ds_bpermute_b32 v19, v19, v18
	s_waitcnt lgkmcnt(0)
	v_add_f32_e32 v18, v18, v19
	v_fmamk_f32 v18, v18, 0x3c800000, v210
	v_mul_f32_e32 v19, 0x4f800000, v18
	v_cmp_gt_f32_e32 vcc, s28, v18
	s_nop 1
	v_cndmask_b32_e32 v18, v18, v19, vcc
	v_sqrt_f32_e32 v19, v18
	s_nop 0
	v_add_u32_e32 v20, -1, v19
	v_fma_f32 v21, -v20, v19, v18
	v_cmp_ge_f32_e64 s[10:11], 0, v21
	v_add_u32_e32 v21, 1, v19
	s_nop 0
	v_cndmask_b32_e64 v20, v19, v20, s[10:11]
	v_fma_f32 v19, -v21, v19, v18
	v_cmp_lt_f32_e64 s[10:11], 0, v19
	s_nop 1
	v_cndmask_b32_e64 v19, v20, v21, s[10:11]
	v_mul_f32_e32 v20, 0x37800000, v19
	v_cndmask_b32_e32 v19, v19, v20, vcc
	v_cmp_class_f32_e32 vcc, v18, v211
	s_nop 1
	v_cndmask_b32_e32 v18, v19, v18, vcc
	v_div_scale_f32 v19, s[0:1], v18, v18, s29
	v_rcp_f32_e32 v20, v19
	s_nop 0
	v_fma_f32 v21, -v19, v20, 1.0
	v_fmac_f32_e32 v20, v21, v20
	v_div_scale_f32 v21, vcc, s29, v18, s29
	v_mul_f32_e32 v22, v21, v20
	v_fma_f32 v23, -v19, v22, v21
	v_fmac_f32_e32 v22, v23, v20
	v_fma_f32 v19, -v19, v22, v21
	v_div_fmas_f32 v19, v19, v20, v22
	v_div_fixup_f32 v18, v19, v18, s29
	v_pk_mul_f32 v[20:21], v[78:79], v[18:19] op_sel_hi:[1,0]
	v_pk_mul_f32 v[22:23], v[80:81], v[18:19] op_sel_hi:[1,0]
	s_nop 0
	v_pk_mul_f32 v[26:27], v[14:15], v[20:21]
	v_pk_mul_f32 v[28:29], v[16:17], v[22:23]
	v_pk_mul_f32 v[20:21], v[74:75], v[18:19] op_sel_hi:[1,0]
	v_pk_mul_f32 v[22:23], v[76:77], v[18:19] op_sel_hi:[1,0]
	v_pk_mul_f32 v[30:31], v[10:11], v[20:21]
	v_pk_mul_f32 v[32:33], v[12:13], v[22:23]
	v_pk_mul_f32 v[20:21], v[70:71], v[18:19] op_sel_hi:[1,0]
	v_pk_mul_f32 v[22:23], v[72:73], v[18:19] op_sel_hi:[1,0]
	v_pk_mul_f32 v[162:163], v[66:67], v[18:19] op_sel_hi:[1,0]
	v_pk_mul_f32 v[18:19], v[68:69], v[18:19] op_sel_hi:[1,0]
	v_pk_mul_f32 v[24:25], v[8:9], v[22:23]
	v_pk_mul_f32 v[22:23], v[6:7], v[20:21]
	v_pk_mul_f32 v[20:21], v[4:5], v[18:19]
	v_pk_mul_f32 v[18:19], v[2:3], v[162:163]

; __device__ __forceinline__ unsigned pk4_fp8(float a, float b, float c, float d) { unsigned w = 0u; w = __builtin_amdgcn_cvt_pk_fp8_f32(a, b, w, false); w = __builtin_amdgcn_cvt_pk_fp8_f32(c, d, w, true); return w; }
; template <bool F8OUT = false> __device__ __forceinline__ void head_tile_store(const f32x4 (&acc)[2][2][4][2], bf16_t* obase  , int opitch, const float* gain, float scale, const f32x2e* rope, int row0, int fq) {
;     ...
;             if (gain) {
;                 float ss = 0.f;
; #pragma unroll
;                 for (int bj = 0; bj < 2; ++bj)
; #pragma unroll
;                     for (int n = 0; n < 2; ++n) ss += (x[bj][n][0] * x[bj][n][0] + x[bj][n][1] * x[bj][n][1]) + (x[bj][n][2] * x[bj][n][2] + x[bj][n][3] * x[bj][n][3]);
;                 ss += __shfl_xor(ss, 16); ss += __shfl_xor(ss, 32);
;                 const float r = scale / sqrtf(ss * (1.f / 64.f) + 1e-6f);
; #pragma unroll
;                 for (int bj = 0; bj < 2; ++bj)
; #pragma unroll
;                     for (int n = 0; n < 2; ++n) x[bj][n] = x[bj][n] * r * g[bj][n];
;             }
;     ...
;             if constexpr (F8OUT) { unsigned char* rowp8 = (unsigned char*)obase + (size_t)row * opitch + 8 * fq; typedef unsigned u32x2_ __attribute__((ext_vector_type(2)));
; #pragma unroll
;                 for (int bj = 0; bj < 2; ++bj) *(u32x2_*)(rowp8 + 32 * bj) = (u32x2_){pk4_fp8(x[bj][0][0], x[bj][0][1], x[bj][0][2], x[bj][0][3]), pk4_fp8(x[bj][1][0], x[bj][1][1], x[bj][1][2], x[bj][1][3])};
;                 continue; }
.LBB0_226:
	v_mov_b32_e32 v164, v175
	v_cvt_pk_fp8_f32 v164, v26, v27
	v_mov_b32_e32 v26, v175
	v_mov_b32_e32 v27, v175
	v_cvt_pk_fp8_f32 v26, v22, v23
	v_cvt_pk_fp8_f32 v27, v18, v19
	v_mov_b32_e32 v165, v175
	v_cvt_pk_fp8_f32 v165, v30, v31
	v_cvt_pk_fp8_f32 v26, v24, v25 op_sel:[0,0,1]
	v_cvt_pk_fp8_f32 v27, v20, v21 op_sel:[0,0,1]
	v_ashrrev_i32_e32 v199, 31, v198
	v_lshlrev_b64 v[162:163], 9, v[198:199]
	v_cvt_pk_fp8_f32 v164, v28, v29 op_sel:[0,0,1]
	v_cvt_pk_fp8_f32 v165, v32, v33 op_sel:[0,0,1]
	v_lshl_add_u64 v[162:163], v[190:191], 0, v[162:163]
	global_store_dwordx2 v[162:163], v[26:27], off offset:32
	v_mov_b64_e32 v[18:19], v[50:51]
	v_mov_b64_e32 v[22:23], v[54:55]
	v_mov_b64_e32 v[30:31], v[58:59]
	v_mov_b64_e32 v[26:27], v[62:63]
	s_and_b64 vcc, exec, s[6:7]
	v_mov_b64_e32 v[20:21], v[52:53]
	v_mov_b64_e32 v[24:25], v[56:57]
	v_mov_b64_e32 v[32:33], v[60:61]
	v_mov_b64_e32 v[28:29], v[64:65]
	global_store_dwordx2 v[162:163], v[164:165], off
	s_cbranch_vccnz .LBB0_228
	v_pk_mul_f32 v[18:19], v[64:65], v[64:65]
	v_pk_mul_f32 v[20:21], v[62:63], v[62:63]
	s_nop 0
	v_pk_mov_b32 v[22:23], v[20:21], v[18:19] op_sel:[1,0]
	v_mov_b32_e32 v21, v19
	v_pk_add_f32 v[18:19], v[22:23], v[20:21]
	v_pk_mul_f32 v[20:21], v[60:61], v[60:61]
	v_pk_mul_f32 v[22:23], v[58:59], v[58:59]
	v_pk_add_f32 v[18:19], v[18:19], v[18:19] op_sel:[0,1] op_sel_hi:[1,0]
	v_pk_mov_b32 v[24:25], v[22:23], v[20:21] op_sel:[1,0]
	v_mov_b32_e32 v23, v21
	v_pk_add_f32 v[20:21], v[24:25], v[22:23]
	v_mul_f32_e32 v22, v50, v50
	v_mul_f32_e32 v23, v51, v51
	v_pk_add_f32 v[20:21], v[20:21], v[20:21] op_sel:[0,1] op_sel_hi:[1,0]
	v_mov_b32_e32 v19, v22
	v_mov_b32_e32 v21, v23
	v_pk_add_f32 v[18:19], v[18:19], v[20:21]
	v_mul_f32_e32 v20, v55, v55
	v_mul_f32_e32 v22, v57, v57
	v_mul_f32_e32 v24, v52, v52
	v_mul_f32_e32 v25, v53, v53
	v_pk_fma_f32 v[20:21], v[54:55], v[54:55], v[20:21] op_sel_hi:[1,1,0]
	v_pk_fma_f32 v[22:23], v[56:57], v[56:57], v[22:23] op_sel_hi:[1,1,0]
	v_mov_b32_e32 v21, v24
	v_mov_b32_e32 v23, v25
	v_pk_add_f32 v[20:21], v[20:21], v[22:23]
	s_nop 0
	v_pk_add_f32 v[18:19], v[18:19], v[20:21]
	v_and_b32_e32 v20, 64, v212
	v_add_f32_e32 v18, v18, v19
	v_xor_b32_e32 v19, 16, v212
	v_add_u32_e32 v20, 64, v20
	v_cmp_lt_i32_e32 vcc, v19, v20
	s_nop 1
	v_cndmask_b32_e32 v19, v212, v19, vcc
	v_lshlrev_b32_e32 v19, 2, v19
	ds_bpermute_b32 v19, v19, v18
	s_waitcnt lgkmcnt(0)
	v_add_f32_e32 v18, v18, v19
	v_xor_b32_e32 v19, 32, v212
	v_cmp_lt_i32_e32 vcc, v19, v20
	s_nop 1
	v_cndmask_b32_e32 v19, v212, v19, vcc
	v_lshlrev_b32_e32 v19, 2, v19
	ds_bpermute_b32 v19, v19, v18
	s_waitcnt lgkmcnt(0)
	v_add_f32_e32 v18, v18, v19
	v_fmamk_f32 v18, v18, 0x3c800000, v210
	v_mul_f32_e32 v19, 0x4f800000, v18
	v_cmp_gt_f32_e32 vcc, s28, v18
	s_nop 1
	v_cndmask_b32_e32 v18, v18, v19, vcc
	v_sqrt_f32_e32 v19, v18
	s_nop 0
	v_add_u32_e32 v20, -1, v19
	v_fma_f32 v21, -v20, v19, v18
	v_cmp_ge_f32_e64 s[10:11], 0, v21
	v_add_u32_e32 v21, 1, v19
	s_nop 0
	v_cndmask_b32_e64 v20, v19, v20, s[10:11]
	v_fma_f32 v19, -v21, v19, v18
	v_cmp_lt_f32_e64 s[10:11], 0, v19
	s_nop 1
	v_cndmask_b32_e64 v19, v20, v21, s[10:11]
	v_mul_f32_e32 v20, 0x37800000, v19
	v_cndmask_b32_e32 v19, v19, v20, vcc
	v_cmp_class_f32_e32 vcc, v18, v211
	s_nop 1
	v_cndmask_b32_e32 v18, v19, v18, vcc
	v_div_scale_f32 v19, s[0:1], v18, v18, s29
	v_rcp_f32_e32 v20, v19
	s_nop 0
	v_fma_f32 v21, -v19, v20, 1.0
	v_fmac_f32_e32 v20, v21, v20
	v_div_scale_f32 v21, vcc, s29, v18, s29
	v_mul_f32_e32 v22, v21, v20
	v_fma_f32 v23, -v19, v22, v21
	v_fmac_f32_e32 v22, v23, v20
	v_fma_f32 v19, -v19, v22, v21
	v_div_fmas_f32 v19, v19, v20, v22
	v_div_fixup_f32 v18, v19, v18, s29
	v_pk_mul_f32 v[20:21], v[62:63], v[18:19] op_sel_hi:[1,0]
	v_pk_mul_f32 v[22:23], v[64:65], v[18:19] op_sel_hi:[1,0]
	s_nop 0
	v_pk_mul_f32 v[26:27], v[14:15], v[20:21]
	v_pk_mul_f32 v[28:29], v[16:17], v[22:23]
	v_pk_mul_f32 v[20:21], v[58:59], v[18:19] op_sel_hi:[1,0]
	v_pk_mul_f32 v[22:23], v[60:61], v[18:19] op_sel_hi:[1,0]
	v_pk_mul_f32 v[30:31], v[10:11], v[20:21]
	v_pk_mul_f32 v[32:33], v[12:13], v[22:23]
	v_pk_mul_f32 v[20:21], v[54:55], v[18:19] op_sel_hi:[1,0]
	v_pk_mul_f32 v[22:23], v[56:57], v[18:19] op_sel_hi:[1,0]
	v_pk_mul_f32 v[162:163], v[50:51], v[18:19] op_sel_hi:[1,0]
	v_pk_mul_f32 v[18:19], v[52:53], v[18:19] op_sel_hi:[1,0]
	v_pk_mul_f32 v[24:25], v[8:9], v[22:23]
	v_pk_mul_f32 v[22:23], v[6:7], v[20:21]
	v_pk_mul_f32 v[20:21], v[4:5], v[18:19]
	v_pk_mul_f32 v[18:19], v[2:3], v[162:163]

; __device__ __forceinline__ unsigned pk4_fp8(float a, float b, float c, float d) { unsigned w = 0u; w = __builtin_amdgcn_cvt_pk_fp8_f32(a, b, w, false); w = __builtin_amdgcn_cvt_pk_fp8_f32(c, d, w, true); return w; }
; template <bool F8OUT = false> __device__ __forceinline__ void head_tile_store(const f32x4 (&acc)[2][2][4][2], bf16_t* obase  , int opitch, const float* gain, float scale, const f32x2e* rope, int row0, int fq) {
;     ...
;             if (gain) {
;                 float ss = 0.f;
; #pragma unroll
;                 for (int bj = 0; bj < 2; ++bj)
; #pragma unroll
;                     for (int n = 0; n < 2; ++n) ss += (x[bj][n][0] * x[bj][n][0] + x[bj][n][1] * x[bj][n][1]) + (x[bj][n][2] * x[bj][n][2] + x[bj][n][3] * x[bj][n][3]);
;                 ss += __shfl_xor(ss, 16); ss += __shfl_xor(ss, 32);
;                 const float r = scale / sqrtf(ss * (1.f / 64.f) + 1e-6f);
; #pragma unroll
;                 for (int bj = 0; bj < 2; ++bj)
; #pragma unroll
;                     for (int n = 0; n < 2; ++n) x[bj][n] = x[bj][n] * r * g[bj][n];
;             }
;     ...
;             if constexpr (F8OUT) { unsigned char* rowp8 = (unsigned char*)obase + (size_t)row * opitch + 8 * fq; typedef unsigned u32x2_ __attribute__((ext_vector_type(2)));
; #pragma unroll
;                 for (int bj = 0; bj < 2; ++bj) *(u32x2_*)(rowp8 + 32 * bj) = (u32x2_){pk4_fp8(x[bj][0][0], x[bj][0][1], x[bj][0][2], x[bj][0][3]), pk4_fp8(x[bj][1][0], x[bj][1][1], x[bj][1][2], x[bj][1][3])};
;                 continue; }
.LBB0_230:
	v_mov_b32_e32 v164, v175
	v_cvt_pk_fp8_f32 v164, v26, v27
	v_mov_b32_e32 v26, v175
	v_mov_b32_e32 v27, v175
	v_cvt_pk_fp8_f32 v26, v22, v23
	v_cvt_pk_fp8_f32 v27, v18, v19
	v_mov_b32_e32 v165, v175
	v_cvt_pk_fp8_f32 v165, v30, v31
	v_cvt_pk_fp8_f32 v26, v24, v25 op_sel:[0,0,1]
	v_cvt_pk_fp8_f32 v27, v20, v21 op_sel:[0,0,1]
	v_ashrrev_i32_e32 v193, 31, v192
	v_lshlrev_b64 v[162:163], 9, v[192:193]
	v_cvt_pk_fp8_f32 v164, v28, v29 op_sel:[0,0,1]
	v_cvt_pk_fp8_f32 v165, v32, v33 op_sel:[0,0,1]
	v_lshl_add_u64 v[162:163], v[190:191], 0, v[162:163]
	global_store_dwordx2 v[162:163], v[26:27], off offset:32
	v_mov_b64_e32 v[18:19], v[34:35]
	v_mov_b64_e32 v[22:23], v[38:39]
	v_mov_b64_e32 v[30:31], v[42:43]
	v_mov_b64_e32 v[26:27], v[46:47]
	s_and_b64 vcc, exec, s[6:7]
	v_mov_b64_e32 v[20:21], v[36:37]
	v_mov_b64_e32 v[24:25], v[40:41]
	v_mov_b64_e32 v[32:33], v[44:45]
	v_mov_b64_e32 v[28:29], v[48:49]
	global_store_dwordx2 v[162:163], v[164:165], off
	s_cbranch_vccnz .LBB0_232
	v_pk_mul_f32 v[18:19], v[48:49], v[48:49]
	v_pk_mul_f32 v[20:21], v[46:47], v[46:47]
	s_nop 0
	v_pk_mov_b32 v[22:23], v[20:21], v[18:19] op_sel:[1,0]
	v_mov_b32_e32 v21, v19
	v_pk_add_f32 v[18:19], v[22:23], v[20:21]
	v_pk_mul_f32 v[20:21], v[44:45], v[44:45]
	v_pk_mul_f32 v[22:23], v[42:43], v[42:43]
	v_pk_add_f32 v[18:19], v[18:19], v[18:19] op_sel:[0,1] op_sel_hi:[1,0]
	v_pk_mov_b32 v[24:25], v[22:23], v[20:21] op_sel:[1,0]
	v_mov_b32_e32 v23, v21
	v_pk_add_f32 v[20:21], v[24:25], v[22:23]
	v_mul_f32_e32 v22, v34, v34
	v_mul_f32_e32 v23, v35, v35
	v_pk_add_f32 v[20:21], v[20:21], v[20:21] op_sel:[0,1] op_sel_hi:[1,0]
	v_mov_b32_e32 v19, v22
	v_mov_b32_e32 v21, v23
	v_pk_add_f32 v[18:19], v[18:19], v[20:21]
	v_mul_f32_e32 v20, v39, v39
	v_mul_f32_e32 v22, v41, v41
	v_mul_f32_e32 v24, v36, v36
	v_mul_f32_e32 v25, v37, v37
	v_pk_fma_f32 v[20:21], v[38:39], v[38:39], v[20:21] op_sel_hi:[1,1,0]
	v_pk_fma_f32 v[22:23], v[40:41], v[40:41], v[22:23] op_sel_hi:[1,1,0]
	v_mov_b32_e32 v21, v24
	v_mov_b32_e32 v23, v25
	v_pk_add_f32 v[20:21], v[20:21], v[22:23]
	s_nop 0
	v_pk_add_f32 v[18:19], v[18:19], v[20:21]
	v_and_b32_e32 v20, 64, v212
	v_add_f32_e32 v18, v18, v19
	v_xor_b32_e32 v19, 16, v212
	v_add_u32_e32 v20, 64, v20
	v_cmp_lt_i32_e32 vcc, v19, v20
	s_nop 1
	v_cndmask_b32_e32 v19, v212, v19, vcc
	v_lshlrev_b32_e32 v19, 2, v19
	ds_bpermute_b32 v19, v19, v18
	s_waitcnt lgkmcnt(0)
	v_add_f32_e32 v18, v18, v19
	v_xor_b32_e32 v19, 32, v212
	v_cmp_lt_i32_e32 vcc, v19, v20
	s_nop 1
	v_cndmask_b32_e32 v19, v212, v19, vcc
	v_lshlrev_b32_e32 v19, 2, v19
	ds_bpermute_b32 v19, v19, v18
	s_waitcnt lgkmcnt(0)
	v_add_f32_e32 v18, v18, v19
	v_fmamk_f32 v18, v18, 0x3c800000, v210
	v_mul_f32_e32 v19, 0x4f800000, v18
	v_cmp_gt_f32_e32 vcc, s28, v18
	s_nop 1
	v_cndmask_b32_e32 v18, v18, v19, vcc
	v_sqrt_f32_e32 v19, v18
	s_nop 0
	v_add_u32_e32 v20, -1, v19
	v_fma_f32 v21, -v20, v19, v18
	v_cmp_ge_f32_e64 s[6:7], 0, v21
	v_add_u32_e32 v21, 1, v19
	s_nop 0
	v_cndmask_b32_e64 v20, v19, v20, s[6:7]
	v_fma_f32 v19, -v21, v19, v18
	v_cmp_lt_f32_e64 s[6:7], 0, v19
	s_nop 1
	v_cndmask_b32_e64 v19, v20, v21, s[6:7]
	v_mul_f32_e32 v20, 0x37800000, v19
	v_cndmask_b32_e32 v19, v19, v20, vcc
	v_cmp_class_f32_e32 vcc, v18, v211
	s_nop 1
	v_cndmask_b32_e32 v18, v19, v18, vcc
	v_div_scale_f32 v19, s[0:1], v18, v18, s29
	v_rcp_f32_e32 v20, v19
	s_nop 0
	v_fma_f32 v21, -v19, v20, 1.0
	v_fmac_f32_e32 v20, v21, v20
	v_div_scale_f32 v21, vcc, s29, v18, s29
	v_mul_f32_e32 v22, v21, v20
	v_fma_f32 v23, -v19, v22, v21
	v_fmac_f32_e32 v22, v23, v20
	v_fma_f32 v19, -v19, v22, v21
	v_div_fmas_f32 v19, v19, v20, v22
	v_div_fixup_f32 v18, v19, v18, s29
	v_pk_mul_f32 v[20:21], v[46:47], v[18:19] op_sel_hi:[1,0]
	v_pk_mul_f32 v[22:23], v[48:49], v[18:19] op_sel_hi:[1,0]
	s_nop 0
	v_pk_mul_f32 v[26:27], v[14:15], v[20:21]
	v_pk_mul_f32 v[28:29], v[16:17], v[22:23]
	v_pk_mul_f32 v[14:15], v[42:43], v[18:19] op_sel_hi:[1,0]
	v_pk_mul_f32 v[16:17], v[44:45], v[18:19] op_sel_hi:[1,0]
	v_pk_mul_f32 v[30:31], v[10:11], v[14:15]
	v_pk_mul_f32 v[32:33], v[12:13], v[16:17]
	v_pk_mul_f32 v[10:11], v[38:39], v[18:19] op_sel_hi:[1,0]
	v_pk_mul_f32 v[12:13], v[40:41], v[18:19] op_sel_hi:[1,0]
	v_pk_mul_f32 v[22:23], v[6:7], v[10:11]
	v_pk_mul_f32 v[24:25], v[8:9], v[12:13]
	v_pk_mul_f32 v[6:7], v[34:35], v[18:19] op_sel_hi:[1,0]
	v_pk_mul_f32 v[8:9], v[36:37], v[18:19] op_sel_hi:[1,0]
	v_pk_mul_f32 v[18:19], v[2:3], v[6:7]
	v_pk_mul_f32 v[20:21], v[4:5], v[8:9]

; __device__ __forceinline__ unsigned cvt_pk_bf16(float lo, float hi) { unsigned r; asm volatile("v_cvt_pk_bf16_f32 %0, %1, %2" : "=v"(r) : "v"(lo), "v"(hi)); return r; }
; template <bool F8OUT = false> __device__ __forceinline__ void head_tile_store(const f32x4 (&acc)[2][2][4][2], bf16_t* obase  , int opitch, const float* gain, float scale, const f32x2e* rope, int row0, int fq) {
;     ...
;             if (gain) {
;                 float ss = 0.f;
; #pragma unroll
;                 for (int bj = 0; bj < 2; ++bj)
; #pragma unroll
;                     for (int n = 0; n < 2; ++n) ss += (x[bj][n][0] * x[bj][n][0] + x[bj][n][1] * x[bj][n][1]) + (x[bj][n][2] * x[bj][n][2] + x[bj][n][3] * x[bj][n][3]);
;                 ss += __shfl_xor(ss, 16); ss += __shfl_xor(ss, 32);
;                 const float r = scale / sqrtf(ss * (1.f / 64.f) + 1e-6f);
; #pragma unroll
;                 for (int bj = 0; bj < 2; ++bj)
; #pragma unroll
;                     for (int n = 0; n < 2; ++n) x[bj][n] = x[bj][n] * r * g[bj][n];
;             }
;     ...
;             bf16_t* rowp = obase + (size_t)row * opitch + 8 * fq;
; #pragma unroll
;             for (int bj = 0; bj < 2; ++bj) { u32x4 w; w.x = cvt_pk_bf16(x[bj][0][0], x[bj][0][1]); w.y = cvt_pk_bf16(x[bj][0][2], x[bj][0][3]); w.z = cvt_pk_bf16(x[bj][1][0], x[bj][1][1]); w.w = cvt_pk_bf16(x[bj][1][2], x[bj][1][3]);
;                 *(u32x4*)(rowp + 32 * bj) = w; }
.LBB0_244:
	s_lshl_b32 s0, s18, 7
	s_add_u32 s0, s90, s0
	s_addc_u32 s1, s91, 0
	v_ashrrev_i32_e32 v19, 31, v18
	v_lshl_add_u64 v[20:21], v[20:21], 1, s[0:1]
	v_lshlrev_b64 v[22:23], 10, v[18:19]
	v_lshl_add_u64 v[22:23], v[20:21], 0, v[22:23]
	v_cvt_pk_bf16_f32 v188, v164, v165
	v_cvt_pk_bf16_f32 v189, v30, v31
	v_cvt_pk_bf16_f32 v190, v186, v187
	v_cvt_pk_bf16_f32 v191, v32, v33
	global_store_dwordx4 v[22:23], v[188:191], off
	v_cvt_pk_bf16_f32 v28, v28, v29
	v_cvt_pk_bf16_f32 v29, v24, v25
	v_cvt_pk_bf16_f32 v30, v162, v163
	v_cvt_pk_bf16_f32 v31, v26, v27
	global_store_dwordx4 v[22:23], v[28:31], off offset:64
	s_and_b64 vcc, exec, s[4:5]
	v_mov_b32_e32 v27, v133
	v_mov_b32_e32 v26, v132
	v_mov_b32_e32 v31, v131
	v_mov_b32_e32 v30, v130
	v_mov_b32_e32 v25, v137
	v_mov_b32_e32 v24, v136
	v_mov_b32_e32 v29, v135
	v_mov_b32_e32 v28, v134
	v_mov_b32_e32 v163, v141
	v_mov_b32_e32 v162, v140
	v_mov_b32_e32 v187, v139
	v_mov_b32_e32 v186, v138
	v_mov_b32_e32 v33, v145
	v_mov_b32_e32 v32, v144
	v_mov_b32_e32 v165, v143
	v_mov_b32_e32 v164, v142
	s_cbranch_vccnz .LBB0_246
	v_pk_mul_f32 v[24:25], v[144:145], v[144:145]
	v_pk_mul_f32 v[26:27], v[142:143], v[142:143]
	s_nop 0
	v_pk_mov_b32 v[28:29], v[26:27], v[24:25] op_sel:[1,0]
	v_mov_b32_e32 v27, v25
	v_pk_add_f32 v[24:25], v[28:29], v[26:27]
	v_pk_mul_f32 v[26:27], v[140:141], v[140:141]
	v_pk_mul_f32 v[28:29], v[138:139], v[138:139]
	v_pk_add_f32 v[24:25], v[24:25], v[24:25] op_sel:[0,1] op_sel_hi:[1,0]
	v_pk_mov_b32 v[30:31], v[28:29], v[26:27] op_sel:[1,0]
	v_mov_b32_e32 v29, v27
	v_pk_add_f32 v[26:27], v[30:31], v[28:29]
	v_mul_f32_e32 v28, v130, v130
	v_mul_f32_e32 v29, v131, v131
	v_pk_add_f32 v[26:27], v[26:27], v[26:27] op_sel:[0,1] op_sel_hi:[1,0]
	v_mov_b32_e32 v25, v28
	v_mov_b32_e32 v27, v29
	v_pk_add_f32 v[24:25], v[24:25], v[26:27]
	v_mul_f32_e32 v26, v135, v135
	v_mul_f32_e32 v28, v137, v137
	v_mul_f32_e32 v30, v132, v132
	v_mul_f32_e32 v31, v133, v133
	v_pk_fma_f32 v[26:27], v[134:135], v[134:135], v[26:27] op_sel_hi:[1,1,0]
	v_pk_fma_f32 v[28:29], v[136:137], v[136:137], v[28:29] op_sel_hi:[1,1,0]
	v_mov_b32_e32 v27, v30
	v_mov_b32_e32 v29, v31
	v_pk_add_f32 v[26:27], v[26:27], v[28:29]
	s_nop 0
	v_pk_add_f32 v[24:25], v[24:25], v[26:27]
	v_and_b32_e32 v26, 64, v212
	v_add_f32_e32 v24, v24, v25
	v_xor_b32_e32 v25, 16, v212
	v_add_u32_e32 v26, 64, v26
	v_cmp_lt_i32_e32 vcc, v25, v26
	s_nop 1
	v_cndmask_b32_e32 v25, v212, v25, vcc
	v_lshlrev_b32_e32 v25, 2, v25
	ds_bpermute_b32 v25, v25, v24
	s_waitcnt lgkmcnt(0)
	v_add_f32_e32 v24, v24, v25
	v_xor_b32_e32 v25, 32, v212
	v_cmp_lt_i32_e32 vcc, v25, v26
	s_nop 1
	v_cndmask_b32_e32 v25, v212, v25, vcc
	v_lshlrev_b32_e32 v25, 2, v25
	ds_bpermute_b32 v25, v25, v24
	s_waitcnt lgkmcnt(0)
	v_add_f32_e32 v24, v24, v25
	v_fmamk_f32 v24, v24, 0x3c800000, v210
	v_mul_f32_e32 v25, 0x4f800000, v24
	v_cmp_gt_f32_e32 vcc, s28, v24
	s_nop 1
	v_cndmask_b32_e32 v24, v24, v25, vcc
	v_sqrt_f32_e32 v25, v24
	s_nop 0
	v_add_u32_e32 v26, -1, v25
	v_fma_f32 v27, -v26, v25, v24
	v_cmp_ge_f32_e64 s[6:7], 0, v27
	v_add_u32_e32 v27, 1, v25
	s_nop 0
	v_cndmask_b32_e64 v26, v25, v26, s[6:7]
	v_fma_f32 v25, -v27, v25, v24
	v_cmp_lt_f32_e64 s[6:7], 0, v25
	s_nop 1
	v_cndmask_b32_e64 v25, v26, v27, s[6:7]
	v_mul_f32_e32 v26, 0x37800000, v25
	v_cndmask_b32_e32 v25, v25, v26, vcc
	v_cmp_class_f32_e32 vcc, v24, v211
	s_nop 1
	v_cndmask_b32_e32 v24, v25, v24, vcc
	v_div_scale_f32 v25, s[0:1], v24, v24, 1.0
	v_rcp_f32_e32 v26, v25
	s_nop 0
	v_fma_f32 v27, -v25, v26, 1.0
	v_fmac_f32_e32 v26, v27, v26
	v_div_scale_f32 v27, vcc, 1.0, v24, 1.0
	v_mul_f32_e32 v28, v27, v26
	v_fma_f32 v29, -v25, v28, v27
	v_fmac_f32_e32 v28, v29, v26
	v_fma_f32 v25, -v25, v28, v27
	v_div_fmas_f32 v25, v25, v26, v28
	v_div_fixup_f32 v26, v25, v24, 1.0
	v_pk_mul_f32 v[24:25], v[142:143], v[26:27] op_sel_hi:[1,0]
	v_pk_mul_f32 v[28:29], v[144:145], v[26:27] op_sel_hi:[1,0]
	s_nop 0
	v_pk_mul_f32 v[164:165], v[14:15], v[24:25]
	v_pk_mul_f32 v[32:33], v[16:17], v[28:29]
	v_pk_mul_f32 v[24:25], v[138:139], v[26:27] op_sel_hi:[1,0]
	v_pk_mul_f32 v[28:29], v[140:141], v[26:27] op_sel_hi:[1,0]
	v_pk_mul_f32 v[186:187], v[6:7], v[24:25]
	v_pk_mul_f32 v[162:163], v[8:9], v[28:29]
	v_pk_mul_f32 v[28:29], v[134:135], v[26:27] op_sel_hi:[1,0]
	v_pk_mul_f32 v[24:25], v[136:137], v[26:27] op_sel_hi:[1,0]
	v_pk_mul_f32 v[30:31], v[130:131], v[26:27] op_sel_hi:[1,0]
	v_pk_mul_f32 v[26:27], v[132:133], v[26:27] op_sel_hi:[1,0]
	v_pk_mul_f32 v[24:25], v[12:13], v[24:25]
	v_pk_mul_f32 v[28:29], v[10:11], v[28:29]
	v_pk_mul_f32 v[26:27], v[4:5], v[26:27]
	v_pk_mul_f32 v[30:31], v[2:3], v[30:31]
; __device__ __forceinline__ unsigned cvt_pk_bf16(float lo, float hi) { unsigned r; asm volatile("v_cvt_pk_bf16_f32 %0, %1, %2" : "=v"(r) : "v"(lo), "v"(hi)); return r; }
; template <bool F8OUT = false> __device__ __forceinline__ void head_tile_store(const f32x4 (&acc)[2][2][4][2], bf16_t* obase  , int opitch, const float* gain, float scale, const f32x2e* rope, int row0, int fq) {
;     ...
;             if (gain) {
;                 float ss = 0.f;
; #pragma unroll
;                 for (int bj = 0; bj < 2; ++bj)
; #pragma unroll
;                     for (int n = 0; n < 2; ++n) ss += (x[bj][n][0] * x[bj][n][0] + x[bj][n][1] * x[bj][n][1]) + (x[bj][n][2] * x[bj][n][2] + x[bj][n][3] * x[bj][n][3]);
;                 ss += __shfl_xor(ss, 16); ss += __shfl_xor(ss, 32);
;                 const float r = scale / sqrtf(ss * (1.f / 64.f) + 1e-6f);
; #pragma unroll
;                 for (int bj = 0; bj < 2; ++bj)
; #pragma unroll
;                     for (int n = 0; n < 2; ++n) x[bj][n] = x[bj][n] * r * g[bj][n];
;             }
;     ...
;             bf16_t* rowp = obase + (size_t)row * opitch + 8 * fq;
; #pragma unroll
;             for (int bj = 0; bj < 2; ++bj) { u32x4 w; w.x = cvt_pk_bf16(x[bj][0][0], x[bj][0][1]); w.y = cvt_pk_bf16(x[bj][0][2], x[bj][0][3]); w.z = cvt_pk_bf16(x[bj][1][0], x[bj][1][1]); w.w = cvt_pk_bf16(x[bj][1][2], x[bj][1][3]);
;                 *(u32x4*)(rowp + 32 * bj) = w; }
.LBB0_246:
	v_cvt_pk_bf16_f32 v188, v164, v165
	v_cvt_pk_bf16_f32 v189, v32, v33
	v_add_co_u32_e32 v32, vcc, 0x4000, v22
	v_lshl_add_u64 v[192:193], v[22:23], 0, s[92:93]
	s_nop 0
	v_addc_co_u32_e32 v33, vcc, 0, v23, vcc
	v_cvt_pk_bf16_f32 v190, v186, v187
	v_cvt_pk_bf16_f32 v191, v162, v163
	global_store_dwordx4 v[32:33], v[188:191], off
	v_cvt_pk_bf16_f32 v28, v28, v29
	v_cvt_pk_bf16_f32 v29, v24, v25
	v_cvt_pk_bf16_f32 v30, v30, v31
	v_cvt_pk_bf16_f32 v31, v26, v27
	global_store_dwordx4 v[192:193], v[28:31], off offset:64
	s_and_b64 vcc, exec, s[4:5]
	v_mov_b32_e32 v27, v117
	v_mov_b32_e32 v26, v116
	v_mov_b32_e32 v31, v115
	v_mov_b32_e32 v30, v114
	v_mov_b32_e32 v25, v121
	v_mov_b32_e32 v24, v120
	v_mov_b32_e32 v29, v119
	v_mov_b32_e32 v28, v118
	v_mov_b32_e32 v163, v125
	v_mov_b32_e32 v162, v124
	v_mov_b32_e32 v187, v123
	v_mov_b32_e32 v186, v122
	v_mov_b32_e32 v33, v129
	v_mov_b32_e32 v32, v128
	v_mov_b32_e32 v165, v127
	v_mov_b32_e32 v164, v126
	s_cbranch_vccnz .LBB0_248
	v_pk_mul_f32 v[24:25], v[128:129], v[128:129]
	v_pk_mul_f32 v[26:27], v[126:127], v[126:127]
	s_nop 0
	v_pk_mov_b32 v[28:29], v[26:27], v[24:25] op_sel:[1,0]
	v_mov_b32_e32 v27, v25
	v_pk_add_f32 v[24:25], v[28:29], v[26:27]
	v_pk_mul_f32 v[26:27], v[124:125], v[124:125]
	v_pk_mul_f32 v[28:29], v[122:123], v[122:123]
	v_pk_add_f32 v[24:25], v[24:25], v[24:25] op_sel:[0,1] op_sel_hi:[1,0]
	v_pk_mov_b32 v[30:31], v[28:29], v[26:27] op_sel:[1,0]
	v_mov_b32_e32 v29, v27
	v_pk_add_f32 v[26:27], v[30:31], v[28:29]
	v_mul_f32_e32 v28, v114, v114
	v_mul_f32_e32 v29, v115, v115
	v_pk_add_f32 v[26:27], v[26:27], v[26:27] op_sel:[0,1] op_sel_hi:[1,0]
	v_mov_b32_e32 v25, v28
	v_mov_b32_e32 v27, v29
	v_pk_add_f32 v[24:25], v[24:25], v[26:27]
	v_mul_f32_e32 v26, v119, v119
	v_mul_f32_e32 v28, v121, v121
	v_mul_f32_e32 v30, v116, v116
	v_mul_f32_e32 v31, v117, v117
	v_pk_fma_f32 v[26:27], v[118:119], v[118:119], v[26:27] op_sel_hi:[1,1,0]
	v_pk_fma_f32 v[28:29], v[120:121], v[120:121], v[28:29] op_sel_hi:[1,1,0]
	v_mov_b32_e32 v27, v30
	v_mov_b32_e32 v29, v31
	v_pk_add_f32 v[26:27], v[26:27], v[28:29]
	s_nop 0
	v_pk_add_f32 v[24:25], v[24:25], v[26:27]
	v_and_b32_e32 v26, 64, v212
	v_add_f32_e32 v24, v24, v25
	v_xor_b32_e32 v25, 16, v212
	v_add_u32_e32 v26, 64, v26
	v_cmp_lt_i32_e32 vcc, v25, v26
	s_nop 1
	v_cndmask_b32_e32 v25, v212, v25, vcc
	v_lshlrev_b32_e32 v25, 2, v25
	ds_bpermute_b32 v25, v25, v24
	s_waitcnt lgkmcnt(0)
	v_add_f32_e32 v24, v24, v25
	v_xor_b32_e32 v25, 32, v212
	v_cmp_lt_i32_e32 vcc, v25, v26
	s_nop 1
	v_cndmask_b32_e32 v25, v212, v25, vcc
	v_lshlrev_b32_e32 v25, 2, v25
	ds_bpermute_b32 v25, v25, v24
	s_waitcnt lgkmcnt(0)
	v_add_f32_e32 v24, v24, v25
	v_fmamk_f32 v24, v24, 0x3c800000, v210
	v_mul_f32_e32 v25, 0x4f800000, v24
	v_cmp_gt_f32_e32 vcc, s28, v24
	s_nop 1
	v_cndmask_b32_e32 v24, v24, v25, vcc
	v_sqrt_f32_e32 v25, v24
	s_nop 0
	v_add_u32_e32 v26, -1, v25
	v_fma_f32 v27, -v26, v25, v24
	v_cmp_ge_f32_e64 s[6:7], 0, v27
	v_add_u32_e32 v27, 1, v25
	s_nop 0
	v_cndmask_b32_e64 v26, v25, v26, s[6:7]
	v_fma_f32 v25, -v27, v25, v24
	v_cmp_lt_f32_e64 s[6:7], 0, v25
	s_nop 1
	v_cndmask_b32_e64 v25, v26, v27, s[6:7]
	v_mul_f32_e32 v26, 0x37800000, v25
	v_cndmask_b32_e32 v25, v25, v26, vcc
	v_cmp_class_f32_e32 vcc, v24, v211
	s_nop 1
	v_cndmask_b32_e32 v24, v25, v24, vcc
	v_div_scale_f32 v25, s[0:1], v24, v24, 1.0
	v_rcp_f32_e32 v26, v25
	s_nop 0
	v_fma_f32 v27, -v25, v26, 1.0
	v_fmac_f32_e32 v26, v27, v26
	v_div_scale_f32 v27, vcc, 1.0, v24, 1.0
	v_mul_f32_e32 v28, v27, v26
	v_fma_f32 v29, -v25, v28, v27
	v_fmac_f32_e32 v28, v29, v26
	v_fma_f32 v25, -v25, v28, v27
	v_div_fmas_f32 v25, v25, v26, v28
	v_div_fixup_f32 v26, v25, v24, 1.0
	v_pk_mul_f32 v[24:25], v[126:127], v[26:27] op_sel_hi:[1,0]
	v_pk_mul_f32 v[28:29], v[128:129], v[26:27] op_sel_hi:[1,0]
	s_nop 0
	v_pk_mul_f32 v[164:165], v[14:15], v[24:25]
	v_pk_mul_f32 v[32:33], v[16:17], v[28:29]
	v_pk_mul_f32 v[24:25], v[122:123], v[26:27] op_sel_hi:[1,0]
	v_pk_mul_f32 v[28:29], v[124:125], v[26:27] op_sel_hi:[1,0]
	v_pk_mul_f32 v[186:187], v[6:7], v[24:25]
	v_pk_mul_f32 v[162:163], v[8:9], v[28:29]
	v_pk_mul_f32 v[28:29], v[118:119], v[26:27] op_sel_hi:[1,0]
	v_pk_mul_f32 v[24:25], v[120:121], v[26:27] op_sel_hi:[1,0]
	v_pk_mul_f32 v[30:31], v[114:115], v[26:27] op_sel_hi:[1,0]
	v_pk_mul_f32 v[26:27], v[116:117], v[26:27] op_sel_hi:[1,0]
	v_pk_mul_f32 v[24:25], v[12:13], v[24:25]
	v_pk_mul_f32 v[28:29], v[10:11], v[28:29]
	v_pk_mul_f32 v[26:27], v[4:5], v[26:27]
	v_pk_mul_f32 v[30:31], v[2:3], v[30:31]
; __device__ __forceinline__ unsigned cvt_pk_bf16(float lo, float hi) { unsigned r; asm volatile("v_cvt_pk_bf16_f32 %0, %1, %2" : "=v"(r) : "v"(lo), "v"(hi)); return r; }
; template <bool F8OUT = false> __device__ __forceinline__ void head_tile_store(const f32x4 (&acc)[2][2][4][2], bf16_t* obase  , int opitch, const float* gain, float scale, const f32x2e* rope, int row0, int fq) {
;     ...
;             if (gain) {
;                 float ss = 0.f;
; #pragma unroll
;                 for (int bj = 0; bj < 2; ++bj)
; #pragma unroll
;                     for (int n = 0; n < 2; ++n) ss += (x[bj][n][0] * x[bj][n][0] + x[bj][n][1] * x[bj][n][1]) + (x[bj][n][2] * x[bj][n][2] + x[bj][n][3] * x[bj][n][3]);
;                 ss += __shfl_xor(ss, 16); ss += __shfl_xor(ss, 32);
;                 const float r = scale / sqrtf(ss * (1.f / 64.f) + 1e-6f);
; #pragma unroll
;                 for (int bj = 0; bj < 2; ++bj)
; #pragma unroll
;                     for (int n = 0; n < 2; ++n) x[bj][n] = x[bj][n] * r * g[bj][n];
;             }
;     ...
;             bf16_t* rowp = obase + (size_t)row * opitch + 8 * fq;
; #pragma unroll
;             for (int bj = 0; bj < 2; ++bj) { u32x4 w; w.x = cvt_pk_bf16(x[bj][0][0], x[bj][0][1]); w.y = cvt_pk_bf16(x[bj][0][2], x[bj][0][3]); w.z = cvt_pk_bf16(x[bj][1][0], x[bj][1][1]); w.w = cvt_pk_bf16(x[bj][1][2], x[bj][1][3]);
;                 *(u32x4*)(rowp + 32 * bj) = w; }
.LBB0_248:
	s_mov_b64 s[0:1], 0x8000
	v_lshl_add_u64 v[192:193], v[22:23], 0, s[0:1]
	v_add_co_u32_e32 v22, vcc, 0x8000, v22
	v_cvt_pk_bf16_f32 v188, v164, v165
	v_cvt_pk_bf16_f32 v189, v32, v33
	v_cvt_pk_bf16_f32 v190, v186, v187
	v_cvt_pk_bf16_f32 v191, v162, v163
	s_nop 1
	v_addc_co_u32_e32 v23, vcc, 0, v23, vcc
	global_store_dwordx4 v[22:23], v[188:191], off
	v_cvt_pk_bf16_f32 v22, v28, v29
	v_cvt_pk_bf16_f32 v23, v24, v25
	v_cvt_pk_bf16_f32 v24, v30, v31
	v_cvt_pk_bf16_f32 v25, v26, v27
	global_store_dwordx4 v[192:193], v[22:25], off offset:64
	s_and_b64 vcc, exec, s[4:5]
	v_mov_b32_e32 v27, v101
	v_mov_b32_e32 v26, v100
	v_mov_b32_e32 v31, v99
	v_mov_b32_e32 v30, v98
	v_mov_b32_e32 v25, v105
	v_mov_b32_e32 v24, v104
	v_mov_b32_e32 v29, v103
	v_mov_b32_e32 v28, v102
	v_mov_b32_e32 v163, v109
	v_mov_b32_e32 v162, v108
	v_mov_b32_e32 v187, v107
	v_mov_b32_e32 v186, v106
	v_mov_b32_e32 v33, v113
	v_mov_b32_e32 v32, v112
	v_mov_b32_e32 v165, v111
	v_mov_b32_e32 v164, v110
	s_cbranch_vccnz .LBB0_250
	v_pk_mul_f32 v[22:23], v[112:113], v[112:113]
	v_pk_mul_f32 v[24:25], v[110:111], v[110:111]
	s_nop 0
	v_pk_mov_b32 v[26:27], v[24:25], v[22:23] op_sel:[1,0]
	v_mov_b32_e32 v25, v23
	v_pk_add_f32 v[22:23], v[26:27], v[24:25]
	v_pk_mul_f32 v[24:25], v[108:109], v[108:109]
	v_pk_mul_f32 v[26:27], v[106:107], v[106:107]
	v_pk_add_f32 v[22:23], v[22:23], v[22:23] op_sel:[0,1] op_sel_hi:[1,0]
	v_pk_mov_b32 v[28:29], v[26:27], v[24:25] op_sel:[1,0]
	v_mov_b32_e32 v27, v25
	v_pk_add_f32 v[24:25], v[28:29], v[26:27]
	v_mul_f32_e32 v26, v98, v98
	v_mul_f32_e32 v27, v99, v99
	v_pk_add_f32 v[24:25], v[24:25], v[24:25] op_sel:[0,1] op_sel_hi:[1,0]
	v_mov_b32_e32 v23, v26
	v_mov_b32_e32 v25, v27
	v_pk_add_f32 v[22:23], v[22:23], v[24:25]
	v_mul_f32_e32 v24, v103, v103
	v_mul_f32_e32 v26, v105, v105
	v_mul_f32_e32 v28, v100, v100
	v_mul_f32_e32 v29, v101, v101
	v_pk_fma_f32 v[24:25], v[102:103], v[102:103], v[24:25] op_sel_hi:[1,1,0]
	v_pk_fma_f32 v[26:27], v[104:105], v[104:105], v[26:27] op_sel_hi:[1,1,0]
	v_mov_b32_e32 v25, v28
	v_mov_b32_e32 v27, v29
	v_pk_add_f32 v[24:25], v[24:25], v[26:27]
	s_nop 0
	v_pk_add_f32 v[22:23], v[22:23], v[24:25]
	v_and_b32_e32 v24, 64, v212
	v_add_f32_e32 v22, v22, v23
	v_xor_b32_e32 v23, 16, v212
	v_add_u32_e32 v24, 64, v24
	v_cmp_lt_i32_e32 vcc, v23, v24
	s_nop 1
	v_cndmask_b32_e32 v23, v212, v23, vcc
	v_lshlrev_b32_e32 v23, 2, v23
	ds_bpermute_b32 v23, v23, v22
	s_waitcnt lgkmcnt(0)
	v_add_f32_e32 v22, v22, v23
	v_xor_b32_e32 v23, 32, v212
	v_cmp_lt_i32_e32 vcc, v23, v24
	s_nop 1
	v_cndmask_b32_e32 v23, v212, v23, vcc
	v_lshlrev_b32_e32 v23, 2, v23
	ds_bpermute_b32 v23, v23, v22
	s_waitcnt lgkmcnt(0)
	v_add_f32_e32 v22, v22, v23
	v_fmamk_f32 v22, v22, 0x3c800000, v210
	v_mul_f32_e32 v23, 0x4f800000, v22
	v_cmp_gt_f32_e32 vcc, s28, v22
	s_nop 1
	v_cndmask_b32_e32 v22, v22, v23, vcc
	v_sqrt_f32_e32 v23, v22
	s_nop 0
	v_add_u32_e32 v24, -1, v23
	v_fma_f32 v25, -v24, v23, v22
	v_cmp_ge_f32_e64 s[6:7], 0, v25
	v_add_u32_e32 v25, 1, v23
	s_nop 0
	v_cndmask_b32_e64 v24, v23, v24, s[6:7]
	v_fma_f32 v23, -v25, v23, v22
	v_cmp_lt_f32_e64 s[6:7], 0, v23
	s_nop 1
	v_cndmask_b32_e64 v23, v24, v25, s[6:7]
	v_mul_f32_e32 v24, 0x37800000, v23
	v_cndmask_b32_e32 v23, v23, v24, vcc
	v_cmp_class_f32_e32 vcc, v22, v211
	s_nop 1
	v_cndmask_b32_e32 v22, v23, v22, vcc
	v_div_scale_f32 v23, s[0:1], v22, v22, 1.0
	v_rcp_f32_e32 v24, v23
	s_nop 0
	v_fma_f32 v25, -v23, v24, 1.0
	v_fmac_f32_e32 v24, v25, v24
	v_div_scale_f32 v25, vcc, 1.0, v22, 1.0
	v_mul_f32_e32 v26, v25, v24
	v_fma_f32 v27, -v23, v26, v25
	v_fmac_f32_e32 v26, v27, v24
	v_fma_f32 v23, -v23, v26, v25
	v_div_fmas_f32 v23, v23, v24, v26
	v_div_fixup_f32 v22, v23, v22, 1.0
	v_pk_mul_f32 v[24:25], v[110:111], v[22:23] op_sel_hi:[1,0]
	v_pk_mul_f32 v[26:27], v[112:113], v[22:23] op_sel_hi:[1,0]
	s_nop 0
	v_pk_mul_f32 v[164:165], v[14:15], v[24:25]
	v_pk_mul_f32 v[32:33], v[16:17], v[26:27]
	v_pk_mul_f32 v[24:25], v[106:107], v[22:23] op_sel_hi:[1,0]
	v_pk_mul_f32 v[26:27], v[108:109], v[22:23] op_sel_hi:[1,0]
	v_pk_mul_f32 v[186:187], v[6:7], v[24:25]
	v_pk_mul_f32 v[162:163], v[8:9], v[26:27]
	v_pk_mul_f32 v[26:27], v[102:103], v[22:23] op_sel_hi:[1,0]
	v_pk_mul_f32 v[24:25], v[104:105], v[22:23] op_sel_hi:[1,0]
	v_pk_mul_f32 v[30:31], v[98:99], v[22:23] op_sel_hi:[1,0]
	v_pk_mul_f32 v[22:23], v[100:101], v[22:23] op_sel_hi:[1,0]
	v_pk_mul_f32 v[24:25], v[12:13], v[24:25]
	v_pk_mul_f32 v[28:29], v[10:11], v[26:27]
	v_pk_mul_f32 v[26:27], v[4:5], v[22:23]
	v_pk_mul_f32 v[30:31], v[2:3], v[30:31]
; __device__ __forceinline__ unsigned cvt_pk_bf16(float lo, float hi) { unsigned r; asm volatile("v_cvt_pk_bf16_f32 %0, %1, %2" : "=v"(r) : "v"(lo), "v"(hi)); return r; }
; template <bool F8OUT = false> __device__ __forceinline__ void head_tile_store(const f32x4 (&acc)[2][2][4][2], bf16_t* obase  , int opitch, const float* gain, float scale, const f32x2e* rope, int row0, int fq) {
;     ...
;             if (gain) {
;                 float ss = 0.f;
; #pragma unroll
;                 for (int bj = 0; bj < 2; ++bj)
; #pragma unroll
;                     for (int n = 0; n < 2; ++n) ss += (x[bj][n][0] * x[bj][n][0] + x[bj][n][1] * x[bj][n][1]) + (x[bj][n][2] * x[bj][n][2] + x[bj][n][3] * x[bj][n][3]);
;                 ss += __shfl_xor(ss, 16); ss += __shfl_xor(ss, 32);
;                 const float r = scale / sqrtf(ss * (1.f / 64.f) + 1e-6f);
; #pragma unroll
;                 for (int bj = 0; bj < 2; ++bj)
; #pragma unroll
;                     for (int n = 0; n < 2; ++n) x[bj][n] = x[bj][n] * r * g[bj][n];
;             }
;     ...
;             bf16_t* rowp = obase + (size_t)row * opitch + 8 * fq;
; #pragma unroll
;             for (int bj = 0; bj < 2; ++bj) { u32x4 w; w.x = cvt_pk_bf16(x[bj][0][0], x[bj][0][1]); w.y = cvt_pk_bf16(x[bj][0][2], x[bj][0][3]); w.z = cvt_pk_bf16(x[bj][1][0], x[bj][1][1]); w.w = cvt_pk_bf16(x[bj][1][2], x[bj][1][3]);
;                 *(u32x4*)(rowp + 32 * bj) = w; }
.LBB0_250:
	v_lshlrev_b64 v[22:23], 10, v[18:19]
	v_lshl_add_u64 v[22:23], v[20:21], 0, v[22:23]
	v_cvt_pk_bf16_f32 v188, v164, v165
	v_cvt_pk_bf16_f32 v189, v32, v33
	v_add_co_u32_e32 v32, vcc, 0xc000, v22
	v_lshl_add_u64 v[192:193], v[22:23], 0, s[34:35]
	s_nop 0
	v_addc_co_u32_e32 v33, vcc, 0, v23, vcc
	v_cvt_pk_bf16_f32 v190, v186, v187
	v_cvt_pk_bf16_f32 v191, v162, v163
	global_store_dwordx4 v[32:33], v[188:191], off
	v_cvt_pk_bf16_f32 v28, v28, v29
	v_cvt_pk_bf16_f32 v29, v24, v25
	v_cvt_pk_bf16_f32 v30, v30, v31
	v_cvt_pk_bf16_f32 v31, v26, v27
	global_store_dwordx4 v[192:193], v[28:31], off offset:64
	s_and_b64 vcc, exec, s[4:5]
	v_mov_b32_e32 v27, v85
	v_mov_b32_e32 v26, v84
	v_mov_b32_e32 v31, v83
	v_mov_b32_e32 v30, v82
	v_mov_b32_e32 v25, v89
	v_mov_b32_e32 v24, v88
	v_mov_b32_e32 v29, v87
	v_mov_b32_e32 v28, v86
	v_mov_b32_e32 v163, v93
	v_mov_b32_e32 v162, v92
	v_mov_b32_e32 v187, v91
	v_mov_b32_e32 v186, v90
	v_mov_b32_e32 v33, v97
	v_mov_b32_e32 v32, v96
	v_mov_b32_e32 v165, v95
	v_mov_b32_e32 v164, v94
	s_cbranch_vccnz .LBB0_252
	v_pk_mul_f32 v[24:25], v[96:97], v[96:97]
	v_pk_mul_f32 v[26:27], v[94:95], v[94:95]
	s_nop 0
	v_pk_mov_b32 v[28:29], v[26:27], v[24:25] op_sel:[1,0]
	v_mov_b32_e32 v27, v25
	v_pk_add_f32 v[24:25], v[28:29], v[26:27]
	v_pk_mul_f32 v[26:27], v[92:93], v[92:93]
	v_pk_mul_f32 v[28:29], v[90:91], v[90:91]
	v_pk_add_f32 v[24:25], v[24:25], v[24:25] op_sel:[0,1] op_sel_hi:[1,0]
	v_pk_mov_b32 v[30:31], v[28:29], v[26:27] op_sel:[1,0]
	v_mov_b32_e32 v29, v27
	v_pk_add_f32 v[26:27], v[30:31], v[28:29]
	v_mul_f32_e32 v28, v82, v82
	v_mul_f32_e32 v29, v83, v83
	v_pk_add_f32 v[26:27], v[26:27], v[26:27] op_sel:[0,1] op_sel_hi:[1,0]
	v_mov_b32_e32 v25, v28
	v_mov_b32_e32 v27, v29
	v_pk_add_f32 v[24:25], v[24:25], v[26:27]
	v_mul_f32_e32 v26, v87, v87
	v_mul_f32_e32 v28, v89, v89
	v_mul_f32_e32 v30, v84, v84
	v_mul_f32_e32 v31, v85, v85
	v_pk_fma_f32 v[26:27], v[86:87], v[86:87], v[26:27] op_sel_hi:[1,1,0]
	v_pk_fma_f32 v[28:29], v[88:89], v[88:89], v[28:29] op_sel_hi:[1,1,0]
	v_mov_b32_e32 v27, v30
	v_mov_b32_e32 v29, v31
	v_pk_add_f32 v[26:27], v[26:27], v[28:29]
	s_nop 0
	v_pk_add_f32 v[24:25], v[24:25], v[26:27]
	v_and_b32_e32 v26, 64, v212
	v_add_f32_e32 v24, v24, v25
	v_xor_b32_e32 v25, 16, v212
	v_add_u32_e32 v26, 64, v26
	v_cmp_lt_i32_e32 vcc, v25, v26
	s_nop 1
	v_cndmask_b32_e32 v25, v212, v25, vcc
	v_lshlrev_b32_e32 v25, 2, v25
	ds_bpermute_b32 v25, v25, v24
	s_waitcnt lgkmcnt(0)
	v_add_f32_e32 v24, v24, v25
	v_xor_b32_e32 v25, 32, v212
	v_cmp_lt_i32_e32 vcc, v25, v26
	s_nop 1
	v_cndmask_b32_e32 v25, v212, v25, vcc
	v_lshlrev_b32_e32 v25, 2, v25
	ds_bpermute_b32 v25, v25, v24
	s_waitcnt lgkmcnt(0)
	v_add_f32_e32 v24, v24, v25
	v_fmamk_f32 v24, v24, 0x3c800000, v210
	v_mul_f32_e32 v25, 0x4f800000, v24
	v_cmp_gt_f32_e32 vcc, s28, v24
	s_nop 1
	v_cndmask_b32_e32 v24, v24, v25, vcc
	v_sqrt_f32_e32 v25, v24
	s_nop 0
	v_add_u32_e32 v26, -1, v25
	v_fma_f32 v27, -v26, v25, v24
	v_cmp_ge_f32_e64 s[6:7], 0, v27
	v_add_u32_e32 v27, 1, v25
	s_nop 0
	v_cndmask_b32_e64 v26, v25, v26, s[6:7]
	v_fma_f32 v25, -v27, v25, v24
	v_cmp_lt_f32_e64 s[6:7], 0, v25
	s_nop 1
	v_cndmask_b32_e64 v25, v26, v27, s[6:7]
	v_mul_f32_e32 v26, 0x37800000, v25
	v_cndmask_b32_e32 v25, v25, v26, vcc
	v_cmp_class_f32_e32 vcc, v24, v211
	s_nop 1
	v_cndmask_b32_e32 v24, v25, v24, vcc
	v_div_scale_f32 v25, s[0:1], v24, v24, 1.0
	v_rcp_f32_e32 v26, v25
	s_nop 0
	v_fma_f32 v27, -v25, v26, 1.0
	v_fmac_f32_e32 v26, v27, v26
	v_div_scale_f32 v27, vcc, 1.0, v24, 1.0
	v_mul_f32_e32 v28, v27, v26
	v_fma_f32 v29, -v25, v28, v27
	v_fmac_f32_e32 v28, v29, v26
	v_fma_f32 v25, -v25, v28, v27
	v_div_fmas_f32 v25, v25, v26, v28
	v_div_fixup_f32 v26, v25, v24, 1.0
	v_pk_mul_f32 v[24:25], v[94:95], v[26:27] op_sel_hi:[1,0]
	v_pk_mul_f32 v[28:29], v[96:97], v[26:27] op_sel_hi:[1,0]
	s_nop 0
	v_pk_mul_f32 v[164:165], v[14:15], v[24:25]
	v_pk_mul_f32 v[32:33], v[16:17], v[28:29]
	v_pk_mul_f32 v[24:25], v[90:91], v[26:27] op_sel_hi:[1,0]
	v_pk_mul_f32 v[28:29], v[92:93], v[26:27] op_sel_hi:[1,0]
	v_pk_mul_f32 v[186:187], v[6:7], v[24:25]
	v_pk_mul_f32 v[162:163], v[8:9], v[28:29]
	v_pk_mul_f32 v[28:29], v[86:87], v[26:27] op_sel_hi:[1,0]
	v_pk_mul_f32 v[24:25], v[88:89], v[26:27] op_sel_hi:[1,0]
	v_pk_mul_f32 v[30:31], v[82:83], v[26:27] op_sel_hi:[1,0]
	v_pk_mul_f32 v[26:27], v[84:85], v[26:27] op_sel_hi:[1,0]
	v_pk_mul_f32 v[24:25], v[12:13], v[24:25]
	v_pk_mul_f32 v[28:29], v[10:11], v[28:29]
	v_pk_mul_f32 v[26:27], v[4:5], v[26:27]
	v_pk_mul_f32 v[30:31], v[2:3], v[30:31]
; __device__ __forceinline__ unsigned cvt_pk_bf16(float lo, float hi) { unsigned r; asm volatile("v_cvt_pk_bf16_f32 %0, %1, %2" : "=v"(r) : "v"(lo), "v"(hi)); return r; }
; template <bool F8OUT = false> __device__ __forceinline__ void head_tile_store(const f32x4 (&acc)[2][2][4][2], bf16_t* obase  , int opitch, const float* gain, float scale, const f32x2e* rope, int row0, int fq) {
;     ...
;             if (gain) {
;                 float ss = 0.f;
; #pragma unroll
;                 for (int bj = 0; bj < 2; ++bj)
; #pragma unroll
;                     for (int n = 0; n < 2; ++n) ss += (x[bj][n][0] * x[bj][n][0] + x[bj][n][1] * x[bj][n][1]) + (x[bj][n][2] * x[bj][n][2] + x[bj][n][3] * x[bj][n][3]);
;                 ss += __shfl_xor(ss, 16); ss += __shfl_xor(ss, 32);
;                 const float r = scale / sqrtf(ss * (1.f / 64.f) + 1e-6f);
; #pragma unroll
;                 for (int bj = 0; bj < 2; ++bj)
; #pragma unroll
;                     for (int n = 0; n < 2; ++n) x[bj][n] = x[bj][n] * r * g[bj][n];
;             }
;     ...
;             bf16_t* rowp = obase + (size_t)row * opitch + 8 * fq;
; #pragma unroll
;             for (int bj = 0; bj < 2; ++bj) { u32x4 w; w.x = cvt_pk_bf16(x[bj][0][0], x[bj][0][1]); w.y = cvt_pk_bf16(x[bj][0][2], x[bj][0][3]); w.z = cvt_pk_bf16(x[bj][1][0], x[bj][1][1]); w.w = cvt_pk_bf16(x[bj][1][2], x[bj][1][3]);
;                 *(u32x4*)(rowp + 32 * bj) = w; }
.LBB0_252:
	s_mov_b64 s[0:1], 0x20000
	v_lshl_add_u64 v[192:193], v[22:23], 0, s[0:1]
	v_add_co_u32_e32 v22, vcc, 0x20000, v22
	v_cvt_pk_bf16_f32 v188, v164, v165
	v_cvt_pk_bf16_f32 v189, v32, v33
	v_cvt_pk_bf16_f32 v190, v186, v187
	v_cvt_pk_bf16_f32 v191, v162, v163
	s_nop 1
	v_addc_co_u32_e32 v23, vcc, 0, v23, vcc
	global_store_dwordx4 v[22:23], v[188:191], off
	v_cvt_pk_bf16_f32 v22, v28, v29
	v_cvt_pk_bf16_f32 v23, v24, v25
	v_cvt_pk_bf16_f32 v24, v30, v31
	v_cvt_pk_bf16_f32 v25, v26, v27
	global_store_dwordx4 v[192:193], v[22:25], off offset:64
	s_and_b64 vcc, exec, s[4:5]
	v_mov_b32_e32 v27, v69
	v_mov_b32_e32 v26, v68
	v_mov_b32_e32 v31, v67
	v_mov_b32_e32 v30, v66
	v_mov_b32_e32 v25, v73
	v_mov_b32_e32 v24, v72
	v_mov_b32_e32 v29, v71
	v_mov_b32_e32 v28, v70
	v_mov_b32_e32 v163, v77
	v_mov_b32_e32 v162, v76
	v_mov_b32_e32 v187, v75
	v_mov_b32_e32 v186, v74
	v_mov_b32_e32 v33, v81
	v_mov_b32_e32 v32, v80
	v_mov_b32_e32 v165, v79
	v_mov_b32_e32 v164, v78
	s_cbranch_vccnz .LBB0_254
	v_pk_mul_f32 v[22:23], v[80:81], v[80:81]
	v_pk_mul_f32 v[24:25], v[78:79], v[78:79]
	s_nop 0
	v_pk_mov_b32 v[26:27], v[24:25], v[22:23] op_sel:[1,0]
	v_mov_b32_e32 v25, v23
	v_pk_add_f32 v[22:23], v[26:27], v[24:25]
	v_pk_mul_f32 v[24:25], v[76:77], v[76:77]
	v_pk_mul_f32 v[26:27], v[74:75], v[74:75]
	v_pk_add_f32 v[22:23], v[22:23], v[22:23] op_sel:[0,1] op_sel_hi:[1,0]
	v_pk_mov_b32 v[28:29], v[26:27], v[24:25] op_sel:[1,0]
	v_mov_b32_e32 v27, v25
	v_pk_add_f32 v[24:25], v[28:29], v[26:27]
	v_mul_f32_e32 v26, v66, v66
	v_mul_f32_e32 v27, v67, v67
	v_pk_add_f32 v[24:25], v[24:25], v[24:25] op_sel:[0,1] op_sel_hi:[1,0]
	v_mov_b32_e32 v23, v26
	v_mov_b32_e32 v25, v27
	v_pk_add_f32 v[22:23], v[22:23], v[24:25]
	v_mul_f32_e32 v24, v71, v71
	v_mul_f32_e32 v26, v73, v73
	v_mul_f32_e32 v28, v68, v68
	v_mul_f32_e32 v29, v69, v69
	v_pk_fma_f32 v[24:25], v[70:71], v[70:71], v[24:25] op_sel_hi:[1,1,0]
	v_pk_fma_f32 v[26:27], v[72:73], v[72:73], v[26:27] op_sel_hi:[1,1,0]
	v_mov_b32_e32 v25, v28
	v_mov_b32_e32 v27, v29
	v_pk_add_f32 v[24:25], v[24:25], v[26:27]
	s_nop 0
	v_pk_add_f32 v[22:23], v[22:23], v[24:25]
	v_and_b32_e32 v24, 64, v212
	v_add_f32_e32 v22, v22, v23
	v_xor_b32_e32 v23, 16, v212
	v_add_u32_e32 v24, 64, v24
	v_cmp_lt_i32_e32 vcc, v23, v24
	s_nop 1
	v_cndmask_b32_e32 v23, v212, v23, vcc
	v_lshlrev_b32_e32 v23, 2, v23
	ds_bpermute_b32 v23, v23, v22
	s_waitcnt lgkmcnt(0)
	v_add_f32_e32 v22, v22, v23
	v_xor_b32_e32 v23, 32, v212
	v_cmp_lt_i32_e32 vcc, v23, v24
	s_nop 1
	v_cndmask_b32_e32 v23, v212, v23, vcc
	v_lshlrev_b32_e32 v23, 2, v23
	ds_bpermute_b32 v23, v23, v22
	s_waitcnt lgkmcnt(0)
	v_add_f32_e32 v22, v22, v23
	v_fmamk_f32 v22, v22, 0x3c800000, v210
	v_mul_f32_e32 v23, 0x4f800000, v22
	v_cmp_gt_f32_e32 vcc, s28, v22
	s_nop 1
	v_cndmask_b32_e32 v22, v22, v23, vcc
	v_sqrt_f32_e32 v23, v22
	s_nop 0
	v_add_u32_e32 v24, -1, v23
	v_fma_f32 v25, -v24, v23, v22
	v_cmp_ge_f32_e64 s[6:7], 0, v25
	v_add_u32_e32 v25, 1, v23
	s_nop 0
	v_cndmask_b32_e64 v24, v23, v24, s[6:7]
	v_fma_f32 v23, -v25, v23, v22
	v_cmp_lt_f32_e64 s[6:7], 0, v23
	s_nop 1
	v_cndmask_b32_e64 v23, v24, v25, s[6:7]
	v_mul_f32_e32 v24, 0x37800000, v23
	v_cndmask_b32_e32 v23, v23, v24, vcc
	v_cmp_class_f32_e32 vcc, v22, v211
	s_nop 1
	v_cndmask_b32_e32 v22, v23, v22, vcc
	v_div_scale_f32 v23, s[0:1], v22, v22, 1.0
	v_rcp_f32_e32 v24, v23
	s_nop 0
	v_fma_f32 v25, -v23, v24, 1.0
	v_fmac_f32_e32 v24, v25, v24
	v_div_scale_f32 v25, vcc, 1.0, v22, 1.0
	v_mul_f32_e32 v26, v25, v24
	v_fma_f32 v27, -v23, v26, v25
	v_fmac_f32_e32 v26, v27, v24
	v_fma_f32 v23, -v23, v26, v25
	v_div_fmas_f32 v23, v23, v24, v26
	v_div_fixup_f32 v22, v23, v22, 1.0
	v_pk_mul_f32 v[24:25], v[78:79], v[22:23] op_sel_hi:[1,0]
	v_pk_mul_f32 v[26:27], v[80:81], v[22:23] op_sel_hi:[1,0]
	s_nop 0
	v_pk_mul_f32 v[164:165], v[14:15], v[24:25]
	v_pk_mul_f32 v[32:33], v[16:17], v[26:27]
	v_pk_mul_f32 v[24:25], v[74:75], v[22:23] op_sel_hi:[1,0]
	v_pk_mul_f32 v[26:27], v[76:77], v[22:23] op_sel_hi:[1,0]
	v_pk_mul_f32 v[186:187], v[6:7], v[24:25]
	v_pk_mul_f32 v[162:163], v[8:9], v[26:27]
	v_pk_mul_f32 v[26:27], v[70:71], v[22:23] op_sel_hi:[1,0]
	v_pk_mul_f32 v[24:25], v[72:73], v[22:23] op_sel_hi:[1,0]
	v_pk_mul_f32 v[30:31], v[66:67], v[22:23] op_sel_hi:[1,0]
	v_pk_mul_f32 v[22:23], v[68:69], v[22:23] op_sel_hi:[1,0]
	v_pk_mul_f32 v[24:25], v[12:13], v[24:25]
	v_pk_mul_f32 v[28:29], v[10:11], v[26:27]
	v_pk_mul_f32 v[26:27], v[4:5], v[22:23]
	v_pk_mul_f32 v[30:31], v[2:3], v[30:31]
; __device__ __forceinline__ unsigned cvt_pk_bf16(float lo, float hi) { unsigned r; asm volatile("v_cvt_pk_bf16_f32 %0, %1, %2" : "=v"(r) : "v"(lo), "v"(hi)); return r; }
; template <bool F8OUT = false> __device__ __forceinline__ void head_tile_store(const f32x4 (&acc)[2][2][4][2], bf16_t* obase  , int opitch, const float* gain, float scale, const f32x2e* rope, int row0, int fq) {
;     ...
;             if (gain) {
;                 float ss = 0.f;
; #pragma unroll
;                 for (int bj = 0; bj < 2; ++bj)
; #pragma unroll
;                     for (int n = 0; n < 2; ++n) ss += (x[bj][n][0] * x[bj][n][0] + x[bj][n][1] * x[bj][n][1]) + (x[bj][n][2] * x[bj][n][2] + x[bj][n][3] * x[bj][n][3]);
;                 ss += __shfl_xor(ss, 16); ss += __shfl_xor(ss, 32);
;                 const float r = scale / sqrtf(ss * (1.f / 64.f) + 1e-6f);
; #pragma unroll
;                 for (int bj = 0; bj < 2; ++bj)
; #pragma unroll
;                     for (int n = 0; n < 2; ++n) x[bj][n] = x[bj][n] * r * g[bj][n];
;             }
;     ...
;             bf16_t* rowp = obase + (size_t)row * opitch + 8 * fq;
; #pragma unroll
;             for (int bj = 0; bj < 2; ++bj) { u32x4 w; w.x = cvt_pk_bf16(x[bj][0][0], x[bj][0][1]); w.y = cvt_pk_bf16(x[bj][0][2], x[bj][0][3]); w.z = cvt_pk_bf16(x[bj][1][0], x[bj][1][1]); w.w = cvt_pk_bf16(x[bj][1][2], x[bj][1][3]);
;                 *(u32x4*)(rowp + 32 * bj) = w; }
.LBB0_254:
	v_lshlrev_b64 v[22:23], 10, v[18:19]
	v_lshl_add_u64 v[22:23], v[20:21], 0, v[22:23]
	v_cvt_pk_bf16_f32 v188, v164, v165
	v_cvt_pk_bf16_f32 v189, v32, v33
	v_add_co_u32_e32 v32, vcc, 0x24000, v22
	v_lshl_add_u64 v[192:193], v[22:23], 0, s[30:31]
	s_nop 0
	v_addc_co_u32_e32 v33, vcc, 0, v23, vcc
	v_cvt_pk_bf16_f32 v190, v186, v187
	v_cvt_pk_bf16_f32 v191, v162, v163
	global_store_dwordx4 v[32:33], v[188:191], off
	v_cvt_pk_bf16_f32 v28, v28, v29
	v_cvt_pk_bf16_f32 v29, v24, v25
	v_cvt_pk_bf16_f32 v30, v30, v31
	v_cvt_pk_bf16_f32 v31, v26, v27
	global_store_dwordx4 v[192:193], v[28:31], off offset:64
	s_and_b64 vcc, exec, s[4:5]
	v_mov_b32_e32 v27, v53
	v_mov_b32_e32 v26, v52
	v_mov_b32_e32 v31, v51
	v_mov_b32_e32 v30, v50
	v_mov_b32_e32 v25, v57
	v_mov_b32_e32 v24, v56
	v_mov_b32_e32 v29, v55
	v_mov_b32_e32 v28, v54
	v_mov_b32_e32 v163, v61
	v_mov_b32_e32 v162, v60
	v_mov_b32_e32 v187, v59
	v_mov_b32_e32 v186, v58
	v_mov_b32_e32 v33, v65
	v_mov_b32_e32 v32, v64
	v_mov_b32_e32 v165, v63
	v_mov_b32_e32 v164, v62
	s_cbranch_vccnz .LBB0_256
	v_pk_mul_f32 v[24:25], v[64:65], v[64:65]
	v_pk_mul_f32 v[26:27], v[62:63], v[62:63]
	s_nop 0
	v_pk_mov_b32 v[28:29], v[26:27], v[24:25] op_sel:[1,0]
	v_mov_b32_e32 v27, v25
	v_pk_add_f32 v[24:25], v[28:29], v[26:27]
	v_pk_mul_f32 v[26:27], v[60:61], v[60:61]
	v_pk_mul_f32 v[28:29], v[58:59], v[58:59]
	v_pk_add_f32 v[24:25], v[24:25], v[24:25] op_sel:[0,1] op_sel_hi:[1,0]
	v_pk_mov_b32 v[30:31], v[28:29], v[26:27] op_sel:[1,0]
	v_mov_b32_e32 v29, v27
	v_pk_add_f32 v[26:27], v[30:31], v[28:29]
	v_mul_f32_e32 v28, v50, v50
	v_mul_f32_e32 v29, v51, v51
	v_pk_add_f32 v[26:27], v[26:27], v[26:27] op_sel:[0,1] op_sel_hi:[1,0]
	v_mov_b32_e32 v25, v28
	v_mov_b32_e32 v27, v29
	v_pk_add_f32 v[24:25], v[24:25], v[26:27]
	v_mul_f32_e32 v26, v55, v55
	v_mul_f32_e32 v28, v57, v57
	v_mul_f32_e32 v30, v52, v52
	v_mul_f32_e32 v31, v53, v53
	v_pk_fma_f32 v[26:27], v[54:55], v[54:55], v[26:27] op_sel_hi:[1,1,0]
	v_pk_fma_f32 v[28:29], v[56:57], v[56:57], v[28:29] op_sel_hi:[1,1,0]
	v_mov_b32_e32 v27, v30
	v_mov_b32_e32 v29, v31
	v_pk_add_f32 v[26:27], v[26:27], v[28:29]
	s_nop 0
	v_pk_add_f32 v[24:25], v[24:25], v[26:27]
	v_and_b32_e32 v26, 64, v212
	v_add_f32_e32 v24, v24, v25
	v_xor_b32_e32 v25, 16, v212
	v_add_u32_e32 v26, 64, v26
	v_cmp_lt_i32_e32 vcc, v25, v26
	s_nop 1
	v_cndmask_b32_e32 v25, v212, v25, vcc
	v_lshlrev_b32_e32 v25, 2, v25
	ds_bpermute_b32 v25, v25, v24
	s_waitcnt lgkmcnt(0)
	v_add_f32_e32 v24, v24, v25
	v_xor_b32_e32 v25, 32, v212
	v_cmp_lt_i32_e32 vcc, v25, v26
	s_nop 1
	v_cndmask_b32_e32 v25, v212, v25, vcc
	v_lshlrev_b32_e32 v25, 2, v25
	ds_bpermute_b32 v25, v25, v24
	s_waitcnt lgkmcnt(0)
	v_add_f32_e32 v24, v24, v25
	v_fmamk_f32 v24, v24, 0x3c800000, v210
	v_mul_f32_e32 v25, 0x4f800000, v24
	v_cmp_gt_f32_e32 vcc, s28, v24
	s_nop 1
	v_cndmask_b32_e32 v24, v24, v25, vcc
	v_sqrt_f32_e32 v25, v24
	s_nop 0
	v_add_u32_e32 v26, -1, v25
	v_fma_f32 v27, -v26, v25, v24
	v_cmp_ge_f32_e64 s[6:7], 0, v27
	v_add_u32_e32 v27, 1, v25
	s_nop 0
	v_cndmask_b32_e64 v26, v25, v26, s[6:7]
	v_fma_f32 v25, -v27, v25, v24
	v_cmp_lt_f32_e64 s[6:7], 0, v25
	s_nop 1
	v_cndmask_b32_e64 v25, v26, v27, s[6:7]
	v_mul_f32_e32 v26, 0x37800000, v25
	v_cndmask_b32_e32 v25, v25, v26, vcc
	v_cmp_class_f32_e32 vcc, v24, v211
	s_nop 1
	v_cndmask_b32_e32 v24, v25, v24, vcc
	v_div_scale_f32 v25, s[0:1], v24, v24, 1.0
	v_rcp_f32_e32 v26, v25
	s_nop 0
	v_fma_f32 v27, -v25, v26, 1.0
	v_fmac_f32_e32 v26, v27, v26
	v_div_scale_f32 v27, vcc, 1.0, v24, 1.0
	v_mul_f32_e32 v28, v27, v26
	v_fma_f32 v29, -v25, v28, v27
	v_fmac_f32_e32 v28, v29, v26
	v_fma_f32 v25, -v25, v28, v27
	v_div_fmas_f32 v25, v25, v26, v28
	v_div_fixup_f32 v26, v25, v24, 1.0
	v_pk_mul_f32 v[24:25], v[62:63], v[26:27] op_sel_hi:[1,0]
	v_pk_mul_f32 v[28:29], v[64:65], v[26:27] op_sel_hi:[1,0]
	s_nop 0
	v_pk_mul_f32 v[164:165], v[14:15], v[24:25]
	v_pk_mul_f32 v[32:33], v[16:17], v[28:29]
	v_pk_mul_f32 v[24:25], v[58:59], v[26:27] op_sel_hi:[1,0]
	v_pk_mul_f32 v[28:29], v[60:61], v[26:27] op_sel_hi:[1,0]
	v_pk_mul_f32 v[186:187], v[6:7], v[24:25]
	v_pk_mul_f32 v[162:163], v[8:9], v[28:29]
	v_pk_mul_f32 v[28:29], v[54:55], v[26:27] op_sel_hi:[1,0]
	v_pk_mul_f32 v[24:25], v[56:57], v[26:27] op_sel_hi:[1,0]
	v_pk_mul_f32 v[30:31], v[50:51], v[26:27] op_sel_hi:[1,0]
	v_pk_mul_f32 v[26:27], v[52:53], v[26:27] op_sel_hi:[1,0]
	v_pk_mul_f32 v[24:25], v[12:13], v[24:25]
	v_pk_mul_f32 v[28:29], v[10:11], v[28:29]
	v_pk_mul_f32 v[26:27], v[4:5], v[26:27]
	v_pk_mul_f32 v[30:31], v[2:3], v[30:31]
; __device__ __forceinline__ unsigned cvt_pk_bf16(float lo, float hi) { unsigned r; asm volatile("v_cvt_pk_bf16_f32 %0, %1, %2" : "=v"(r) : "v"(lo), "v"(hi)); return r; }
; template <bool F8OUT = false> __device__ __forceinline__ void head_tile_store(const f32x4 (&acc)[2][2][4][2], bf16_t* obase  , int opitch, const float* gain, float scale, const f32x2e* rope, int row0, int fq) {
;     ...
;             if (gain) {
;                 float ss = 0.f;
; #pragma unroll
;                 for (int bj = 0; bj < 2; ++bj)
; #pragma unroll
;                     for (int n = 0; n < 2; ++n) ss += (x[bj][n][0] * x[bj][n][0] + x[bj][n][1] * x[bj][n][1]) + (x[bj][n][2] * x[bj][n][2] + x[bj][n][3] * x[bj][n][3]);
;                 ss += __shfl_xor(ss, 16); ss += __shfl_xor(ss, 32);
;                 const float r = scale / sqrtf(ss * (1.f / 64.f) + 1e-6f);
; #pragma unroll
;                 for (int bj = 0; bj < 2; ++bj)
; #pragma unroll
;                     for (int n = 0; n < 2; ++n) x[bj][n] = x[bj][n] * r * g[bj][n];
;             }
;     ...
;             bf16_t* rowp = obase + (size_t)row * opitch + 8 * fq;
; #pragma unroll
;             for (int bj = 0; bj < 2; ++bj) { u32x4 w; w.x = cvt_pk_bf16(x[bj][0][0], x[bj][0][1]); w.y = cvt_pk_bf16(x[bj][0][2], x[bj][0][3]); w.z = cvt_pk_bf16(x[bj][1][0], x[bj][1][1]); w.w = cvt_pk_bf16(x[bj][1][2], x[bj][1][3]);
;                 *(u32x4*)(rowp + 32 * bj) = w; }
.LBB0_256:
	v_lshl_add_u64 v[192:193], v[22:23], 0, s[12:13]
	v_add_co_u32_e32 v22, vcc, 0x28000, v22
	v_cvt_pk_bf16_f32 v188, v164, v165
	v_cvt_pk_bf16_f32 v189, v32, v33
	v_cvt_pk_bf16_f32 v190, v186, v187
	v_cvt_pk_bf16_f32 v191, v162, v163
	s_nop 1
	v_addc_co_u32_e32 v23, vcc, 0, v23, vcc
	global_store_dwordx4 v[22:23], v[188:191], off
	v_cvt_pk_bf16_f32 v22, v28, v29
	v_cvt_pk_bf16_f32 v23, v24, v25
	v_cvt_pk_bf16_f32 v24, v30, v31
	v_cvt_pk_bf16_f32 v25, v26, v27
	global_store_dwordx4 v[192:193], v[22:25], off offset:64
	s_and_b64 vcc, exec, s[4:5]
	v_mov_b32_e32 v27, v35
	v_mov_b32_e32 v23, v37
	v_mov_b32_e32 v22, v36
	v_mov_b32_e32 v26, v34
	v_mov_b32_e32 v25, v41
	v_mov_b32_e32 v24, v40
	v_mov_b32_e32 v29, v39
	v_mov_b32_e32 v28, v38
	v_mov_b32_e32 v31, v45
	v_mov_b32_e32 v30, v44
	v_mov_b32_e32 v163, v43
	v_mov_b32_e32 v162, v42
	v_mov_b32_e32 v33, v49
	v_mov_b32_e32 v32, v48
	v_mov_b32_e32 v165, v47
	v_mov_b32_e32 v164, v46
	s_cbranch_vccnz .LBB0_258
	v_pk_mul_f32 v[22:23], v[48:49], v[48:49]
	v_pk_mul_f32 v[24:25], v[46:47], v[46:47]
	s_nop 0
	v_pk_mov_b32 v[26:27], v[24:25], v[22:23] op_sel:[1,0]
	v_mov_b32_e32 v25, v23
	v_pk_add_f32 v[22:23], v[26:27], v[24:25]
	v_pk_mul_f32 v[24:25], v[44:45], v[44:45]
	v_pk_mul_f32 v[26:27], v[42:43], v[42:43]
	v_pk_add_f32 v[22:23], v[22:23], v[22:23] op_sel:[0,1] op_sel_hi:[1,0]
	v_pk_mov_b32 v[28:29], v[26:27], v[24:25] op_sel:[1,0]
	v_mov_b32_e32 v27, v25
	v_pk_add_f32 v[24:25], v[28:29], v[26:27]
	v_mul_f32_e32 v26, v34, v34
	v_mul_f32_e32 v27, v35, v35
	v_pk_add_f32 v[24:25], v[24:25], v[24:25] op_sel:[0,1] op_sel_hi:[1,0]
	v_mov_b32_e32 v23, v26
	v_mov_b32_e32 v25, v27
	v_pk_add_f32 v[22:23], v[22:23], v[24:25]
	v_mul_f32_e32 v24, v39, v39
	v_mul_f32_e32 v26, v41, v41
	v_mul_f32_e32 v28, v36, v36
	v_mul_f32_e32 v29, v37, v37
	v_pk_fma_f32 v[24:25], v[38:39], v[38:39], v[24:25] op_sel_hi:[1,1,0]
	v_pk_fma_f32 v[26:27], v[40:41], v[40:41], v[26:27] op_sel_hi:[1,1,0]
	v_mov_b32_e32 v25, v28
	v_mov_b32_e32 v27, v29
	v_pk_add_f32 v[24:25], v[24:25], v[26:27]
	s_nop 0
	v_pk_add_f32 v[22:23], v[22:23], v[24:25]
	v_and_b32_e32 v24, 64, v212
	v_add_f32_e32 v22, v22, v23
	v_xor_b32_e32 v23, 16, v212
	v_add_u32_e32 v24, 64, v24
	v_cmp_lt_i32_e32 vcc, v23, v24
	s_nop 1
	v_cndmask_b32_e32 v23, v212, v23, vcc
	v_lshlrev_b32_e32 v23, 2, v23
	ds_bpermute_b32 v23, v23, v22
	s_waitcnt lgkmcnt(0)
	v_add_f32_e32 v22, v22, v23
	v_xor_b32_e32 v23, 32, v212
	v_cmp_lt_i32_e32 vcc, v23, v24
	s_nop 1
	v_cndmask_b32_e32 v23, v212, v23, vcc
	v_lshlrev_b32_e32 v23, 2, v23
	ds_bpermute_b32 v23, v23, v22
	s_waitcnt lgkmcnt(0)
	v_add_f32_e32 v22, v22, v23
	v_fmamk_f32 v22, v22, 0x3c800000, v210
	v_mul_f32_e32 v23, 0x4f800000, v22
	v_cmp_gt_f32_e32 vcc, s28, v22
	s_nop 1
	v_cndmask_b32_e32 v22, v22, v23, vcc
	v_sqrt_f32_e32 v23, v22
	s_nop 0
	v_add_u32_e32 v24, -1, v23
	v_fma_f32 v25, -v24, v23, v22
	v_cmp_ge_f32_e64 s[4:5], 0, v25
	v_add_u32_e32 v25, 1, v23
	s_nop 0
	v_cndmask_b32_e64 v24, v23, v24, s[4:5]
	v_fma_f32 v23, -v25, v23, v22
	v_cmp_lt_f32_e64 s[4:5], 0, v23
	s_nop 1
	v_cndmask_b32_e64 v23, v24, v25, s[4:5]
	v_mul_f32_e32 v24, 0x37800000, v23
	v_cndmask_b32_e32 v23, v23, v24, vcc
	v_cmp_class_f32_e32 vcc, v22, v211
	s_nop 1
	v_cndmask_b32_e32 v22, v23, v22, vcc
	v_div_scale_f32 v23, s[0:1], v22, v22, 1.0
	v_rcp_f32_e32 v24, v23
	s_nop 0
	v_fma_f32 v25, -v23, v24, 1.0
	v_fmac_f32_e32 v24, v25, v24
	v_div_scale_f32 v25, vcc, 1.0, v22, 1.0
	v_mul_f32_e32 v26, v25, v24
	v_fma_f32 v27, -v23, v26, v25
	v_fmac_f32_e32 v26, v27, v24
	v_fma_f32 v23, -v23, v26, v25
	v_div_fmas_f32 v23, v23, v24, v26
	v_div_fixup_f32 v22, v23, v22, 1.0
	v_pk_mul_f32 v[24:25], v[46:47], v[22:23] op_sel_hi:[1,0]
	v_pk_mul_f32 v[26:27], v[48:49], v[22:23] op_sel_hi:[1,0]
	s_nop 0
	v_pk_mul_f32 v[164:165], v[14:15], v[24:25]
	v_pk_mul_f32 v[32:33], v[16:17], v[26:27]
	v_pk_mul_f32 v[14:15], v[42:43], v[22:23] op_sel_hi:[1,0]
	v_pk_mul_f32 v[16:17], v[44:45], v[22:23] op_sel_hi:[1,0]
	v_pk_mul_f32 v[162:163], v[6:7], v[14:15]
	v_pk_mul_f32 v[30:31], v[8:9], v[16:17]
	v_pk_mul_f32 v[6:7], v[38:39], v[22:23] op_sel_hi:[1,0]
	v_pk_mul_f32 v[8:9], v[40:41], v[22:23] op_sel_hi:[1,0]
	v_pk_mul_f32 v[28:29], v[10:11], v[6:7]
	v_pk_mul_f32 v[24:25], v[12:13], v[8:9]
	v_pk_mul_f32 v[6:7], v[34:35], v[22:23] op_sel_hi:[1,0]
	v_pk_mul_f32 v[8:9], v[36:37], v[22:23] op_sel_hi:[1,0]
	v_pk_mul_f32 v[26:27], v[2:3], v[6:7]
	v_pk_mul_f32 v[22:23], v[4:5], v[8:9]
.LBB0_258:
	s_nop 0
	v_lshlrev_b64 v[2:3], 10, v[18:19]
	v_lshl_add_u64 v[6:7], v[20:21], 0, v[2:3]
	v_lshl_add_u64 v[8:9], v[6:7], 0, s[22:23]
	v_add_co_u32_e32 v6, vcc, s24, v6
	v_cvt_pk_bf16_f32 v2, v164, v165
	v_cvt_pk_bf16_f32 v3, v32, v33
	v_cvt_pk_bf16_f32 v4, v162, v163
	v_cvt_pk_bf16_f32 v5, v30, v31
	s_nop 1
	v_addc_co_u32_e32 v7, vcc, 0, v7, vcc
	global_store_dwordx4 v[6:7], v[2:5], off
	s_nop 1
	v_cvt_pk_bf16_f32 v2, v28, v29
	v_cvt_pk_bf16_f32 v3, v24, v25
	v_cvt_pk_bf16_f32 v4, v26, v27
	v_cvt_pk_bf16_f32 v5, v22, v23
	global_store_dwordx4 v[8:9], v[2:5], off offset:64

; __device__ __forceinline__ unsigned cvt_pk_bf16(float lo, float hi) { unsigned r; asm volatile("v_cvt_pk_bf16_f32 %0, %1, %2" : "=v"(r) : "v"(lo), "v"(hi)); return r; }
; template <bool F8OUT = false> __device__ __forceinline__ void head_tile_store(const f32x4 (&acc)[2][2][4][2], bf16_t* obase  , int opitch, const float* gain, float scale, const f32x2e* rope, int row0, int fq) {
;     ...
;             if (gain) {
;                 float ss = 0.f;
; #pragma unroll
;                 for (int bj = 0; bj < 2; ++bj)
; #pragma unroll
;                     for (int n = 0; n < 2; ++n) ss += (x[bj][n][0] * x[bj][n][0] + x[bj][n][1] * x[bj][n][1]) + (x[bj][n][2] * x[bj][n][2] + x[bj][n][3] * x[bj][n][3]);
;                 ss += __shfl_xor(ss, 16); ss += __shfl_xor(ss, 32);
;                 const float r = scale / sqrtf(ss * (1.f / 64.f) + 1e-6f);
; #pragma unroll
;                 for (int bj = 0; bj < 2; ++bj)
; #pragma unroll
;                     for (int n = 0; n < 2; ++n) x[bj][n] = x[bj][n] * r * g[bj][n];
;             }
;     ...
;             bf16_t* rowp = obase + (size_t)row * opitch + 8 * fq;
; #pragma unroll
;             for (int bj = 0; bj < 2; ++bj) { u32x4 w; w.x = cvt_pk_bf16(x[bj][0][0], x[bj][0][1]); w.y = cvt_pk_bf16(x[bj][0][2], x[bj][0][3]); w.z = cvt_pk_bf16(x[bj][1][0], x[bj][1][1]); w.w = cvt_pk_bf16(x[bj][1][2], x[bj][1][3]);
;                 *(u32x4*)(rowp + 32 * bj) = w; }
.LBB0_266:
	s_lshl_b32 s0, s18, 7
	s_add_u32 s0, s8, s0
	s_addc_u32 s1, s9, 0
	v_ashrrev_i32_e32 v185, 31, v184
	v_lshl_add_u64 v[18:19], v[18:19], 1, s[0:1]
	v_lshlrev_b64 v[20:21], 10, v[184:185]
	v_lshl_add_u64 v[20:21], v[18:19], 0, v[20:21]
	v_cvt_pk_bf16_f32 v22, v158, v159
	v_cvt_pk_bf16_f32 v23, v160, v161
	v_cvt_pk_bf16_f32 v24, v154, v155
	v_cvt_pk_bf16_f32 v25, v156, v157
	s_and_b64 vcc, exec, s[4:5]
	global_store_dwordx4 v[20:21], v[22:25], off
	s_nop 1
	v_cvt_pk_bf16_f32 v22, v150, v151
	v_cvt_pk_bf16_f32 v23, v152, v153
	v_cvt_pk_bf16_f32 v24, v146, v147
	v_cvt_pk_bf16_f32 v25, v148, v149
	global_store_dwordx4 v[20:21], v[22:25], off offset:64
	s_cbranch_vccnz .LBB0_268
	s_nop 0
	v_pk_mul_f32 v[22:23], v[144:145], v[144:145]
	v_pk_mul_f32 v[24:25], v[142:143], v[142:143]
	s_nop 0
	v_pk_mov_b32 v[26:27], v[24:25], v[22:23] op_sel:[1,0]
	v_mov_b32_e32 v25, v23
	v_pk_add_f32 v[22:23], v[26:27], v[24:25]
	v_pk_mul_f32 v[24:25], v[140:141], v[140:141]
	v_pk_mul_f32 v[26:27], v[138:139], v[138:139]
	v_pk_add_f32 v[22:23], v[22:23], v[22:23] op_sel:[0,1] op_sel_hi:[1,0]
	v_pk_mov_b32 v[28:29], v[26:27], v[24:25] op_sel:[1,0]
	v_mov_b32_e32 v27, v25
	v_pk_add_f32 v[24:25], v[28:29], v[26:27]
	v_mul_f32_e32 v26, v130, v130
	v_mul_f32_e32 v27, v131, v131
	v_pk_add_f32 v[24:25], v[24:25], v[24:25] op_sel:[0,1] op_sel_hi:[1,0]
	v_mov_b32_e32 v23, v26
	v_mov_b32_e32 v25, v27
	v_pk_add_f32 v[22:23], v[22:23], v[24:25]
	v_mul_f32_e32 v24, v135, v135
	v_mul_f32_e32 v26, v137, v137
	v_mul_f32_e32 v28, v132, v132
	v_mul_f32_e32 v29, v133, v133
	v_pk_fma_f32 v[24:25], v[134:135], v[134:135], v[24:25] op_sel_hi:[1,1,0]
	v_pk_fma_f32 v[26:27], v[136:137], v[136:137], v[26:27] op_sel_hi:[1,1,0]
	v_mov_b32_e32 v25, v28
	v_mov_b32_e32 v27, v29
	v_pk_add_f32 v[24:25], v[24:25], v[26:27]
	s_nop 0
	v_pk_add_f32 v[22:23], v[22:23], v[24:25]
	v_and_b32_e32 v24, 64, v212
	v_add_f32_e32 v22, v22, v23
	v_xor_b32_e32 v23, 16, v212
	v_add_u32_e32 v24, 64, v24
	v_cmp_lt_i32_e32 vcc, v23, v24
	s_nop 1
	v_cndmask_b32_e32 v23, v212, v23, vcc
	v_lshlrev_b32_e32 v23, 2, v23
	ds_bpermute_b32 v23, v23, v22
	s_waitcnt lgkmcnt(0)
	v_add_f32_e32 v22, v22, v23
	v_xor_b32_e32 v23, 32, v212
	v_cmp_lt_i32_e32 vcc, v23, v24
	s_nop 1
	v_cndmask_b32_e32 v23, v212, v23, vcc
	v_lshlrev_b32_e32 v23, 2, v23
	ds_bpermute_b32 v23, v23, v22
	s_waitcnt lgkmcnt(0)
	v_add_f32_e32 v22, v22, v23
	v_fmamk_f32 v22, v22, 0x3c800000, v210
	v_mul_f32_e32 v23, 0x4f800000, v22
	v_cmp_gt_f32_e32 vcc, s28, v22
	s_nop 1
	v_cndmask_b32_e32 v22, v22, v23, vcc
	v_sqrt_f32_e32 v23, v22
	s_nop 0
	v_add_u32_e32 v24, -1, v23
	v_fma_f32 v25, -v24, v23, v22
	v_cmp_ge_f32_e64 s[6:7], 0, v25
	v_add_u32_e32 v25, 1, v23
	s_nop 0
	v_cndmask_b32_e64 v24, v23, v24, s[6:7]
	v_fma_f32 v23, -v25, v23, v22
	v_cmp_lt_f32_e64 s[6:7], 0, v23
	s_nop 1
	v_cndmask_b32_e64 v23, v24, v25, s[6:7]
	v_mul_f32_e32 v24, 0x37800000, v23
	v_cndmask_b32_e32 v23, v23, v24, vcc
	v_cmp_class_f32_e32 vcc, v22, v211
	s_nop 1
	v_cndmask_b32_e32 v22, v23, v22, vcc
	v_div_scale_f32 v23, s[0:1], v22, v22, s25
	v_rcp_f32_e32 v24, v23
	s_nop 0
	v_fma_f32 v25, -v23, v24, 1.0
	v_fmac_f32_e32 v24, v25, v24
	v_div_scale_f32 v25, vcc, s25, v22, s25
	v_mul_f32_e32 v26, v25, v24
	v_fma_f32 v27, -v23, v26, v25
	v_fmac_f32_e32 v26, v27, v24
	v_fma_f32 v23, -v23, v26, v25
	v_div_fmas_f32 v23, v23, v24, v26
	v_div_fixup_f32 v22, v23, v22, s25
	v_pk_mul_f32 v[24:25], v[142:143], v[22:23] op_sel_hi:[1,0]
	v_pk_mul_f32 v[26:27], v[144:145], v[22:23] op_sel_hi:[1,0]
	s_nop 0
	v_pk_mul_f32 v[142:143], v[14:15], v[24:25]
	v_pk_mul_f32 v[24:25], v[138:139], v[22:23] op_sel_hi:[1,0]
	v_pk_mul_f32 v[144:145], v[16:17], v[26:27]
	v_pk_mul_f32 v[26:27], v[140:141], v[22:23] op_sel_hi:[1,0]
	v_pk_mul_f32 v[138:139], v[6:7], v[24:25]
	v_pk_mul_f32 v[24:25], v[134:135], v[22:23] op_sel_hi:[1,0]
	v_pk_mul_f32 v[140:141], v[8:9], v[26:27]
	v_pk_mul_f32 v[26:27], v[136:137], v[22:23] op_sel_hi:[1,0]
	v_pk_mul_f32 v[134:135], v[10:11], v[24:25]
	v_pk_mul_f32 v[24:25], v[130:131], v[22:23] op_sel_hi:[1,0]
	v_pk_mul_f32 v[22:23], v[132:133], v[22:23] op_sel_hi:[1,0]
	v_pk_mul_f32 v[136:137], v[12:13], v[26:27]
	v_pk_mul_f32 v[132:133], v[4:5], v[22:23]
	v_pk_mul_f32 v[130:131], v[2:3], v[24:25]
; __device__ __forceinline__ unsigned cvt_pk_bf16(float lo, float hi) { unsigned r; asm volatile("v_cvt_pk_bf16_f32 %0, %1, %2" : "=v"(r) : "v"(lo), "v"(hi)); return r; }
; template <bool F8OUT = false> __device__ __forceinline__ void head_tile_store(const f32x4 (&acc)[2][2][4][2], bf16_t* obase  , int opitch, const float* gain, float scale, const f32x2e* rope, int row0, int fq) {
;     ...
;             if (gain) {
;                 float ss = 0.f;
; #pragma unroll
;                 for (int bj = 0; bj < 2; ++bj)
; #pragma unroll
;                     for (int n = 0; n < 2; ++n) ss += (x[bj][n][0] * x[bj][n][0] + x[bj][n][1] * x[bj][n][1]) + (x[bj][n][2] * x[bj][n][2] + x[bj][n][3] * x[bj][n][3]);
;                 ss += __shfl_xor(ss, 16); ss += __shfl_xor(ss, 32);
;                 const float r = scale / sqrtf(ss * (1.f / 64.f) + 1e-6f);
; #pragma unroll
;                 for (int bj = 0; bj < 2; ++bj)
; #pragma unroll
;                     for (int n = 0; n < 2; ++n) x[bj][n] = x[bj][n] * r * g[bj][n];
;             }
;     ...
;             bf16_t* rowp = obase + (size_t)row * opitch + 8 * fq;
; #pragma unroll
;             for (int bj = 0; bj < 2; ++bj) { u32x4 w; w.x = cvt_pk_bf16(x[bj][0][0], x[bj][0][1]); w.y = cvt_pk_bf16(x[bj][0][2], x[bj][0][3]); w.z = cvt_pk_bf16(x[bj][1][0], x[bj][1][1]); w.w = cvt_pk_bf16(x[bj][1][2], x[bj][1][3]);
;                 *(u32x4*)(rowp + 32 * bj) = w; }
.LBB0_268:
	v_add_co_u32_e32 v28, vcc, 0x4000, v20
	v_lshl_add_u64 v[26:27], v[20:21], 0, s[92:93]
	s_nop 0
	v_addc_co_u32_e32 v29, vcc, 0, v21, vcc
	v_cvt_pk_bf16_f32 v22, v142, v143
	v_cvt_pk_bf16_f32 v23, v144, v145
	v_cvt_pk_bf16_f32 v24, v138, v139
	v_cvt_pk_bf16_f32 v25, v140, v141
	s_and_b64 vcc, exec, s[4:5]
	global_store_dwordx4 v[28:29], v[22:25], off
	s_nop 1
	v_cvt_pk_bf16_f32 v22, v134, v135
	v_cvt_pk_bf16_f32 v23, v136, v137
	v_cvt_pk_bf16_f32 v24, v130, v131
	v_cvt_pk_bf16_f32 v25, v132, v133
	global_store_dwordx4 v[26:27], v[22:25], off offset:64
	s_cbranch_vccnz .LBB0_270
	s_nop 0
	v_pk_mul_f32 v[22:23], v[128:129], v[128:129]
	v_pk_mul_f32 v[24:25], v[126:127], v[126:127]
	s_nop 0
	v_pk_mov_b32 v[26:27], v[24:25], v[22:23] op_sel:[1,0]
	v_mov_b32_e32 v25, v23
	v_pk_add_f32 v[22:23], v[26:27], v[24:25]
	v_pk_mul_f32 v[24:25], v[124:125], v[124:125]
	v_pk_mul_f32 v[26:27], v[122:123], v[122:123]
	v_pk_add_f32 v[22:23], v[22:23], v[22:23] op_sel:[0,1] op_sel_hi:[1,0]
	v_pk_mov_b32 v[28:29], v[26:27], v[24:25] op_sel:[1,0]
	v_mov_b32_e32 v27, v25
	v_pk_add_f32 v[24:25], v[28:29], v[26:27]
	v_mul_f32_e32 v26, v114, v114
	v_mul_f32_e32 v27, v115, v115
	v_pk_add_f32 v[24:25], v[24:25], v[24:25] op_sel:[0,1] op_sel_hi:[1,0]
	v_mov_b32_e32 v23, v26
	v_mov_b32_e32 v25, v27
	v_pk_add_f32 v[22:23], v[22:23], v[24:25]
	v_mul_f32_e32 v24, v119, v119
	v_mul_f32_e32 v26, v121, v121
	v_mul_f32_e32 v28, v116, v116
	v_mul_f32_e32 v29, v117, v117
	v_pk_fma_f32 v[24:25], v[118:119], v[118:119], v[24:25] op_sel_hi:[1,1,0]
	v_pk_fma_f32 v[26:27], v[120:121], v[120:121], v[26:27] op_sel_hi:[1,1,0]
	v_mov_b32_e32 v25, v28
	v_mov_b32_e32 v27, v29
	v_pk_add_f32 v[24:25], v[24:25], v[26:27]
	s_nop 0
	v_pk_add_f32 v[22:23], v[22:23], v[24:25]
	v_and_b32_e32 v24, 64, v212
	v_add_f32_e32 v22, v22, v23
	v_xor_b32_e32 v23, 16, v212
	v_add_u32_e32 v24, 64, v24
	v_cmp_lt_i32_e32 vcc, v23, v24
	s_nop 1
	v_cndmask_b32_e32 v23, v212, v23, vcc
	v_lshlrev_b32_e32 v23, 2, v23
	ds_bpermute_b32 v23, v23, v22
	s_waitcnt lgkmcnt(0)
	v_add_f32_e32 v22, v22, v23
	v_xor_b32_e32 v23, 32, v212
	v_cmp_lt_i32_e32 vcc, v23, v24
	s_nop 1
	v_cndmask_b32_e32 v23, v212, v23, vcc
	v_lshlrev_b32_e32 v23, 2, v23
	ds_bpermute_b32 v23, v23, v22
	s_waitcnt lgkmcnt(0)
	v_add_f32_e32 v22, v22, v23
	v_fmamk_f32 v22, v22, 0x3c800000, v210
	v_mul_f32_e32 v23, 0x4f800000, v22
	v_cmp_gt_f32_e32 vcc, s28, v22
	s_nop 1
	v_cndmask_b32_e32 v22, v22, v23, vcc
	v_sqrt_f32_e32 v23, v22
	s_nop 0
	v_add_u32_e32 v24, -1, v23
	v_fma_f32 v25, -v24, v23, v22
	v_cmp_ge_f32_e64 s[6:7], 0, v25
	v_add_u32_e32 v25, 1, v23
	s_nop 0
	v_cndmask_b32_e64 v24, v23, v24, s[6:7]
	v_fma_f32 v23, -v25, v23, v22
	v_cmp_lt_f32_e64 s[6:7], 0, v23
	s_nop 1
	v_cndmask_b32_e64 v23, v24, v25, s[6:7]
	v_mul_f32_e32 v24, 0x37800000, v23
	v_cndmask_b32_e32 v23, v23, v24, vcc
	v_cmp_class_f32_e32 vcc, v22, v211
	s_nop 1
	v_cndmask_b32_e32 v22, v23, v22, vcc
	v_div_scale_f32 v23, s[0:1], v22, v22, s25
	v_rcp_f32_e32 v24, v23
	s_nop 0
	v_fma_f32 v25, -v23, v24, 1.0
	v_fmac_f32_e32 v24, v25, v24
	v_div_scale_f32 v25, vcc, s25, v22, s25
	v_mul_f32_e32 v26, v25, v24
	v_fma_f32 v27, -v23, v26, v25
	v_fmac_f32_e32 v26, v27, v24
	v_fma_f32 v23, -v23, v26, v25
	v_div_fmas_f32 v23, v23, v24, v26
	v_div_fixup_f32 v22, v23, v22, s25
	v_pk_mul_f32 v[24:25], v[126:127], v[22:23] op_sel_hi:[1,0]
	v_pk_mul_f32 v[26:27], v[128:129], v[22:23] op_sel_hi:[1,0]
	s_nop 0
	v_pk_mul_f32 v[126:127], v[14:15], v[24:25]
	v_pk_mul_f32 v[24:25], v[122:123], v[22:23] op_sel_hi:[1,0]
	v_pk_mul_f32 v[128:129], v[16:17], v[26:27]
	v_pk_mul_f32 v[26:27], v[124:125], v[22:23] op_sel_hi:[1,0]
	v_pk_mul_f32 v[122:123], v[6:7], v[24:25]
	v_pk_mul_f32 v[24:25], v[118:119], v[22:23] op_sel_hi:[1,0]
	v_pk_mul_f32 v[124:125], v[8:9], v[26:27]
	v_pk_mul_f32 v[26:27], v[120:121], v[22:23] op_sel_hi:[1,0]
	v_pk_mul_f32 v[118:119], v[10:11], v[24:25]
	v_pk_mul_f32 v[24:25], v[114:115], v[22:23] op_sel_hi:[1,0]
	v_pk_mul_f32 v[22:23], v[116:117], v[22:23] op_sel_hi:[1,0]
	v_pk_mul_f32 v[120:121], v[12:13], v[26:27]
	v_pk_mul_f32 v[116:117], v[4:5], v[22:23]
	v_pk_mul_f32 v[114:115], v[2:3], v[24:25]
.LBB0_270:
	s_mov_b64 s[0:1], 0x8000
	v_lshl_add_u64 v[26:27], v[20:21], 0, s[0:1]
	v_add_co_u32_e32 v20, vcc, 0x8000, v20
	v_cvt_pk_bf16_f32 v22, v126, v127
	v_cvt_pk_bf16_f32 v23, v128, v129
	v_cvt_pk_bf16_f32 v24, v122, v123
	v_cvt_pk_bf16_f32 v25, v124, v125
	s_nop 1
	v_addc_co_u32_e32 v21, vcc, 0, v21, vcc
	s_and_b64 vcc, exec, s[4:5]
	global_store_dwordx4 v[20:21], v[22:25], off
	v_cvt_pk_bf16_f32 v20, v118, v119
	v_cvt_pk_bf16_f32 v21, v120, v121
	s_nop 1
	v_cvt_pk_bf16_f32 v22, v114, v115
	v_cvt_pk_bf16_f32 v23, v116, v117
	global_store_dwordx4 v[26:27], v[20:23], off offset:64
	s_cbranch_vccnz .LBB0_272
; __device__ __forceinline__ unsigned cvt_pk_bf16(float lo, float hi) { unsigned r; asm volatile("v_cvt_pk_bf16_f32 %0, %1, %2" : "=v"(r) : "v"(lo), "v"(hi)); return r; }
; template <bool F8OUT = false> __device__ __forceinline__ void head_tile_store(const f32x4 (&acc)[2][2][4][2], bf16_t* obase  , int opitch, const float* gain, float scale, const f32x2e* rope, int row0, int fq) {
;     ...
;             if (gain) {
;                 float ss = 0.f;
; #pragma unroll
;                 for (int bj = 0; bj < 2; ++bj)
; #pragma unroll
;                     for (int n = 0; n < 2; ++n) ss += (x[bj][n][0] * x[bj][n][0] + x[bj][n][1] * x[bj][n][1]) + (x[bj][n][2] * x[bj][n][2] + x[bj][n][3] * x[bj][n][3]);
;                 ss += __shfl_xor(ss, 16); ss += __shfl_xor(ss, 32);
;                 const float r = scale / sqrtf(ss * (1.f / 64.f) + 1e-6f);
; #pragma unroll
;                 for (int bj = 0; bj < 2; ++bj)
; #pragma unroll
;                     for (int n = 0; n < 2; ++n) x[bj][n] = x[bj][n] * r * g[bj][n];
;             }
;     ...
;             bf16_t* rowp = obase + (size_t)row * opitch + 8 * fq;
; #pragma unroll
;             for (int bj = 0; bj < 2; ++bj) { u32x4 w; w.x = cvt_pk_bf16(x[bj][0][0], x[bj][0][1]); w.y = cvt_pk_bf16(x[bj][0][2], x[bj][0][3]); w.z = cvt_pk_bf16(x[bj][1][0], x[bj][1][1]); w.w = cvt_pk_bf16(x[bj][1][2], x[bj][1][3]);
;                 *(u32x4*)(rowp + 32 * bj) = w; }
	s_nop 0
	v_pk_mul_f32 v[20:21], v[112:113], v[112:113]
	v_pk_mul_f32 v[22:23], v[110:111], v[110:111]
	s_nop 0
	v_pk_mov_b32 v[24:25], v[22:23], v[20:21] op_sel:[1,0]
	v_mov_b32_e32 v23, v21
	v_pk_add_f32 v[20:21], v[24:25], v[22:23]
	v_pk_mul_f32 v[22:23], v[108:109], v[108:109]
	v_pk_mul_f32 v[24:25], v[106:107], v[106:107]
	v_pk_add_f32 v[20:21], v[20:21], v[20:21] op_sel:[0,1] op_sel_hi:[1,0]
	v_pk_mov_b32 v[26:27], v[24:25], v[22:23] op_sel:[1,0]
	v_mov_b32_e32 v25, v23
	v_pk_add_f32 v[22:23], v[26:27], v[24:25]
	v_mul_f32_e32 v24, v98, v98
	v_mul_f32_e32 v25, v99, v99
	v_pk_add_f32 v[22:23], v[22:23], v[22:23] op_sel:[0,1] op_sel_hi:[1,0]
	v_mov_b32_e32 v21, v24
	v_mov_b32_e32 v23, v25
	v_pk_add_f32 v[20:21], v[20:21], v[22:23]
	v_mul_f32_e32 v22, v103, v103
	v_mul_f32_e32 v24, v105, v105
	v_mul_f32_e32 v26, v100, v100
	v_mul_f32_e32 v27, v101, v101
	v_pk_fma_f32 v[22:23], v[102:103], v[102:103], v[22:23] op_sel_hi:[1,1,0]
	v_pk_fma_f32 v[24:25], v[104:105], v[104:105], v[24:25] op_sel_hi:[1,1,0]
	v_mov_b32_e32 v23, v26
	v_mov_b32_e32 v25, v27
	v_pk_add_f32 v[22:23], v[22:23], v[24:25]
	s_nop 0
	v_pk_add_f32 v[20:21], v[20:21], v[22:23]
	v_and_b32_e32 v22, 64, v212
	v_add_f32_e32 v20, v20, v21
	v_xor_b32_e32 v21, 16, v212
	v_add_u32_e32 v22, 64, v22
	v_cmp_lt_i32_e32 vcc, v21, v22
	s_nop 1
	v_cndmask_b32_e32 v21, v212, v21, vcc
	v_lshlrev_b32_e32 v21, 2, v21
	ds_bpermute_b32 v21, v21, v20
	s_waitcnt lgkmcnt(0)
	v_add_f32_e32 v20, v20, v21
	v_xor_b32_e32 v21, 32, v212
	v_cmp_lt_i32_e32 vcc, v21, v22
	s_nop 1
	v_cndmask_b32_e32 v21, v212, v21, vcc
	v_lshlrev_b32_e32 v21, 2, v21
	ds_bpermute_b32 v21, v21, v20
	s_waitcnt lgkmcnt(0)
	v_add_f32_e32 v20, v20, v21
	v_fmamk_f32 v20, v20, 0x3c800000, v210
	v_mul_f32_e32 v21, 0x4f800000, v20
	v_cmp_gt_f32_e32 vcc, s28, v20
	s_nop 1
	v_cndmask_b32_e32 v20, v20, v21, vcc
	v_sqrt_f32_e32 v21, v20
	s_nop 0
	v_add_u32_e32 v22, -1, v21
	v_fma_f32 v23, -v22, v21, v20
	v_cmp_ge_f32_e64 s[6:7], 0, v23
	v_add_u32_e32 v23, 1, v21
	s_nop 0
	v_cndmask_b32_e64 v22, v21, v22, s[6:7]
	v_fma_f32 v21, -v23, v21, v20
	v_cmp_lt_f32_e64 s[6:7], 0, v21
	s_nop 1
	v_cndmask_b32_e64 v21, v22, v23, s[6:7]
	v_mul_f32_e32 v22, 0x37800000, v21
	v_cndmask_b32_e32 v21, v21, v22, vcc
	v_cmp_class_f32_e32 vcc, v20, v211
	s_nop 1
	v_cndmask_b32_e32 v20, v21, v20, vcc
	v_div_scale_f32 v21, s[0:1], v20, v20, s25
	v_rcp_f32_e32 v22, v21
	s_nop 0
	v_fma_f32 v23, -v21, v22, 1.0
	v_fmac_f32_e32 v22, v23, v22
	v_div_scale_f32 v23, vcc, s25, v20, s25
	v_mul_f32_e32 v24, v23, v22
	v_fma_f32 v25, -v21, v24, v23
	v_fmac_f32_e32 v24, v25, v22
	v_fma_f32 v21, -v21, v24, v23
	v_div_fmas_f32 v21, v21, v22, v24
	v_div_fixup_f32 v20, v21, v20, s25
	v_pk_mul_f32 v[22:23], v[110:111], v[20:21] op_sel_hi:[1,0]
	v_pk_mul_f32 v[24:25], v[112:113], v[20:21] op_sel_hi:[1,0]
	s_nop 0
	v_pk_mul_f32 v[110:111], v[14:15], v[22:23]
	v_pk_mul_f32 v[22:23], v[106:107], v[20:21] op_sel_hi:[1,0]
	v_pk_mul_f32 v[112:113], v[16:17], v[24:25]
	v_pk_mul_f32 v[24:25], v[108:109], v[20:21] op_sel_hi:[1,0]
	v_pk_mul_f32 v[106:107], v[6:7], v[22:23]
	v_pk_mul_f32 v[22:23], v[102:103], v[20:21] op_sel_hi:[1,0]
	v_pk_mul_f32 v[108:109], v[8:9], v[24:25]
	v_pk_mul_f32 v[24:25], v[104:105], v[20:21] op_sel_hi:[1,0]
	v_pk_mul_f32 v[102:103], v[10:11], v[22:23]
	v_pk_mul_f32 v[22:23], v[98:99], v[20:21] op_sel_hi:[1,0]
	v_pk_mul_f32 v[20:21], v[100:101], v[20:21] op_sel_hi:[1,0]
	v_pk_mul_f32 v[104:105], v[12:13], v[24:25]
	v_pk_mul_f32 v[100:101], v[4:5], v[20:21]
	v_pk_mul_f32 v[98:99], v[2:3], v[22:23]
.LBB0_272:
	s_nop 0
	v_lshlrev_b64 v[20:21], 10, v[184:185]
	v_lshl_add_u64 v[20:21], v[18:19], 0, v[20:21]
	v_add_co_u32_e32 v28, vcc, 0xc000, v20
	v_lshl_add_u64 v[26:27], v[20:21], 0, s[34:35]
	s_nop 0
	v_addc_co_u32_e32 v29, vcc, 0, v21, vcc
	v_cvt_pk_bf16_f32 v22, v110, v111
	v_cvt_pk_bf16_f32 v23, v112, v113
	v_cvt_pk_bf16_f32 v24, v106, v107
	v_cvt_pk_bf16_f32 v25, v108, v109
	s_and_b64 vcc, exec, s[4:5]
	global_store_dwordx4 v[28:29], v[22:25], off
	s_nop 1
	v_cvt_pk_bf16_f32 v22, v102, v103
	v_cvt_pk_bf16_f32 v23, v104, v105
	v_cvt_pk_bf16_f32 v24, v98, v99
	v_cvt_pk_bf16_f32 v25, v100, v101
	global_store_dwordx4 v[26:27], v[22:25], off offset:64
	s_cbranch_vccnz .LBB0_274
	s_nop 0
	v_pk_mul_f32 v[22:23], v[96:97], v[96:97]
	v_pk_mul_f32 v[24:25], v[94:95], v[94:95]
	s_nop 0
	v_pk_mov_b32 v[26:27], v[24:25], v[22:23] op_sel:[1,0]
	v_mov_b32_e32 v25, v23
	v_pk_add_f32 v[22:23], v[26:27], v[24:25]
	v_pk_mul_f32 v[24:25], v[92:93], v[92:93]
	v_pk_mul_f32 v[26:27], v[90:91], v[90:91]
	v_pk_add_f32 v[22:23], v[22:23], v[22:23] op_sel:[0,1] op_sel_hi:[1,0]
	v_pk_mov_b32 v[28:29], v[26:27], v[24:25] op_sel:[1,0]
	v_mov_b32_e32 v27, v25
	v_pk_add_f32 v[24:25], v[28:29], v[26:27]
	v_mul_f32_e32 v26, v82, v82
	v_mul_f32_e32 v27, v83, v83
	v_pk_add_f32 v[24:25], v[24:25], v[24:25] op_sel:[0,1] op_sel_hi:[1,0]
	v_mov_b32_e32 v23, v26
	v_mov_b32_e32 v25, v27
	v_pk_add_f32 v[22:23], v[22:23], v[24:25]
	v_mul_f32_e32 v24, v87, v87
	v_mul_f32_e32 v26, v89, v89
	v_mul_f32_e32 v28, v84, v84
	v_mul_f32_e32 v29, v85, v85
	v_pk_fma_f32 v[24:25], v[86:87], v[86:87], v[24:25] op_sel_hi:[1,1,0]
	v_pk_fma_f32 v[26:27], v[88:89], v[88:89], v[26:27] op_sel_hi:[1,1,0]
	v_mov_b32_e32 v25, v28
	v_mov_b32_e32 v27, v29
	v_pk_add_f32 v[24:25], v[24:25], v[26:27]
	s_nop 0
	v_pk_add_f32 v[22:23], v[22:23], v[24:25]
	v_and_b32_e32 v24, 64, v212
	v_add_f32_e32 v22, v22, v23
	v_xor_b32_e32 v23, 16, v212
	v_add_u32_e32 v24, 64, v24
	v_cmp_lt_i32_e32 vcc, v23, v24
	s_nop 1
	v_cndmask_b32_e32 v23, v212, v23, vcc
	v_lshlrev_b32_e32 v23, 2, v23
	ds_bpermute_b32 v23, v23, v22
	s_waitcnt lgkmcnt(0)
; template <bool F8OUT = false> __device__ __forceinline__ void head_tile_store(const f32x4 (&acc)[2][2][4][2], bf16_t* obase  , int opitch, const float* gain, float scale, const f32x2e* rope, int row0, int fq) {
;     ...
;             if (gain) {
;                 float ss = 0.f;
; #pragma unroll
;                 for (int bj = 0; bj < 2; ++bj)
; #pragma unroll
;                     for (int n = 0; n < 2; ++n) ss += (x[bj][n][0] * x[bj][n][0] + x[bj][n][1] * x[bj][n][1]) + (x[bj][n][2] * x[bj][n][2] + x[bj][n][3] * x[bj][n][3]);
;                 ss += __shfl_xor(ss, 16); ss += __shfl_xor(ss, 32);
;                 const float r = scale / sqrtf(ss * (1.f / 64.f) + 1e-6f);
; #pragma unroll
;                 for (int bj = 0; bj < 2; ++bj)
; #pragma unroll
;                     for (int n = 0; n < 2; ++n) x[bj][n] = x[bj][n] * r * g[bj][n];
;             }
;             if (rope) {
;                 const int t = row & 8191; const bool second = (fq & 2) != 0;
; #pragma unroll
;                 for (int bj = 0; bj < 2; ++bj) { const int pos = bj ? (t & 63) : (t >> 6); const f32x2e* tb = rope + pos * 16 + 8 * (fq & 1);
; #pragma unroll
;                     for (int n = 0; n < 2; ++n)
; #pragma unroll
;                         for (int e = 0; e < 4; ++e) { const float p = __shfl_xor(x[bj][n][e], 32); const f32x2e cs = tb[4 * n + e]; const float v = x[bj][n][e];
;                             x[bj][n][e] = second ? (p * cs.y + v * cs.x) : (v * cs.x - p * cs.y); } }
;             }
;             if constexpr (F8OUT) { unsigned char* rowp8 = (unsigned char*)obase + (size_t)row * opitch + 8 * fq; typedef unsigned u32x2_ __attribute__((ext_vector_type(2)));
; #pragma unroll
;                 for (int bj = 0; bj < 2; ++bj) *(u32x2_*)(rowp8 + 32 * bj) = (u32x2_){pk4_fp8(x[bj][0][0], x[bj][0][1], x[bj][0][2], x[bj][0][3]), pk4_fp8(x[bj][1][0], x[bj][1][1], x[bj][1][2], x[bj][1][3])};
;                 continue; }
;             bf16_t* rowp = obase + (size_t)row * opitch + 8 * fq;
; #pragma unroll
;             for (int bj = 0; bj < 2; ++bj) { u32x4 w; w.x = cvt_pk_bf16(x[bj][0][0], x[bj][0][1]); w.y = cvt_pk_bf16(x[bj][0][2], x[bj][0][3]); w.z = cvt_pk_bf16(x[bj][1][0], x[bj][1][1]); w.w = cvt_pk_bf16(x[bj][1][2], x[bj][1][3]);
;                 *(u32x4*)(rowp + 32 * bj) = w; }
	v_add_f32_e32 v22, v22, v23
	v_xor_b32_e32 v23, 32, v212
	v_cmp_lt_i32_e32 vcc, v23, v24
	s_nop 1
	v_cndmask_b32_e32 v23, v212, v23, vcc
	v_lshlrev_b32_e32 v23, 2, v23
	ds_bpermute_b32 v23, v23, v22
	s_waitcnt lgkmcnt(0)
	v_add_f32_e32 v22, v22, v23
	v_fmamk_f32 v22, v22, 0x3c800000, v210
	v_mul_f32_e32 v23, 0x4f800000, v22
	v_cmp_gt_f32_e32 vcc, s28, v22
	s_nop 1
	v_cndmask_b32_e32 v22, v22, v23, vcc
	v_sqrt_f32_e32 v23, v22
	s_nop 0
	v_add_u32_e32 v24, -1, v23
	v_fma_f32 v25, -v24, v23, v22
	v_cmp_ge_f32_e64 s[6:7], 0, v25
	v_add_u32_e32 v25, 1, v23
	s_nop 0
	v_cndmask_b32_e64 v24, v23, v24, s[6:7]
	v_fma_f32 v23, -v25, v23, v22
	v_cmp_lt_f32_e64 s[6:7], 0, v23
	s_nop 1
	v_cndmask_b32_e64 v23, v24, v25, s[6:7]
	v_mul_f32_e32 v24, 0x37800000, v23
	v_cndmask_b32_e32 v23, v23, v24, vcc
	v_cmp_class_f32_e32 vcc, v22, v211
	s_nop 1
	v_cndmask_b32_e32 v22, v23, v22, vcc
	v_div_scale_f32 v23, s[0:1], v22, v22, s25
	v_rcp_f32_e32 v24, v23
	s_nop 0
	v_fma_f32 v25, -v23, v24, 1.0
	v_fmac_f32_e32 v24, v25, v24
	v_div_scale_f32 v25, vcc, s25, v22, s25
	v_mul_f32_e32 v26, v25, v24
	v_fma_f32 v27, -v23, v26, v25
	v_fmac_f32_e32 v26, v27, v24
	v_fma_f32 v23, -v23, v26, v25
	v_div_fmas_f32 v23, v23, v24, v26
	v_div_fixup_f32 v22, v23, v22, s25
	v_pk_mul_f32 v[24:25], v[94:95], v[22:23] op_sel_hi:[1,0]
	v_pk_mul_f32 v[26:27], v[96:97], v[22:23] op_sel_hi:[1,0]
	s_nop 0
	v_pk_mul_f32 v[94:95], v[14:15], v[24:25]
	v_pk_mul_f32 v[24:25], v[90:91], v[22:23] op_sel_hi:[1,0]
	v_pk_mul_f32 v[96:97], v[16:17], v[26:27]
	v_pk_mul_f32 v[26:27], v[92:93], v[22:23] op_sel_hi:[1,0]
	v_pk_mul_f32 v[90:91], v[6:7], v[24:25]
	v_pk_mul_f32 v[24:25], v[86:87], v[22:23] op_sel_hi:[1,0]
	v_pk_mul_f32 v[92:93], v[8:9], v[26:27]
	v_pk_mul_f32 v[26:27], v[88:89], v[22:23] op_sel_hi:[1,0]
	v_pk_mul_f32 v[86:87], v[10:11], v[24:25]
	v_pk_mul_f32 v[24:25], v[82:83], v[22:23] op_sel_hi:[1,0]
	v_pk_mul_f32 v[22:23], v[84:85], v[22:23] op_sel_hi:[1,0]
	v_pk_mul_f32 v[88:89], v[12:13], v[26:27]
	v_pk_mul_f32 v[84:85], v[4:5], v[22:23]
	v_pk_mul_f32 v[82:83], v[2:3], v[24:25]
.LBB0_274:
	s_mov_b64 s[0:1], 0x20000
	v_lshl_add_u64 v[26:27], v[20:21], 0, s[0:1]
	v_add_co_u32_e32 v20, vcc, 0x20000, v20
	v_cvt_pk_bf16_f32 v22, v94, v95
	v_cvt_pk_bf16_f32 v23, v96, v97
	v_cvt_pk_bf16_f32 v24, v90, v91
	v_cvt_pk_bf16_f32 v25, v92, v93
	s_nop 1
	v_addc_co_u32_e32 v21, vcc, 0, v21, vcc
	s_and_b64 vcc, exec, s[4:5]
	global_store_dwordx4 v[20:21], v[22:25], off
	v_cvt_pk_bf16_f32 v20, v86, v87
	v_cvt_pk_bf16_f32 v21, v88, v89
	s_nop 1
	v_cvt_pk_bf16_f32 v22, v82, v83
	v_cvt_pk_bf16_f32 v23, v84, v85
	global_store_dwordx4 v[26:27], v[20:23], off offset:64
	s_cbranch_vccnz .LBB0_276
	s_nop 0
	v_pk_mul_f32 v[20:21], v[80:81], v[80:81]
	v_pk_mul_f32 v[22:23], v[78:79], v[78:79]
	s_nop 0
	v_pk_mov_b32 v[24:25], v[22:23], v[20:21] op_sel:[1,0]
	v_mov_b32_e32 v23, v21
	v_pk_add_f32 v[20:21], v[24:25], v[22:23]
	v_pk_mul_f32 v[22:23], v[76:77], v[76:77]
	v_pk_mul_f32 v[24:25], v[74:75], v[74:75]
	v_pk_add_f32 v[20:21], v[20:21], v[20:21] op_sel:[0,1] op_sel_hi:[1,0]
	v_pk_mov_b32 v[26:27], v[24:25], v[22:23] op_sel:[1,0]
	v_mov_b32_e32 v25, v23
	v_pk_add_f32 v[22:23], v[26:27], v[24:25]
	v_mul_f32_e32 v24, v66, v66
	v_mul_f32_e32 v25, v67, v67
	v_pk_add_f32 v[22:23], v[22:23], v[22:23] op_sel:[0,1] op_sel_hi:[1,0]
	v_mov_b32_e32 v21, v24
	v_mov_b32_e32 v23, v25
	v_pk_add_f32 v[20:21], v[20:21], v[22:23]
	v_mul_f32_e32 v22, v71, v71
	v_mul_f32_e32 v24, v73, v73
	v_mul_f32_e32 v26, v68, v68
	v_mul_f32_e32 v27, v69, v69
	v_pk_fma_f32 v[22:23], v[70:71], v[70:71], v[22:23] op_sel_hi:[1,1,0]
	v_pk_fma_f32 v[24:25], v[72:73], v[72:73], v[24:25] op_sel_hi:[1,1,0]
	v_mov_b32_e32 v23, v26
	v_mov_b32_e32 v25, v27
	v_pk_add_f32 v[22:23], v[22:23], v[24:25]
	s_nop 0
	v_pk_add_f32 v[20:21], v[20:21], v[22:23]
	v_and_b32_e32 v22, 64, v212
	v_add_f32_e32 v20, v20, v21
	v_xor_b32_e32 v21, 16, v212
	v_add_u32_e32 v22, 64, v22
	v_cmp_lt_i32_e32 vcc, v21, v22
	s_nop 1
	v_cndmask_b32_e32 v21, v212, v21, vcc
	v_lshlrev_b32_e32 v21, 2, v21
	ds_bpermute_b32 v21, v21, v20
	s_waitcnt lgkmcnt(0)
	v_add_f32_e32 v20, v20, v21
	v_xor_b32_e32 v21, 32, v212
	v_cmp_lt_i32_e32 vcc, v21, v22
	s_nop 1
	v_cndmask_b32_e32 v21, v212, v21, vcc
	v_lshlrev_b32_e32 v21, 2, v21
	ds_bpermute_b32 v21, v21, v20
	s_waitcnt lgkmcnt(0)
	v_add_f32_e32 v20, v20, v21
	v_fmamk_f32 v20, v20, 0x3c800000, v210
	v_mul_f32_e32 v21, 0x4f800000, v20
	v_cmp_gt_f32_e32 vcc, s28, v20
	s_nop 1
	v_cndmask_b32_e32 v20, v20, v21, vcc
	v_sqrt_f32_e32 v21, v20
	s_nop 0
	v_add_u32_e32 v22, -1, v21
	v_fma_f32 v23, -v22, v21, v20
	v_cmp_ge_f32_e64 s[6:7], 0, v23
	v_add_u32_e32 v23, 1, v21
	s_nop 0
	v_cndmask_b32_e64 v22, v21, v22, s[6:7]
	v_fma_f32 v21, -v23, v21, v20
	v_cmp_lt_f32_e64 s[6:7], 0, v21
	s_nop 1
	v_cndmask_b32_e64 v21, v22, v23, s[6:7]
	v_mul_f32_e32 v22, 0x37800000, v21
	v_cndmask_b32_e32 v21, v21, v22, vcc
	v_cmp_class_f32_e32 vcc, v20, v211
	s_nop 1
	v_cndmask_b32_e32 v20, v21, v20, vcc
	v_div_scale_f32 v21, s[0:1], v20, v20, s25
	v_rcp_f32_e32 v22, v21
	s_nop 0
	v_fma_f32 v23, -v21, v22, 1.0
	v_fmac_f32_e32 v22, v23, v22
	v_div_scale_f32 v23, vcc, s25, v20, s25
	v_mul_f32_e32 v24, v23, v22
	v_fma_f32 v25, -v21, v24, v23
	v_fmac_f32_e32 v24, v25, v22
	v_fma_f32 v21, -v21, v24, v23
	v_div_fmas_f32 v21, v21, v22, v24
	v_div_fixup_f32 v20, v21, v20, s25
	v_pk_mul_f32 v[22:23], v[78:79], v[20:21] op_sel_hi:[1,0]
	v_pk_mul_f32 v[24:25], v[80:81], v[20:21] op_sel_hi:[1,0]
	s_nop 0
	v_pk_mul_f32 v[78:79], v[14:15], v[22:23]
	v_pk_mul_f32 v[22:23], v[74:75], v[20:21] op_sel_hi:[1,0]
	v_pk_mul_f32 v[80:81], v[16:17], v[24:25]
	v_pk_mul_f32 v[24:25], v[76:77], v[20:21] op_sel_hi:[1,0]
	v_pk_mul_f32 v[74:75], v[6:7], v[22:23]
	v_pk_mul_f32 v[22:23], v[70:71], v[20:21] op_sel_hi:[1,0]
	v_pk_mul_f32 v[76:77], v[8:9], v[24:25]
	v_pk_mul_f32 v[24:25], v[72:73], v[20:21] op_sel_hi:[1,0]
	v_pk_mul_f32 v[70:71], v[10:11], v[22:23]
	v_pk_mul_f32 v[22:23], v[66:67], v[20:21] op_sel_hi:[1,0]
	v_pk_mul_f32 v[20:21], v[68:69], v[20:21] op_sel_hi:[1,0]
	v_pk_mul_f32 v[72:73], v[12:13], v[24:25]
	v_pk_mul_f32 v[68:69], v[4:5], v[20:21]
	v_pk_mul_f32 v[66:67], v[2:3], v[22:23]
; template <bool F8OUT = false> __device__ __forceinline__ void head_tile_store(const f32x4 (&acc)[2][2][4][2], bf16_t* obase  , int opitch, const float* gain, float scale, const f32x2e* rope, int row0, int fq) {
;     ...
;             if (gain) {
;                 float ss = 0.f;
; #pragma unroll
;                 for (int bj = 0; bj < 2; ++bj)
; #pragma unroll
;                     for (int n = 0; n < 2; ++n) ss += (x[bj][n][0] * x[bj][n][0] + x[bj][n][1] * x[bj][n][1]) + (x[bj][n][2] * x[bj][n][2] + x[bj][n][3] * x[bj][n][3]);
;                 ss += __shfl_xor(ss, 16); ss += __shfl_xor(ss, 32);
;                 const float r = scale / sqrtf(ss * (1.f / 64.f) + 1e-6f);
; #pragma unroll
;                 for (int bj = 0; bj < 2; ++bj)
; #pragma unroll
;                     for (int n = 0; n < 2; ++n) x[bj][n] = x[bj][n] * r * g[bj][n];
;             }
;             if (rope) {
;                 const int t = row & 8191; const bool second = (fq & 2) != 0;
; #pragma unroll
;                 for (int bj = 0; bj < 2; ++bj) { const int pos = bj ? (t & 63) : (t >> 6); const f32x2e* tb = rope + pos * 16 + 8 * (fq & 1);
; #pragma unroll
;                     for (int n = 0; n < 2; ++n)
; #pragma unroll
;                         for (int e = 0; e < 4; ++e) { const float p = __shfl_xor(x[bj][n][e], 32); const f32x2e cs = tb[4 * n + e]; const float v = x[bj][n][e];
;                             x[bj][n][e] = second ? (p * cs.y + v * cs.x) : (v * cs.x - p * cs.y); } }
;             }
;             if constexpr (F8OUT) { unsigned char* rowp8 = (unsigned char*)obase + (size_t)row * opitch + 8 * fq; typedef unsigned u32x2_ __attribute__((ext_vector_type(2)));
; #pragma unroll
;                 for (int bj = 0; bj < 2; ++bj) *(u32x2_*)(rowp8 + 32 * bj) = (u32x2_){pk4_fp8(x[bj][0][0], x[bj][0][1], x[bj][0][2], x[bj][0][3]), pk4_fp8(x[bj][1][0], x[bj][1][1], x[bj][1][2], x[bj][1][3])};
;                 continue; }
;             bf16_t* rowp = obase + (size_t)row * opitch + 8 * fq;
; #pragma unroll
;             for (int bj = 0; bj < 2; ++bj) { u32x4 w; w.x = cvt_pk_bf16(x[bj][0][0], x[bj][0][1]); w.y = cvt_pk_bf16(x[bj][0][2], x[bj][0][3]); w.z = cvt_pk_bf16(x[bj][1][0], x[bj][1][1]); w.w = cvt_pk_bf16(x[bj][1][2], x[bj][1][3]);
;                 *(u32x4*)(rowp + 32 * bj) = w; }
.LBB0_276:
	s_nop 0
	v_lshlrev_b64 v[20:21], 10, v[184:185]
	v_lshl_add_u64 v[20:21], v[18:19], 0, v[20:21]
	v_add_co_u32_e32 v28, vcc, 0x24000, v20
	v_lshl_add_u64 v[26:27], v[20:21], 0, s[30:31]
	s_nop 0
	v_addc_co_u32_e32 v29, vcc, 0, v21, vcc
	v_cvt_pk_bf16_f32 v22, v78, v79
	v_cvt_pk_bf16_f32 v23, v80, v81
	v_cvt_pk_bf16_f32 v24, v74, v75
	v_cvt_pk_bf16_f32 v25, v76, v77
	s_and_b64 vcc, exec, s[4:5]
	global_store_dwordx4 v[28:29], v[22:25], off
	s_nop 1
	v_cvt_pk_bf16_f32 v22, v70, v71
	v_cvt_pk_bf16_f32 v23, v72, v73
	v_cvt_pk_bf16_f32 v24, v66, v67
	v_cvt_pk_bf16_f32 v25, v68, v69
	global_store_dwordx4 v[26:27], v[22:25], off offset:64
	s_cbranch_vccnz .LBB0_278
	s_nop 0
	v_pk_mul_f32 v[22:23], v[64:65], v[64:65]
	v_pk_mul_f32 v[24:25], v[62:63], v[62:63]
	s_nop 0
	v_pk_mov_b32 v[26:27], v[24:25], v[22:23] op_sel:[1,0]
	v_mov_b32_e32 v25, v23
	v_pk_add_f32 v[22:23], v[26:27], v[24:25]
	v_pk_mul_f32 v[24:25], v[60:61], v[60:61]
	v_pk_mul_f32 v[26:27], v[58:59], v[58:59]
	v_pk_add_f32 v[22:23], v[22:23], v[22:23] op_sel:[0,1] op_sel_hi:[1,0]
	v_pk_mov_b32 v[28:29], v[26:27], v[24:25] op_sel:[1,0]
	v_mov_b32_e32 v27, v25
	v_pk_add_f32 v[24:25], v[28:29], v[26:27]
	v_mul_f32_e32 v26, v50, v50
	v_mul_f32_e32 v27, v51, v51
	v_pk_add_f32 v[24:25], v[24:25], v[24:25] op_sel:[0,1] op_sel_hi:[1,0]
	v_mov_b32_e32 v23, v26
	v_mov_b32_e32 v25, v27
	v_pk_add_f32 v[22:23], v[22:23], v[24:25]
	v_mul_f32_e32 v24, v55, v55
	v_mul_f32_e32 v26, v57, v57
	v_mul_f32_e32 v28, v52, v52
	v_mul_f32_e32 v29, v53, v53
	v_pk_fma_f32 v[24:25], v[54:55], v[54:55], v[24:25] op_sel_hi:[1,1,0]
	v_pk_fma_f32 v[26:27], v[56:57], v[56:57], v[26:27] op_sel_hi:[1,1,0]
	v_mov_b32_e32 v25, v28
	v_mov_b32_e32 v27, v29
	v_pk_add_f32 v[24:25], v[24:25], v[26:27]
	s_nop 0
	v_pk_add_f32 v[22:23], v[22:23], v[24:25]
	v_and_b32_e32 v24, 64, v212
	v_add_f32_e32 v22, v22, v23
	v_xor_b32_e32 v23, 16, v212
	v_add_u32_e32 v24, 64, v24
	v_cmp_lt_i32_e32 vcc, v23, v24
	s_nop 1
	v_cndmask_b32_e32 v23, v212, v23, vcc
	v_lshlrev_b32_e32 v23, 2, v23
	ds_bpermute_b32 v23, v23, v22
	s_waitcnt lgkmcnt(0)
	v_add_f32_e32 v22, v22, v23
	v_xor_b32_e32 v23, 32, v212
	v_cmp_lt_i32_e32 vcc, v23, v24
	s_nop 1
	v_cndmask_b32_e32 v23, v212, v23, vcc
	v_lshlrev_b32_e32 v23, 2, v23
	ds_bpermute_b32 v23, v23, v22
	s_waitcnt lgkmcnt(0)
	v_add_f32_e32 v22, v22, v23
	v_fmamk_f32 v22, v22, 0x3c800000, v210
	v_mul_f32_e32 v23, 0x4f800000, v22
	v_cmp_gt_f32_e32 vcc, s28, v22
	s_nop 1
	v_cndmask_b32_e32 v22, v22, v23, vcc
	v_sqrt_f32_e32 v23, v22
	s_nop 0
	v_add_u32_e32 v24, -1, v23
	v_fma_f32 v25, -v24, v23, v22
	v_cmp_ge_f32_e64 s[6:7], 0, v25
	v_add_u32_e32 v25, 1, v23
	s_nop 0
	v_cndmask_b32_e64 v24, v23, v24, s[6:7]
	v_fma_f32 v23, -v25, v23, v22
	v_cmp_lt_f32_e64 s[6:7], 0, v23
	s_nop 1
	v_cndmask_b32_e64 v23, v24, v25, s[6:7]
	v_mul_f32_e32 v24, 0x37800000, v23
	v_cndmask_b32_e32 v23, v23, v24, vcc
	v_cmp_class_f32_e32 vcc, v22, v211
	s_nop 1
	v_cndmask_b32_e32 v22, v23, v22, vcc
	v_div_scale_f32 v23, s[0:1], v22, v22, s25
	v_rcp_f32_e32 v24, v23
	s_nop 0
	v_fma_f32 v25, -v23, v24, 1.0
	v_fmac_f32_e32 v24, v25, v24
	v_div_scale_f32 v25, vcc, s25, v22, s25
	v_mul_f32_e32 v26, v25, v24
	v_fma_f32 v27, -v23, v26, v25
	v_fmac_f32_e32 v26, v27, v24
	v_fma_f32 v23, -v23, v26, v25
	v_div_fmas_f32 v23, v23, v24, v26
	v_div_fixup_f32 v22, v23, v22, s25
	v_pk_mul_f32 v[24:25], v[62:63], v[22:23] op_sel_hi:[1,0]
	v_pk_mul_f32 v[26:27], v[64:65], v[22:23] op_sel_hi:[1,0]
	s_nop 0
	v_pk_mul_f32 v[62:63], v[14:15], v[24:25]
	v_pk_mul_f32 v[24:25], v[58:59], v[22:23] op_sel_hi:[1,0]
	v_pk_mul_f32 v[64:65], v[16:17], v[26:27]
	v_pk_mul_f32 v[26:27], v[60:61], v[22:23] op_sel_hi:[1,0]
	v_pk_mul_f32 v[58:59], v[6:7], v[24:25]
	v_pk_mul_f32 v[24:25], v[54:55], v[22:23] op_sel_hi:[1,0]
	v_pk_mul_f32 v[60:61], v[8:9], v[26:27]
	v_pk_mul_f32 v[26:27], v[56:57], v[22:23] op_sel_hi:[1,0]
	v_pk_mul_f32 v[54:55], v[10:11], v[24:25]
	v_pk_mul_f32 v[24:25], v[50:51], v[22:23] op_sel_hi:[1,0]
	v_pk_mul_f32 v[22:23], v[52:53], v[22:23] op_sel_hi:[1,0]
	v_pk_mul_f32 v[56:57], v[12:13], v[26:27]
	v_pk_mul_f32 v[52:53], v[4:5], v[22:23]
	v_pk_mul_f32 v[50:51], v[2:3], v[24:25]
; template <bool F8OUT = false> __device__ __forceinline__ void head_tile_store(const f32x4 (&acc)[2][2][4][2], bf16_t* obase  , int opitch, const float* gain, float scale, const f32x2e* rope, int row0, int fq) {
;     ...
;             if (gain) {
;                 float ss = 0.f;
; #pragma unroll
;                 for (int bj = 0; bj < 2; ++bj)
; #pragma unroll
;                     for (int n = 0; n < 2; ++n) ss += (x[bj][n][0] * x[bj][n][0] + x[bj][n][1] * x[bj][n][1]) + (x[bj][n][2] * x[bj][n][2] + x[bj][n][3] * x[bj][n][3]);
;                 ss += __shfl_xor(ss, 16); ss += __shfl_xor(ss, 32);
;                 const float r = scale / sqrtf(ss * (1.f / 64.f) + 1e-6f);
; #pragma unroll
;                 for (int bj = 0; bj < 2; ++bj)
; #pragma unroll
;                     for (int n = 0; n < 2; ++n) x[bj][n] = x[bj][n] * r * g[bj][n];
;             }
;             if (rope) {
;                 const int t = row & 8191; const bool second = (fq & 2) != 0;
; #pragma unroll
;                 for (int bj = 0; bj < 2; ++bj) { const int pos = bj ? (t & 63) : (t >> 6); const f32x2e* tb = rope + pos * 16 + 8 * (fq & 1);
; #pragma unroll
;                     for (int n = 0; n < 2; ++n)
; #pragma unroll
;                         for (int e = 0; e < 4; ++e) { const float p = __shfl_xor(x[bj][n][e], 32); const f32x2e cs = tb[4 * n + e]; const float v = x[bj][n][e];
;                             x[bj][n][e] = second ? (p * cs.y + v * cs.x) : (v * cs.x - p * cs.y); } }
;             }
;             if constexpr (F8OUT) { unsigned char* rowp8 = (unsigned char*)obase + (size_t)row * opitch + 8 * fq; typedef unsigned u32x2_ __attribute__((ext_vector_type(2)));
; #pragma unroll
;                 for (int bj = 0; bj < 2; ++bj) *(u32x2_*)(rowp8 + 32 * bj) = (u32x2_){pk4_fp8(x[bj][0][0], x[bj][0][1], x[bj][0][2], x[bj][0][3]), pk4_fp8(x[bj][1][0], x[bj][1][1], x[bj][1][2], x[bj][1][3])};
;                 continue; }
;             bf16_t* rowp = obase + (size_t)row * opitch + 8 * fq;
; #pragma unroll
;             for (int bj = 0; bj < 2; ++bj) { u32x4 w; w.x = cvt_pk_bf16(x[bj][0][0], x[bj][0][1]); w.y = cvt_pk_bf16(x[bj][0][2], x[bj][0][3]); w.z = cvt_pk_bf16(x[bj][1][0], x[bj][1][1]); w.w = cvt_pk_bf16(x[bj][1][2], x[bj][1][3]);
;                 *(u32x4*)(rowp + 32 * bj) = w; }
.LBB0_278:
	v_lshl_add_u64 v[26:27], v[20:21], 0, s[12:13]
	v_add_co_u32_e32 v20, vcc, 0x28000, v20
	v_cvt_pk_bf16_f32 v22, v62, v63
	v_cvt_pk_bf16_f32 v23, v64, v65
	v_cvt_pk_bf16_f32 v24, v58, v59
	v_cvt_pk_bf16_f32 v25, v60, v61
	s_nop 1
	v_addc_co_u32_e32 v21, vcc, 0, v21, vcc
	s_and_b64 vcc, exec, s[4:5]
	global_store_dwordx4 v[20:21], v[22:25], off
	v_cvt_pk_bf16_f32 v20, v54, v55
	v_cvt_pk_bf16_f32 v21, v56, v57
	s_nop 1
	v_cvt_pk_bf16_f32 v22, v50, v51
	v_cvt_pk_bf16_f32 v23, v52, v53
	global_store_dwordx4 v[26:27], v[20:23], off offset:64
	s_cbranch_vccnz .LBB0_280
	s_nop 0
	v_pk_mul_f32 v[20:21], v[48:49], v[48:49]
	v_pk_mul_f32 v[22:23], v[46:47], v[46:47]
	s_nop 0
	v_pk_mov_b32 v[24:25], v[22:23], v[20:21] op_sel:[1,0]
	v_mov_b32_e32 v23, v21
	v_pk_add_f32 v[20:21], v[24:25], v[22:23]
	v_pk_mul_f32 v[22:23], v[44:45], v[44:45]
	v_pk_mul_f32 v[24:25], v[42:43], v[42:43]
	v_pk_add_f32 v[20:21], v[20:21], v[20:21] op_sel:[0,1] op_sel_hi:[1,0]
	v_pk_mov_b32 v[26:27], v[24:25], v[22:23] op_sel:[1,0]
	v_mov_b32_e32 v25, v23
	v_pk_add_f32 v[22:23], v[26:27], v[24:25]
	v_mul_f32_e32 v24, v34, v34
	v_mul_f32_e32 v25, v35, v35
	v_pk_add_f32 v[22:23], v[22:23], v[22:23] op_sel:[0,1] op_sel_hi:[1,0]
	v_mov_b32_e32 v21, v24
	v_mov_b32_e32 v23, v25
	v_pk_add_f32 v[20:21], v[20:21], v[22:23]
	v_mul_f32_e32 v22, v39, v39
	v_mul_f32_e32 v24, v41, v41
	v_mul_f32_e32 v26, v36, v36
	v_mul_f32_e32 v27, v37, v37
	v_pk_fma_f32 v[22:23], v[38:39], v[38:39], v[22:23] op_sel_hi:[1,1,0]
	v_pk_fma_f32 v[24:25], v[40:41], v[40:41], v[24:25] op_sel_hi:[1,1,0]
	v_mov_b32_e32 v23, v26
	v_mov_b32_e32 v25, v27
	v_pk_add_f32 v[22:23], v[22:23], v[24:25]
	s_nop 0
	v_pk_add_f32 v[20:21], v[20:21], v[22:23]
	v_and_b32_e32 v22, 64, v212
	v_add_f32_e32 v20, v20, v21
	v_xor_b32_e32 v21, 16, v212
	v_add_u32_e32 v22, 64, v22
	v_cmp_lt_i32_e32 vcc, v21, v22
	s_nop 1
	v_cndmask_b32_e32 v21, v212, v21, vcc
	v_lshlrev_b32_e32 v21, 2, v21
	ds_bpermute_b32 v21, v21, v20
	s_waitcnt lgkmcnt(0)
	v_add_f32_e32 v20, v20, v21
	v_xor_b32_e32 v21, 32, v212
	v_cmp_lt_i32_e32 vcc, v21, v22
	s_nop 1
	v_cndmask_b32_e32 v21, v212, v21, vcc
	v_lshlrev_b32_e32 v21, 2, v21
	ds_bpermute_b32 v21, v21, v20
	s_waitcnt lgkmcnt(0)
	v_add_f32_e32 v20, v20, v21
	v_fmamk_f32 v20, v20, 0x3c800000, v210
	v_mul_f32_e32 v21, 0x4f800000, v20
	v_cmp_gt_f32_e32 vcc, s28, v20
	s_nop 1
	v_cndmask_b32_e32 v20, v20, v21, vcc
	v_sqrt_f32_e32 v21, v20
	s_nop 0
	v_add_u32_e32 v22, -1, v21
	v_fma_f32 v23, -v22, v21, v20
	v_cmp_ge_f32_e64 s[4:5], 0, v23
	v_add_u32_e32 v23, 1, v21
	s_nop 0
	v_cndmask_b32_e64 v22, v21, v22, s[4:5]
	v_fma_f32 v21, -v23, v21, v20
	v_cmp_lt_f32_e64 s[4:5], 0, v21
	s_nop 1
	v_cndmask_b32_e64 v21, v22, v23, s[4:5]
	v_mul_f32_e32 v22, 0x37800000, v21
	v_cndmask_b32_e32 v21, v21, v22, vcc
	v_cmp_class_f32_e32 vcc, v20, v211
	s_nop 1
	v_cndmask_b32_e32 v20, v21, v20, vcc
	v_div_scale_f32 v21, s[0:1], v20, v20, s25
	v_rcp_f32_e32 v22, v21
	s_nop 0
	v_fma_f32 v23, -v21, v22, 1.0
	v_fmac_f32_e32 v22, v23, v22
	v_div_scale_f32 v23, vcc, s25, v20, s25
	v_mul_f32_e32 v24, v23, v22
	v_fma_f32 v25, -v21, v24, v23
	v_fmac_f32_e32 v24, v25, v22
	v_fma_f32 v21, -v21, v24, v23
	v_div_fmas_f32 v21, v21, v22, v24
	v_div_fixup_f32 v20, v21, v20, s25
	v_pk_mul_f32 v[22:23], v[46:47], v[20:21] op_sel_hi:[1,0]
	v_pk_mul_f32 v[24:25], v[48:49], v[20:21] op_sel_hi:[1,0]
	s_nop 0
	v_pk_mul_f32 v[46:47], v[14:15], v[22:23]
	v_pk_mul_f32 v[48:49], v[16:17], v[24:25]
	v_pk_mul_f32 v[14:15], v[42:43], v[20:21] op_sel_hi:[1,0]
	v_pk_mul_f32 v[16:17], v[44:45], v[20:21] op_sel_hi:[1,0]
	v_pk_mul_f32 v[42:43], v[6:7], v[14:15]
	v_pk_mul_f32 v[44:45], v[8:9], v[16:17]
	v_pk_mul_f32 v[6:7], v[38:39], v[20:21] op_sel_hi:[1,0]
	v_pk_mul_f32 v[8:9], v[40:41], v[20:21] op_sel_hi:[1,0]
	v_pk_mul_f32 v[38:39], v[10:11], v[6:7]
	v_pk_mul_f32 v[40:41], v[12:13], v[8:9]
	v_pk_mul_f32 v[6:7], v[34:35], v[20:21] op_sel_hi:[1,0]
	v_pk_mul_f32 v[8:9], v[36:37], v[20:21] op_sel_hi:[1,0]
	v_pk_mul_f32 v[34:35], v[2:3], v[6:7]
	v_pk_mul_f32 v[36:37], v[4:5], v[8:9]
.LBB0_280:
	s_nop 0
	v_lshlrev_b64 v[2:3], 10, v[184:185]
	v_lshl_add_u64 v[6:7], v[18:19], 0, v[2:3]
	v_lshl_add_u64 v[8:9], v[6:7], 0, s[22:23]
	v_add_co_u32_e32 v6, vcc, s24, v6
	v_cvt_pk_bf16_f32 v2, v46, v47
	v_cvt_pk_bf16_f32 v3, v48, v49
	v_cvt_pk_bf16_f32 v4, v42, v43
	v_cvt_pk_bf16_f32 v5, v44, v45
	s_nop 1
	v_addc_co_u32_e32 v7, vcc, 0, v7, vcc
	global_store_dwordx4 v[6:7], v[2:5], off
	s_nop 1
	v_cvt_pk_bf16_f32 v2, v38, v39
	v_cvt_pk_bf16_f32 v3, v40, v41
	v_cvt_pk_bf16_f32 v4, v34, v35
	v_cvt_pk_bf16_f32 v5, v36, v37
	global_store_dwordx4 v[8:9], v[2:5], off offset:64
	s_andn2_b64 vcc, exec, s[2:3]
	s_mov_b64 s[2:3], -1
	s_cbranch_vccnz .LBB0_149
